# latent attention: max-free softmax (logits bounded by RMS-norm x gains, guarded by a runtime gain check with the original loop as fallback), Q carries scale*log2e; scalar-base LDS-DMA; natural-order V
# speedup vs baseline: 1.0464x; 1.0402x over previous
; __device__ __forceinline__ int obid() { int t = blockIdx.x; asm volatile("" : "+s"(t)); return t; }
; __device__ __forceinline__ int ogrid() { int t = gridDim.x; asm volatile("" : "+s"(t)); return t; }
; __device__ __forceinline__ CParams* kparams() { CParams* k = (CParams*)__builtin_amdgcn_kernarg_segment_ptr(); asm volatile("" : "+s"(k)); return k; }
; __global__ void __launch_bounds__(512, 2) mk_fwd(Params p_unused) {
;     ...
;     if (IN(4)) _Pragma("unroll 1") for (int rep_ = 0; rep_ < NREP(4); ++rep_) {
;         CParams* kp = kparams();
;         const bf16_t* Qb = WSP(bf16_t, WS_Q); const bf16_t* Kb = WSP(bf16_t, WS_K); const bf16_t* Vb = WSP(bf16_t, WS_V); bf16_t* Ob = WSP(bf16_t, WS_O);
;         const bf16_t* QKVR = WSP(bf16_t, WS_QKVR); const float* ROPE = WSP(float, WS_ROPE); const float* qgn = kp->q_gain;
;         const int G = ogrid(), bx = obid(); const bool fast = (G % 8) == 0;
;         const int NR = fast ? (G >> 3) : G, rank = fast ? (bx >> 3) : bx, tot = fast ? 132 : 1056;
;         const bool split = fast && NR == 32; const int NA = split ? 26 : NR;
;         if (rank < NA) for (int i = 0;; ++i) {
;             int w = rank + NA * i;
;             if (split && i == 5) w = rank >= 24 ? rank + 106 : tot;
;             if (w >= tot) break;
;             const int combo = fast ? (bx & 7) : (w / 132), ww = fast ? w : (w % 132), b = combo >> 2, kvh = combo & 3;
;             const bool isl = ww < 128; const int rbk = ww >> 2; const int h = kvh * 4 + (isl ? (ww & 3) : (ww - 128));
;             const size_t row0 = isl ? ((size_t)NCTX + (size_t)b * SEQ + (size_t)rbk * 256) : ((size_t)b * CTXL);
;             if (isl) att::attn_dma_body(QKVR + row0 * QKVD + h * HD, QKVD, rbk * 256, ROPE, qgn, Kb + (size_t)combo * SKV * HD, Vb + (size_t)combo * SKV * HD, Ob + row0 * DM + h * HD, SKV, (char*)lds);
.LBB0_372:
	s_cmp_gt_i32 s54, 4
	s_cselect_b64 s[4:5], -1, 0
	s_xor_b64 s[2:3], s[2:3], -1
	s_or_b64 s[2:3], s[4:5], s[2:3]
	s_and_b64 vcc, exec, s[2:3]
	s_cbranch_vccnz .LBB0_557
	s_mov_b64 s[30:31], s[0:1]
	s_load_dword s33, s[0:1], 0xb0
	s_load_dwordx2 s[28:29], s[30:31], 0xa0
	s_mov_b32 s2, s96
	s_waitcnt lgkmcnt(0)
	s_mov_b32 s3, s33
	s_add_u32 s23, s28, 0x5f500000
	s_addc_u32 s94, s29, 0
	s_and_b32 s4, s3, 7
	s_ashr_i32 s6, s3, 3
	s_ashr_i32 s7, s2, 3
	s_cmp_eq_u32 s4, 0
	s_cselect_b64 s[10:11], -1, 0
	s_and_b64 s[4:5], s[10:11], exec
	s_cselect_b32 s3, s6, s3
	s_cselect_b32 s21, s7, s2
	s_cmp_eq_u32 s3, 32
	s_cselect_b64 s[4:5], -1, 0
	s_and_b64 s[12:13], s[10:11], s[4:5]
	s_and_b64 s[4:5], s[12:13], exec
	s_cselect_b32 s56, 26, s3
	s_cmp_ge_i32 s21, s56
	s_cbranch_scc1 .LBB0_440
	s_movk_i32 s3, 0x84
	s_and_b64 s[4:5], s[10:11], exec
	s_cselect_b32 s57, s3, 0x420
	s_cmp_ge_i32 s21, s57
	s_cbranch_scc1 .LBB0_440
	s_load_dwordx4 s[4:7], s[30:31], 0x48
	v_and_b32_e32 v253, 63, v0
	v_lshlrev_b32_e32 v253, 2, v253
	s_waitcnt lgkmcnt(0)
	global_load_dword v251, v253, s[4:5]
	global_load_dword v254, v253, s[4:5] offset:256
	global_load_dword v252, v253, s[6:7]
	global_load_dword v255, v253, s[6:7] offset:256
	s_waitcnt vmcnt(0)
	v_max_f32_e64 v251, |v251|, |v254|
	v_max_f32_e64 v252, |v252|, |v255|
	s_nop 1
	v_max_f32_dpp v251, v251, v251 quad_perm:[1,0,3,2] row_mask:0xf bank_mask:0xf
	v_max_f32_dpp v252, v252, v252 quad_perm:[1,0,3,2] row_mask:0xf bank_mask:0xf
	s_nop 1
	v_max_f32_dpp v251, v251, v251 quad_perm:[2,3,0,1] row_mask:0xf bank_mask:0xf
	v_max_f32_dpp v252, v252, v252 quad_perm:[2,3,0,1] row_mask:0xf bank_mask:0xf
	s_nop 1
	v_max_f32_dpp v251, v251, v251 row_half_mirror row_mask:0xf bank_mask:0xf
	v_max_f32_dpp v252, v252, v252 row_half_mirror row_mask:0xf bank_mask:0xf
	s_nop 1
	v_max_f32_dpp v251, v251, v251 row_mirror row_mask:0xf bank_mask:0xf
	v_max_f32_dpp v252, v252, v252 row_mirror row_mask:0xf bank_mask:0xf
	v_max_f32_e32 v251, v251, v252
	s_nop 1
	v_readlane_b32 s4, v251, 0
	v_readlane_b32 s5, v251, 16
	v_readlane_b32 s6, v251, 32
	v_readlane_b32 s7, v251, 48
	s_nop 3
	s_max_u32 s4, s4, s5
	s_max_u32 s6, s6, s7
	s_max_u32 s4, s4, s6
	s_cmp_gt_u32 s4, 0x4019999a
	s_cselect_b32 s100, 1, 0
	s_add_i32 s3, s21, 0x6a
	s_cmp_gt_i32 s21, 23
	s_cselect_b32 s46, s3, s57
	s_add_u32 s47, s28, 0x59100000
	s_addc_u32 s48, s29, 0
	s_add_u32 s49, s28, 0x5d300000
	s_addc_u32 s50, s29, 0
	s_add_u32 s51, s28, 0x5e400000
	s_addc_u32 s93, s29, 0
	s_add_u32 s22, s28, 0x52e00000
	s_addc_u32 s88, s29, 0
	s_load_dwordx2 s[14:15], s[30:31], 0x48
	s_add_u32 s16, s28, 0x180000
	s_addc_u32 s17, s29, 0
	s_and_b32 s18, s2, 7
	s_add_u32 s19, s28, 0x8000
	s_addc_u32 s2, s29, 0
	v_writelane_b32 v250, s2, 6
	s_mov_b32 s73, 0
	v_mov_b32_e32 v163, 0
	s_mov_b32 s89, 0x42b504f3
	s_mov_b32 s20, 0x3e0293ee
	s_add_i32 s90, 0, 0x20500
	s_movk_i32 s91, 0x2200
	s_movk_i32 s92, 0x7fff
	s_mov_b64 s[24:25], 0x4040
	v_mov_b32_e32 v1, 0x358637bd
	v_mov_b32_e32 v174, 0x260
	s_mov_b64 s[26:27], 0x5d30c000
	s_mov_b64 s[58:59], 0x5e40c000
	s_mov_b64 s[60:61], 0x5d310000
	s_mov_b64 s[62:63], 0x5e410000
	v_mov_b32_e32 v175, 0xf149f2ca
	s_mov_b32 s2, s21
	s_mov_b32 s95, 0
	s_branch .LBB0_377

; __device__ __forceinline__ void attn_dma_body(const bf16_t* __restrict__ Qb, int ldq, int tpos0, const float* __restrict__ rope, const float* __restrict__ qgain, ...
;     ...
;   unsigned koff[2], voff[2];
; #pragma unroll
;   for (int c = 0; c < 2; ++c) { const int g = c * 512 + tid;
;     { const int row = g >> 4, ch = (g & 15) ^ (row & 7); koff[c] = (unsigned)(row * 128 + ch * 8) * 2u; }
;     { const int sub = g >> 5, kk = (sub >> 2) * 8 + ((g >> 2) & 7), k = (kk & ~0xC) | ((kk & 4) << 1) | ((kk & 8) >> 1), col = (sub & 3) * 32 + (g & 3) * 8; voff[c] = (unsigned)(k * 128 + col) * 2u; } }
;   const unsigned wbase = (unsigned)__builtin_amdgcn_readfirstlane(wid) * 1024u;
;   typedef __attribute__((address_space(3))) unsigned lds_u32;
;   lds_u32* ldsl = (lds_u32*)(__attribute__((address_space(3))) char*)lds;
;     ...
;   const int NT = seq / KVBLK;
;   ATT_DMA(0, 0); ATT_DMA(1, 1);
; #pragma unroll
;   for (int d0 = 0; d0 < 8; ++d0) qr[d0] = ld8(Qw + d0 * 16);
;   if (tpos0 >= 0) {
;     float ss = 0.f;
; #pragma unroll
;     for (int d0 = 0; d0 < 8; ++d0)
; #pragma unroll
;       for (int i = 0; i < 8; ++i) { const float x = bf2f((unsigned)(unsigned short)qr[d0][i]); ss += x * x; }
;     { auto rr = __builtin_amdgcn_permlane32_swap(__float_as_uint(ss), __float_as_uint(ss), false, false); ss = __uint_as_float(rr[0]) + __uint_as_float(rr[1]); }
;     const float rinv = 1.0f / sqrtf(ss * (1.0f / 128.0f) + RMS_EPS);
;     const int t = tpos0 + wid * QBLK + r32;
; #pragma unroll
;     for (int ax = 0; ax < 2; ++ax) { const int pos = ax ? (t & 63) : (t >> 6);
; #pragma unroll
;       for (int q = 0; q < 2; ++q) { const int dl = 4 * ax + q, dh = dl + 2, p0 = q * 16 + 8 * hi;
;         const float* cp_ = rope + pos * 32 + p0; const float* gl = qgain + dl * 16 + 8 * hi; const float* gh = qgain + dh * 16 + 8 * hi;
;         float cs[8], sn[8], lo[8], hv[8];
; #pragma unroll
;         for (int i = 0; i < 8; ++i) { cs[i] = cp_[i]; sn[i] = cp_[4096 + i];
;           lo[i] = bf2f((unsigned)(unsigned short)qr[dl][i]) * rinv * gl[i]; hv[i] = bf2f((unsigned)(unsigned short)qr[dh][i]) * rinv * gh[i]; }
.LBB0_405:
	s_and_b64 vcc, exec, s[4:5]
	s_cbranch_vccz .LBB0_437
	s_cmp_lg_u32 s100, 0
	s_cbranch_scc1 .Lorig_entry
	v_mov_b32_e32 v147, v0
	s_mul_i32 s2, s71, 0x1800
	s_waitcnt vmcnt(0)
	v_and_b32_e32 v3, 0x60, v147
	v_lshlrev_b32_e32 v5, 3, v147
	v_and_b32_e32 v176, 15, v147
	v_lshrrev_b32_e32 v2, 2, v147
	v_and_or_b32 v3, v5, 24, v3
	v_ashrrev_i32_e32 v5, 4, v147
	v_bfe_u32 v146, v147, 2, 2
	v_and_b32_e32 v148, 4, v2
	v_bitop3_b32 v6, v5, v176, 7 bitop3:0x6c
	v_lshlrev_b32_e32 v149, 8, v5
	v_and_b32_e32 v154, 0xfffff0, v5
	v_or_b32_e32 v2, v148, v146
	v_and_b32_e32 v156, 8, v5
	s_mul_hi_u32 s3, s70, 0x1800
	v_lshlrev_b32_e32 v3, 1, v3
	v_or3_b32 v5, v154, v156, v2
	s_add_i32 s3, s3, s2
	s_mul_i32 s2, s70, 0x1800
	v_lshl_or_b32 v30, v5, 8, v3
	v_add_u32_e32 v5, 0x200, v147
	s_add_u32 s2, s22, s2
	v_ashrrev_i32_e32 v5, 4, v5
	s_addc_u32 s3, s88, s3
	s_lshl_b64 s[44:45], s[72:73], 1
	v_lshlrev_b32_e32 v150, 4, v6
	v_bitop3_b32 v6, v5, v176, 7 bitop3:0x6c
	v_lshlrev_b32_e32 v151, 8, v5
	v_and_b32_e32 v153, 0xfffff0, v5
	s_add_u32 s2, s2, s44
	v_ashrrev_i32_e32 v179, 6, v147
	v_and_b32_e32 v155, 8, v5
	s_addc_u32 s3, s3, s45
	v_and_b32_e32 v177, 31, v147
	v_lshlrev_b32_e32 v164, 5, v179
	v_or3_b32 v2, v153, v155, v2
	v_or_b32_e32 v4, v164, v177
	v_lshl_or_b32 v34, v2, 8, v3
	v_mov_b64_e32 v[2:3], s[2:3]
	s_movk_i32 s2, 0x1800
	v_mad_i64_i32 v[2:3], s[2:3], v4, s2, v[2:3]
	v_readfirstlane_b32 s2, v179
	s_lshl_b32 s2, s2, 10
	s_add_i32 s96, s2, 0
	v_or_b32_e32 v162, v150, v149
	s_add_i32 s2, s96, 0x4000
	s_mov_b32 m0, s96
	v_lshlrev_b32_e32 v152, 4, v6
	global_load_lds_dwordx4 v162, s[38:39]
	s_mov_b32 m0, s2
	v_or_b32_e32 v32, v152, v151
	global_load_lds_dwordx4 v30, s[40:41]
	s_add_i32 m0, s96, 0x2000
	v_bfe_u32 v178, v147, 5, 1
	global_load_lds_dwordx4 v32, s[38:39]
	s_add_i32 m0, s96, 0x6000
	s_add_u32 s2, s38, 0x4000
	s_addc_u32 s3, s39, 0
	s_add_u32 s4, s40, 0x4000
	global_load_lds_dwordx4 v34, s[40:41]
	s_addc_u32 s5, s41, 0
	s_add_i32 m0, s96, 0x8000
	s_add_i32 s6, s96, 0xc000
	global_load_lds_dwordx4 v162, s[2:3]
	s_mov_b32 m0, s6
	v_lshlrev_b32_e32 v166, 4, v178
	global_load_lds_dwordx4 v30, s[4:5]
	s_add_i32 m0, s96, 0xa000
	v_mov_b32_e32 v167, v163
	global_load_lds_dwordx4 v32, s[2:3]
	s_add_i32 m0, s96, 0xe000
	v_lshl_add_u64 v[2:3], v[2:3], 0, v[166:167]
	global_load_lds_dwordx4 v34, s[4:5]
	global_load_dwordx4 v[102:105], v[2:3], off
	global_load_dwordx4 v[110:113], v[2:3], off offset:32
	global_load_dwordx4 v[98:101], v[2:3], off offset:64
	global_load_dwordx4 v[106:109], v[2:3], off offset:96
	global_load_dwordx4 v[118:121], v[2:3], off offset:128
	global_load_dwordx4 v[126:129], v[2:3], off offset:160
	global_load_dwordx4 v[114:117], v[2:3], off offset:192
	global_load_dwordx4 v[122:125], v[2:3], off offset:224
	s_cmp_lt_i32 s68, 0
	s_cbranch_scc1 .LBB0_408
	v_lshl_or_b32 v3, s68, 8, v177
	v_lshlrev_b32_e32 v2, 3, v178
	v_add_u32_e32 v26, v3, v164
	v_lshlrev_b32_e32 v44, 2, v2
	v_ashrrev_i32_e32 v2, 1, v26
	v_and_b32_e32 v2, 0xffffffe0, v2
	v_ashrrev_i32_e32 v3, 31, v2
	v_mov_b32_e32 v45, v163
	v_lshl_add_u64 v[2:3], v[2:3], 2, s[16:17]
	v_lshl_add_u64 v[76:77], v[2:3], 0, v[44:45]
	s_mov_b64 s[2:3], 0x4000
	v_lshl_add_u64 v[6:7], v[76:77], 0, s[2:3]
	s_waitcnt lgkmcnt(0)
	global_load_dwordx4 v[130:133], v44, s[14:15] offset:16
	global_load_dwordx4 v[14:17], v44, s[14:15] offset:144
	global_load_dwordx4 v[2:5], v[76:77], off offset:16
	s_nop 0
	global_load_dwordx4 v[6:9], v[6:7], off offset:16
	s_nop 0
	global_load_dwordx4 v[22:25], v44, s[14:15]
	global_load_dwordx4 v[18:21], v44, s[14:15] offset:128
	s_waitcnt vmcnt(0)
	v_lshlrev_b32_e32 v38, 16, v129
	v_and_b32_e32 v36, 0xffff0000, v129
	v_lshlrev_b32_e32 v129, 16, v102
	v_lshlrev_b32_e32 v39, 16, v125
	v_and_b32_e32 v37, 0xffff0000, v125
	v_lshlrev_b32_e32 v49, 16, v123
	v_lshlrev_b32_e32 v48, 16, v127
	v_and_b32_e32 v47, 0xffff0000, v123
	v_and_b32_e32 v46, 0xffff0000, v127
	v_lshlrev_b32_e32 v123, 16, v99
	v_and_b32_e32 v127, 0xffff0000, v99
	v_and_b32_e32 v99, 0xffff0000, v102
	v_lshlrev_b32_e32 v53, 16, v122
	v_and_b32_e32 v51, 0xffff0000, v122
	v_lshlrev_b32_e32 v122, 16, v103
	v_lshlrev_b32_e32 v52, 16, v126
	v_and_b32_e32 v50, 0xffff0000, v126
	v_and_b32_e32 v126, 0xffff0000, v103
	v_lshlrev_b32_e32 v90, 16, v111
	v_and_b32_e32 v88, 0xffff0000, v111
	v_lshlrev_b32_e32 v92, 16, v110
	v_and_b32_e32 v94, 0xffff0000, v110
	v_lshlrev_b32_e32 v111, 16, v100
	v_lshlrev_b32_e32 v110, 16, v104
	v_lshlrev_b32_e32 v65, 16, v116
	v_and_b32_e32 v63, 0xffff0000, v116
	v_lshlrev_b32_e32 v73, 16, v114
	v_and_b32_e32 v71, 0xffff0000, v114
	v_lshlrev_b32_e32 v114, 16, v105
	v_and_b32_e32 v116, 0xffff0000, v105
	v_and_b32_e32 v105, 0xffff0000, v100
	v_and_b32_e32 v104, 0xffff0000, v104
	v_lshlrev_b32_e32 v69, 16, v115
	v_and_b32_e32 v67, 0xffff0000, v115
	v_lshlrev_b32_e32 v115, 16, v101
	v_lshlrev_b32_e32 v61, 16, v117
	v_and_b32_e32 v55, 0xffff0000, v117
	v_and_b32_e32 v117, 0xffff0000, v101
	v_lshlrev_b32_e32 v93, 16, v106
	v_and_b32_e32 v95, 0xffff0000, v106
	v_lshlrev_b32_e32 v91, 16, v107
	v_and_b32_e32 v89, 0xffff0000, v107
	v_lshlrev_b32_e32 v87, 16, v108
	v_lshlrev_b32_e32 v86, 16, v112
	v_and_b32_e32 v85, 0xffff0000, v108
	v_and_b32_e32 v84, 0xffff0000, v112
	v_lshlrev_b32_e32 v83, 16, v109
	v_lshlrev_b32_e32 v82, 16, v113
	v_and_b32_e32 v81, 0xffff0000, v109
	v_and_b32_e32 v80, 0xffff0000, v113
	v_lshlrev_b32_e32 v42, 16, v128
	v_and_b32_e32 v40, 0xffff0000, v128
	v_lshlrev_b32_e32 v128, 16, v98
	v_and_b32_e32 v98, 0xffff0000, v98
	s_movk_i32 s4, 0x4000
	v_lshlrev_b32_e32 v26, 7, v26
	v_add_co_u32_e32 v78, vcc, s4, v76
	v_mov_b32_e32 v27, v163
	v_and_b32_e32 v26, 0x1f80, v26
; __device__ __forceinline__ void attn_dma_body(const bf16_t* __restrict__ Qb, int ldq, int tpos0, const float* __restrict__ rope, const float* __restrict__ qgain, ...
;     ...
;     float ss = 0.f;
; #pragma unroll
;     for (int d0 = 0; d0 < 8; ++d0)
; #pragma unroll
;       for (int i = 0; i < 8; ++i) { const float x = bf2f((unsigned)(unsigned short)qr[d0][i]); ss += x * x; }
;     { auto rr = __builtin_amdgcn_permlane32_swap(__float_as_uint(ss), __float_as_uint(ss), false, false); ss = __uint_as_float(rr[0]) + __uint_as_float(rr[1]); }
;     const float rinv = 1.0f / sqrtf(ss * (1.0f / 128.0f) + RMS_EPS);
	v_addc_co_u32_e32 v79, vcc, 0, v77, vcc
	v_lshl_add_u64 v[26:27], s[16:17], 0, v[26:27]
	global_load_dwordx4 v[10:13], v[78:79], off
	v_lshl_add_u64 v[58:59], v[26:27], 0, v[44:45]
	global_load_dwordx4 v[26:29], v[76:77], off
	v_lshlrev_b32_e32 v72, 16, v118
	v_and_b32_e32 v70, 0xffff0000, v118
	v_lshlrev_b32_e32 v68, 16, v119
	v_and_b32_e32 v66, 0xffff0000, v119
	v_lshlrev_b32_e32 v64, 16, v120
	v_and_b32_e32 v62, 0xffff0000, v120
	v_lshlrev_b32_e32 v60, 16, v121
	v_and_b32_e32 v54, 0xffff0000, v121
	v_lshlrev_b32_e32 v43, 16, v124
	v_and_b32_e32 v41, 0xffff0000, v124
	v_mov_b32_e32 v134, v37
	v_mov_b32_e32 v135, v39
	v_lshl_add_u64 v[74:75], v[58:59], 0, s[2:3]
	v_mov_b32_e32 v125, v20
	v_mul_f32_e32 v20, v129, v129
	v_fmac_f32_e32 v20, v99, v99
	v_pk_fma_f32 v[102:103], v[122:123], v[122:123], v[20:21] op_sel_hi:[1,1,0]
	v_mul_f32_e32 v20, v123, v123
	v_pk_fma_f32 v[102:103], v[126:127], v[126:127], v[102:103]
	s_mov_b32 s2, 0xf800000
	v_pk_fma_f32 v[102:103], v[110:111], v[110:111], v[102:103]
	v_mov_b32_e32 v124, v24
	v_pk_fma_f32 v[102:103], v[104:105], v[104:105], v[102:103]
	v_mov_b32_e32 v120, v130
	v_pk_fma_f32 v[102:103], v[114:115], v[114:115], v[102:103]
	v_mov_b32_e32 v121, v14
	v_pk_fma_f32 v[102:103], v[116:117], v[116:117], v[102:103]
	v_mov_b32_e32 v14, v131
	v_pk_fma_f32 v[102:103], v[92:93], v[92:93], v[102:103]
	v_mov_b32_e32 v118, v132
	v_pk_fma_f32 v[102:103], v[94:95], v[94:95], v[102:103]
	v_mov_b32_e32 v119, v16
	v_pk_fma_f32 v[102:103], v[90:91], v[90:91], v[102:103]
	v_mov_b32_e32 v16, v133
	v_pk_fma_f32 v[102:103], v[88:89], v[88:89], v[102:103]
	v_mov_b32_e32 v106, v6
	v_pk_fma_f32 v[102:103], v[86:87], v[86:87], v[102:103]
	v_mov_b32_e32 v107, v2
	v_pk_fma_f32 v[102:103], v[84:85], v[84:85], v[102:103]
	v_lshl_add_u64 v[96:97], v[76:77], 0, s[24:25]
	v_pk_fma_f32 v[102:103], v[82:83], v[82:83], v[102:103]
	v_mov_b32_e32 v112, v8
	v_pk_fma_f32 v[102:103], v[80:81], v[80:81], v[102:103]
	v_mov_b32_e32 v113, v4
	v_pk_fma_f32 v[102:103], v[128:129], v[128:129], v[102:103]
	v_mov_b32_e32 v108, v9
	v_pk_fma_f32 v[102:103], v[98:99], v[98:99], v[102:103]
	v_mov_b32_e32 v109, v5
	v_pk_add_f32 v[102:103], v[20:21], v[102:103] op_sel_hi:[0,1]
	v_mul_f32_e32 v20, v127, v127
	v_pk_add_f32 v[102:103], v[20:21], v[102:103] op_sel_hi:[0,1]
	v_mul_f32_e32 v20, v111, v111
	v_pk_add_f32 v[102:103], v[20:21], v[102:103] op_sel_hi:[0,1]
	v_mul_f32_e32 v20, v105, v105
	v_pk_add_f32 v[102:103], v[20:21], v[102:103] op_sel_hi:[0,1]
	v_mul_f32_e32 v20, v115, v115
	v_pk_add_f32 v[102:103], v[20:21], v[102:103] op_sel_hi:[0,1]
	v_mul_f32_e32 v20, v117, v117
	v_pk_add_f32 v[102:103], v[20:21], v[102:103] op_sel_hi:[0,1]
	v_mul_f32_e32 v20, v93, v93
	v_pk_add_f32 v[102:103], v[20:21], v[102:103] op_sel_hi:[0,1]
	v_mul_f32_e32 v20, v95, v95
	v_pk_add_f32 v[102:103], v[20:21], v[102:103] op_sel_hi:[0,1]
	v_mul_f32_e32 v20, v91, v91
	v_pk_add_f32 v[102:103], v[20:21], v[102:103] op_sel_hi:[0,1]
	v_mul_f32_e32 v20, v89, v89
	v_pk_add_f32 v[102:103], v[20:21], v[102:103] op_sel_hi:[0,1]
	v_mul_f32_e32 v20, v87, v87
	v_pk_add_f32 v[102:103], v[20:21], v[102:103] op_sel_hi:[0,1]
	v_mul_f32_e32 v20, v85, v85
	v_pk_add_f32 v[102:103], v[20:21], v[102:103] op_sel_hi:[0,1]
	v_mul_f32_e32 v20, v83, v83
	v_pk_add_f32 v[102:103], v[20:21], v[102:103] op_sel_hi:[0,1]
	v_mul_f32_e32 v20, v81, v81
	v_pk_add_f32 v[102:103], v[20:21], v[102:103] op_sel_hi:[0,1]
	v_pk_fma_f32 v[102:103], v[72:73], v[72:73], v[102:103]
	v_mul_f32_e32 v20, v73, v73
	v_pk_fma_f32 v[102:103], v[70:71], v[70:71], v[102:103]
	s_waitcnt vmcnt(1)
	v_mov_b32_e32 v100, v12
	v_pk_fma_f32 v[102:103], v[68:69], v[68:69], v[102:103]
	s_waitcnt vmcnt(0)
	v_mov_b32_e32 v101, v28
	v_pk_fma_f32 v[102:103], v[66:67], v[66:67], v[102:103]
	v_lshl_add_u64 v[56:57], v[58:59], 0, s[24:25]
	v_pk_fma_f32 v[102:103], v[64:65], v[64:65], v[102:103]
	s_nop 0
	v_pk_fma_f32 v[102:103], v[62:63], v[62:63], v[102:103]
	s_nop 0
	v_pk_fma_f32 v[102:103], v[60:61], v[60:61], v[102:103]
	s_nop 0
	v_pk_fma_f32 v[102:103], v[54:55], v[54:55], v[102:103]
	s_nop 0
	v_pk_fma_f32 v[102:103], v[52:53], v[52:53], v[102:103]
	s_nop 0
	v_pk_fma_f32 v[102:103], v[50:51], v[50:51], v[102:103]
	s_nop 0
	v_pk_fma_f32 v[102:103], v[48:49], v[48:49], v[102:103]
	s_nop 0
	v_pk_fma_f32 v[102:103], v[46:47], v[46:47], v[102:103]
	s_nop 0
	v_pk_fma_f32 v[102:103], v[42:43], v[42:43], v[102:103]
	s_nop 0
	v_pk_fma_f32 v[102:103], v[40:41], v[40:41], v[102:103]
	s_nop 0
	v_pk_fma_f32 v[102:103], v[38:39], v[38:39], v[102:103]
	s_nop 0
	v_pk_fma_f32 v[102:103], v[36:37], v[36:37], v[102:103]
	s_nop 0
	v_pk_add_f32 v[102:103], v[20:21], v[102:103] op_sel_hi:[0,1]
	v_mul_f32_e32 v20, v71, v71
	v_pk_add_f32 v[102:103], v[20:21], v[102:103] op_sel_hi:[0,1]
	v_mul_f32_e32 v20, v69, v69
	v_pk_add_f32 v[102:103], v[20:21], v[102:103] op_sel_hi:[0,1]
	v_mul_f32_e32 v20, v67, v67
	v_pk_add_f32 v[102:103], v[20:21], v[102:103] op_sel_hi:[0,1]
	v_mul_f32_e32 v20, v65, v65
	v_pk_add_f32 v[102:103], v[20:21], v[102:103] op_sel_hi:[0,1]
	v_mul_f32_e32 v20, v63, v63
	v_pk_add_f32 v[102:103], v[20:21], v[102:103] op_sel_hi:[0,1]
	v_mul_f32_e32 v20, v61, v61
	v_pk_add_f32 v[102:103], v[20:21], v[102:103] op_sel_hi:[0,1]
	v_mul_f32_e32 v20, v55, v55
	v_pk_add_f32 v[102:103], v[20:21], v[102:103] op_sel_hi:[0,1]
	v_mul_f32_e32 v20, v53, v53
	v_pk_add_f32 v[102:103], v[20:21], v[102:103] op_sel_hi:[0,1]
	v_mul_f32_e32 v20, v51, v51
	v_pk_add_f32 v[102:103], v[20:21], v[102:103] op_sel_hi:[0,1]
	v_mul_f32_e32 v20, v49, v49
	v_pk_add_f32 v[102:103], v[20:21], v[102:103] op_sel_hi:[0,1]
	v_mul_f32_e32 v20, v47, v47
	v_pk_add_f32 v[102:103], v[20:21], v[102:103] op_sel_hi:[0,1]
; __device__ __forceinline__ unsigned pk2(float lo, float hi) { unsigned r; asm("v_cvt_pk_bf16_f32 %0, %1, %2" : "=v"(r) : "v"(lo), "v"(hi)); return r; }
; __device__ __forceinline__ void attn_dma_body(const bf16_t* __restrict__ Qb, int ldq, int tpos0, const float* __restrict__ rope, const float* __restrict__ qgain, ...
;     ...
;     const float rinv = 1.0f / sqrtf(ss * (1.0f / 128.0f) + RMS_EPS);
;     const int t = tpos0 + wid * QBLK + r32;
; #pragma unroll
;     for (int ax = 0; ax < 2; ++ax) { const int pos = ax ? (t & 63) : (t >> 6);
; #pragma unroll
;       for (int q = 0; q < 2; ++q) { const int dl = 4 * ax + q, dh = dl + 2, p0 = q * 16 + 8 * hi;
;         const float* cp_ = rope + pos * 32 + p0; const float* gl = qgain + dl * 16 + 8 * hi; const float* gh = qgain + dh * 16 + 8 * hi;
;         float cs[8], sn[8], lo[8], hv[8];
; #pragma unroll
;         for (int i = 0; i < 8; ++i) { cs[i] = cp_[i]; sn[i] = cp_[4096 + i];
;           lo[i] = bf2f((unsigned)(unsigned short)qr[dl][i]) * rinv * gl[i]; hv[i] = bf2f((unsigned)(unsigned short)qr[dh][i]) * rinv * gh[i]; }
;         u32x4 wl, wh;
; #pragma unroll
;         for (int i = 0; i < 4; ++i) { const float l0 = lo[2 * i] * cs[2 * i] - hv[2 * i] * sn[2 * i], l1 = lo[2 * i + 1] * cs[2 * i + 1] - hv[2 * i + 1] * sn[2 * i + 1];
;           const float h0 = hv[2 * i] * cs[2 * i] + lo[2 * i] * sn[2 * i], h1 = hv[2 * i + 1] * cs[2 * i + 1] + lo[2 * i + 1] * sn[2 * i + 1];
;           wl[i] = pk2(l0, l1); wh[i] = pk2(h0, h1); }
;         qr[dl] = *reinterpret_cast<bf16x8*>(&wl); qr[dh] = *reinterpret_cast<bf16x8*>(&wh); } } }
	v_mul_f32_e32 v20, v43, v43
	v_pk_add_f32 v[102:103], v[20:21], v[102:103] op_sel_hi:[0,1]
	v_mul_f32_e32 v20, v41, v41
	v_pk_add_f32 v[102:103], v[20:21], v[102:103] op_sel_hi:[0,1]
	v_mul_f32_e32 v20, v39, v39
	v_pk_add_f32 v[102:103], v[20:21], v[102:103] op_sel_hi:[0,1]
	v_pk_fma_f32 v[102:103], v[134:135], v[134:135], v[102:103]
	global_load_dwordx4 v[130:133], v44, s[14:15] offset:80
	global_load_dwordx4 v[134:137], v44, s[14:15] offset:64
	global_load_dwordx4 v[138:141], v44, s[14:15] offset:208
	global_load_dwordx4 v[142:145], v44, s[14:15] offset:192
	v_mov_b32_e32 v20, v102
	s_nop 1
	v_permlane32_swap_b32_e32 v102, v20
	v_add_f32_e32 v20, v102, v20
	v_fmamk_f32 v20, v20, 0x3c000000, v1
	v_mul_f32_e32 v24, 0x4f800000, v20
	v_cmp_gt_f32_e32 vcc, s2, v20
	v_mov_b32_e32 v102, v26
	v_mov_b32_e32 v103, v10
	v_cndmask_b32_e32 v31, v20, v24, vcc
	v_sqrt_f32_e32 v33, v31
	v_mov_b32_e32 v24, v18
	v_mov_b32_e32 v20, v25
	v_add_u32_e32 v18, -1, v33
	v_fma_f32 v25, -v18, v33, v31
	v_cmp_ge_f32_e64 s[2:3], 0, v25
	v_add_u32_e32 v25, 1, v33
	s_nop 0
	v_cndmask_b32_e64 v18, v33, v18, s[2:3]
	v_fma_f32 v33, -v25, v33, v31
	v_cmp_lt_f32_e64 s[2:3], 0, v33
	s_nop 1
	v_cndmask_b32_e64 v18, v18, v25, s[2:3]
	v_mul_f32_e32 v25, 0x37800000, v18
	v_cndmask_b32_e32 v18, v18, v25, vcc
	v_cmp_class_f32_e32 vcc, v31, v174
	v_mov_b32_e32 v25, v22
	s_nop 0
	v_cndmask_b32_e32 v18, v18, v31, vcc
	v_div_scale_f32 v31, s[2:3], v18, v18, 1.0
	v_rcp_f32_e32 v33, v31
	s_nop 0
	v_fma_f32 v22, -v31, v33, 1.0
	v_fmac_f32_e32 v33, v22, v33
	v_div_scale_f32 v22, vcc, 1.0, v18, 1.0
	v_mul_f32_e32 v35, v22, v33
	v_fma_f32 v45, -v31, v35, v22
	v_fmac_f32_e32 v35, v45, v33
	v_fma_f32 v22, -v31, v35, v22
	v_div_fmas_f32 v22, v22, v33, v35
	v_div_fixup_f32 v18, v22, v18, 1.0
	v_mul_f32_e32 v18, 0x3e0293ee, v18
	v_pk_mul_f32 v[98:99], v[18:19], v[98:99] op_sel_hi:[0,1]
	v_mov_b32_e32 v22, v19
	v_pk_mul_f32 v[98:99], v[98:99], v[22:23]
	v_pk_mul_f32 v[22:23], v[18:19], v[122:123] op_sel_hi:[0,1]
	v_pk_mul_f32 v[122:123], v[22:23], v[124:125]
	v_pk_mul_f32 v[22:23], v[18:19], v[126:127] op_sel_hi:[0,1]
	v_pk_mul_f32 v[124:125], v[22:23], v[20:21]
	v_pk_mul_f32 v[20:21], v[18:19], v[110:111] op_sel_hi:[0,1]
	v_pk_mul_f32 v[110:111], v[20:21], v[120:121]
	v_pk_mul_f32 v[20:21], v[18:19], v[104:105] op_sel_hi:[0,1]
	v_pk_mul_f32 v[104:105], v[20:21], v[14:15]
	v_pk_mul_f32 v[14:15], v[18:19], v[114:115] op_sel_hi:[0,1]
	v_pk_mul_f32 v[128:129], v[18:19], v[128:129] op_sel_hi:[0,1]
	v_pk_mul_f32 v[114:115], v[14:15], v[118:119]
	v_pk_mul_f32 v[14:15], v[18:19], v[116:117] op_sel_hi:[0,1]
	v_pk_mul_f32 v[24:25], v[24:25], v[128:129]
	v_pk_mul_f32 v[116:117], v[14:15], v[16:17]
	v_mov_b32_e32 v14, v10
	v_mov_b32_e32 v15, v26
	v_pk_mul_f32 v[14:15], v[14:15], v[24:25]
	v_mov_b32_e32 v26, v11
	v_sub_f32_e32 v19, v15, v14
	v_pk_mul_f32 v[14:15], v[26:27], v[98:99]
	v_mov_b32_e32 v10, v27
	v_sub_f32_e32 v31, v15, v14
	v_pk_mul_f32 v[14:15], v[102:103], v[24:25]
	v_pk_mul_f32 v[10:11], v[10:11], v[98:99]
	v_add_f32_e32 v33, v14, v15
	global_load_dwordx4 v[14:17], v[76:77], off offset:80
	global_load_dwordx4 v[20:23], v[76:77], off offset:64
	global_load_dwordx4 v[24:27], v[78:79], off offset:64
	v_add_f32_e32 v10, v10, v11
	v_cvt_pk_bf16_f32 v98, v33, v10
	v_mov_b32_e32 v10, v28
	v_mov_b32_e32 v11, v12
	v_pk_mul_f32 v[10:11], v[10:11], v[122:123]
	v_mov_b32_e32 v12, v29
	v_cvt_pk_bf16_f32 v102, v19, v31
	v_sub_f32_e32 v19, v10, v11
	v_pk_mul_f32 v[10:11], v[12:13], v[124:125]
	v_mov_b32_e32 v28, v13
	v_sub_f32_e32 v12, v10, v11
	v_pk_mul_f32 v[10:11], v[100:101], v[122:123]
	v_cvt_pk_bf16_f32 v103, v19, v12
	s_waitcnt vmcnt(3)
	v_mov_b32_e32 v13, v144
	v_add_f32_e32 v31, v10, v11
	v_pk_mul_f32 v[10:11], v[28:29], v[124:125]
	v_mov_b32_e32 v144, v137
	v_add_f32_e32 v10, v10, v11
	v_cvt_pk_bf16_f32 v99, v31, v10
	v_mov_b32_e32 v10, v2
	v_mov_b32_e32 v11, v6
	v_pk_mul_f32 v[10:11], v[10:11], v[110:111]
	v_mov_b32_e32 v6, v3
	v_mov_b32_e32 v2, v7
	v_sub_f32_e32 v12, v10, v11
	v_pk_mul_f32 v[10:11], v[6:7], v[104:105]
	v_pk_mul_f32 v[2:3], v[2:3], v[104:105]
	v_sub_f32_e32 v6, v10, v11
	v_pk_mul_f32 v[10:11], v[106:107], v[110:111]
	v_add_f32_e32 v2, v2, v3
	v_add_f32_e32 v10, v10, v11
	v_cvt_pk_bf16_f32 v100, v10, v2
	v_mov_b32_e32 v2, v4
	v_mov_b32_e32 v3, v8
	v_pk_mul_f32 v[2:3], v[2:3], v[114:115]
	v_mov_b32_e32 v8, v5
	v_cvt_pk_bf16_f32 v104, v12, v6
	v_sub_f32_e32 v4, v2, v3
	v_pk_mul_f32 v[2:3], v[8:9], v[116:117]
	global_load_dwordx4 v[6:9], v[96:97], off offset:16
	v_sub_f32_e32 v5, v2, v3
	v_pk_mul_f32 v[2:3], v[112:113], v[114:115]
	v_mov_b32_e32 v12, v136
	v_add_f32_e32 v10, v2, v3
	v_pk_mul_f32 v[2:3], v[108:109], v[116:117]
	v_cvt_pk_bf16_f32 v105, v4, v5
	v_mov_b32_e32 v4, v134
	v_add_f32_e32 v2, v2, v3
	v_cvt_pk_bf16_f32 v101, v10, v2
	v_pk_mul_f32 v[10:11], v[18:19], v[90:91] op_sel_hi:[0,1]
	v_pk_mul_f32 v[28:29], v[10:11], v[12:13]
	v_pk_mul_f32 v[10:11], v[18:19], v[88:89] op_sel_hi:[0,1]
	v_pk_mul_f32 v[96:97], v[10:11], v[144:145]
	v_pk_mul_f32 v[10:11], v[18:19], v[86:87] op_sel_hi:[0,1]
	v_mov_b32_e32 v12, v130
	v_mov_b32_e32 v13, v138
	v_pk_mul_f32 v[2:3], v[18:19], v[92:93] op_sel_hi:[0,1]
	v_mov_b32_e32 v5, v142
	v_pk_mul_f32 v[108:109], v[10:11], v[12:13]
	v_mov_b32_e32 v13, v140
	v_pk_mul_f32 v[88:89], v[18:19], v[80:81] op_sel_hi:[0,1]
	v_mov_b32_e32 v140, v133
	v_pk_mul_f32 v[2:3], v[2:3], v[4:5]
	v_pk_mul_f32 v[116:117], v[88:89], v[140:141]
	v_pk_mul_f32 v[4:5], v[18:19], v[94:95] op_sel_hi:[0,1]
	v_mov_b32_e32 v142, v135
	v_pk_mul_f32 v[10:11], v[18:19], v[84:85] op_sel_hi:[0,1]
	v_mov_b32_e32 v138, v131
	v_pk_mul_f32 v[4:5], v[4:5], v[142:143]
	v_pk_mul_f32 v[112:113], v[10:11], v[138:139]
	v_pk_mul_f32 v[10:11], v[18:19], v[82:83] op_sel_hi:[0,1]
	v_mov_b32_e32 v12, v132
	v_pk_mul_f32 v[114:115], v[10:11], v[12:13]
	global_load_dwordx4 v[10:13], v44, s[14:15] offset:272
	global_load_dwordx4 v[76:79], v44, s[14:15] offset:256
	global_load_dwordx4 v[80:83], v44, s[14:15] offset:400
	global_load_dwordx4 v[84:87], v44, s[14:15] offset:384
	v_add_co_u32_e32 v118, vcc, s4, v58
	s_waitcnt vmcnt(6)
; __device__ __forceinline__ unsigned pk2(float lo, float hi) { unsigned r; asm("v_cvt_pk_bf16_f32 %0, %1, %2" : "=v"(r) : "v"(lo), "v"(hi)); return r; }
; __device__ __forceinline__ void attn_dma_body(const bf16_t* __restrict__ Qb, int ldq, int tpos0, const float* __restrict__ rope, const float* __restrict__ qgain, ...
;     ...
;     for (int ax = 0; ax < 2; ++ax) { const int pos = ax ? (t & 63) : (t >> 6);
; #pragma unroll
;       for (int q = 0; q < 2; ++q) { const int dl = 4 * ax + q, dh = dl + 2, p0 = q * 16 + 8 * hi;
;         const float* cp_ = rope + pos * 32 + p0; const float* gl = qgain + dl * 16 + 8 * hi; const float* gh = qgain + dh * 16 + 8 * hi;
;         float cs[8], sn[8], lo[8], hv[8];
; #pragma unroll
;         for (int i = 0; i < 8; ++i) { cs[i] = cp_[i]; sn[i] = cp_[4096 + i];
;           lo[i] = bf2f((unsigned)(unsigned short)qr[dl][i]) * rinv * gl[i]; hv[i] = bf2f((unsigned)(unsigned short)qr[dh][i]) * rinv * gh[i]; }
;         u32x4 wl, wh;
; #pragma unroll
;         for (int i = 0; i < 4; ++i) { const float l0 = lo[2 * i] * cs[2 * i] - hv[2 * i] * sn[2 * i], l1 = lo[2 * i + 1] * cs[2 * i + 1] - hv[2 * i + 1] * sn[2 * i + 1];
;           const float h0 = hv[2 * i] * cs[2 * i] + lo[2 * i] * sn[2 * i], h1 = hv[2 * i + 1] * cs[2 * i + 1] + lo[2 * i + 1] * sn[2 * i + 1];
;           wl[i] = pk2(l0, l1); wh[i] = pk2(h0, h1); }
;         qr[dl] = *reinterpret_cast<bf16x8*>(&wl); qr[dh] = *reinterpret_cast<bf16x8*>(&wh); } } }
	v_mov_b32_e32 v88, v20
	s_waitcnt vmcnt(5)
	v_mov_b32_e32 v89, v24
	v_pk_mul_f32 v[88:89], v[88:89], v[2:3]
	v_addc_co_u32_e32 v119, vcc, 0, v59, vcc
	v_sub_f32_e32 v19, v88, v89
	v_mov_b32_e32 v88, v21
	v_mov_b32_e32 v89, v25
	v_pk_mul_f32 v[88:89], v[88:89], v[4:5]
	s_nop 0
	v_sub_f32_e32 v31, v88, v89
	v_mov_b32_e32 v88, v24
	v_mov_b32_e32 v89, v20
	v_pk_mul_f32 v[2:3], v[88:89], v[2:3]
	v_mov_b32_e32 v20, v25
	v_add_f32_e32 v24, v2, v3
	v_pk_mul_f32 v[2:3], v[20:21], v[4:5]
	v_cvt_pk_bf16_f32 v110, v19, v31
	s_nop 0
	v_add_f32_e32 v2, v2, v3
	v_cvt_pk_bf16_f32 v106, v24, v2
	v_mov_b32_e32 v2, v22
	v_mov_b32_e32 v3, v26
	v_pk_mul_f32 v[2:3], v[2:3], v[28:29]
	s_nop 0
	v_sub_f32_e32 v19, v2, v3
	v_mov_b32_e32 v2, v23
	v_mov_b32_e32 v3, v27
	v_pk_mul_f32 v[20:21], v[2:3], v[96:97]
	global_load_dwordx4 v[2:5], v[58:59], off offset:16
	global_load_dwordx4 v[88:91], v[58:59], off
	global_load_dwordx4 v[92:95], v[118:119], off
	v_sub_f32_e32 v24, v20, v21
	v_mov_b32_e32 v20, v26
	v_mov_b32_e32 v21, v22
	v_pk_mul_f32 v[20:21], v[20:21], v[28:29]
	v_mov_b32_e32 v22, v27
	v_add_f32_e32 v25, v20, v21
	v_pk_mul_f32 v[20:21], v[22:23], v[96:97]
	v_cvt_pk_bf16_f32 v111, v19, v24
	s_nop 0
	v_add_f32_e32 v20, v20, v21
	v_cvt_pk_bf16_f32 v107, v25, v20
	v_mov_b32_e32 v20, v14
	s_waitcnt vmcnt(7)
	v_mov_b32_e32 v21, v6
	v_pk_mul_f32 v[20:21], v[20:21], v[108:109]
	s_nop 0
	v_sub_f32_e32 v19, v20, v21
	v_mov_b32_e32 v20, v15
	v_mov_b32_e32 v21, v7
	v_pk_mul_f32 v[20:21], v[20:21], v[112:113]
	s_nop 0
	v_sub_f32_e32 v22, v20, v21
	v_mov_b32_e32 v21, v14
	v_mov_b32_e32 v14, v7
	v_mov_b32_e32 v20, v6
	v_pk_mul_f32 v[6:7], v[14:15], v[112:113]
	v_pk_mul_f32 v[20:21], v[20:21], v[108:109]
	v_add_f32_e32 v6, v6, v7
	v_add_f32_e32 v20, v20, v21
	v_cvt_pk_bf16_f32 v108, v20, v6
	v_mov_b32_e32 v6, v16
	v_mov_b32_e32 v7, v8
	v_cvt_pk_bf16_f32 v112, v19, v22
	v_pk_mul_f32 v[6:7], v[6:7], v[114:115]
	global_load_dwordx4 v[20:23], v[74:75], off offset:16
	v_sub_f32_e32 v14, v6, v7
	v_mov_b32_e32 v6, v17
	v_mov_b32_e32 v7, v9
	v_pk_mul_f32 v[6:7], v[6:7], v[116:117]
	s_nop 0
	v_sub_f32_e32 v15, v6, v7
	v_mov_b32_e32 v6, v8
	v_mov_b32_e32 v7, v16
	v_pk_mul_f32 v[6:7], v[6:7], v[114:115]
	v_mov_b32_e32 v16, v9
	v_add_f32_e32 v8, v6, v7
	v_pk_mul_f32 v[6:7], v[16:17], v[116:117]
	s_waitcnt vmcnt(4)
	v_mov_b32_e32 v9, v84
	v_add_f32_e32 v6, v6, v7
	v_cvt_pk_bf16_f32 v109, v8, v6
	v_pk_mul_f32 v[6:7], v[18:19], v[72:73] op_sel_hi:[0,1]
	v_mov_b32_e32 v8, v76
	v_pk_mul_f32 v[28:29], v[6:7], v[8:9]
	v_pk_mul_f32 v[6:7], v[18:19], v[70:71] op_sel_hi:[0,1]
	v_mov_b32_e32 v84, v77
	v_pk_mul_f32 v[70:71], v[6:7], v[84:85]
	v_pk_mul_f32 v[6:7], v[18:19], v[68:69] op_sel_hi:[0,1]
	v_mov_b32_e32 v8, v78
	v_mov_b32_e32 v9, v86
	v_pk_mul_f32 v[72:73], v[6:7], v[8:9]
	v_pk_mul_f32 v[6:7], v[18:19], v[66:67] op_sel_hi:[0,1]
	v_mov_b32_e32 v86, v79
	v_pk_mul_f32 v[74:75], v[6:7], v[86:87]
	v_pk_mul_f32 v[6:7], v[18:19], v[64:65] op_sel_hi:[0,1]
	v_mov_b32_e32 v8, v10
	v_mov_b32_e32 v9, v80
	v_pk_mul_f32 v[76:77], v[6:7], v[8:9]
	v_pk_mul_f32 v[6:7], v[18:19], v[62:63] op_sel_hi:[0,1]
	v_mov_b32_e32 v80, v11
	v_pk_mul_f32 v[10:11], v[18:19], v[60:61] op_sel_hi:[0,1]
	v_mov_b32_e32 v64, v12
	v_mov_b32_e32 v65, v82
	v_cvt_pk_bf16_f32 v113, v14, v15
	v_pk_mul_f32 v[78:79], v[6:7], v[80:81]
	global_load_dwordx4 v[6:9], v44, s[14:15] offset:336
	global_load_dwordx4 v[14:17], v44, s[14:15] offset:320
	global_load_dwordx4 v[24:27], v44, s[14:15] offset:464
	global_load_dwordx4 v[60:63], v44, s[14:15] offset:448
	v_pk_mul_f32 v[44:45], v[10:11], v[64:65]
	v_pk_mul_f32 v[10:11], v[18:19], v[54:55] op_sel_hi:[0,1]
	v_mov_b32_e32 v82, v13
	v_pk_mul_f32 v[80:81], v[10:11], v[82:83]
	s_waitcnt vmcnt(6)
	v_mov_b32_e32 v54, v88
	s_waitcnt vmcnt(5)
	v_mov_b32_e32 v55, v92
	v_pk_mul_f32 v[54:55], v[54:55], v[28:29]
	global_load_dwordx4 v[10:13], v[118:119], off offset:64
	v_sub_f32_e32 v19, v54, v55
	v_mov_b32_e32 v54, v89
	v_mov_b32_e32 v55, v93
	v_pk_mul_f32 v[54:55], v[54:55], v[70:71]
	s_nop 0
	v_sub_f32_e32 v31, v54, v55
	v_mov_b32_e32 v54, v92
	v_mov_b32_e32 v55, v88
	v_pk_mul_f32 v[28:29], v[54:55], v[28:29]
	v_mov_b32_e32 v88, v93
	v_add_f32_e32 v33, v28, v29
	v_pk_mul_f32 v[28:29], v[88:89], v[70:71]
	global_load_dwordx4 v[64:67], v[58:59], off offset:80
	global_load_dwordx4 v[68:71], v[58:59], off offset:64
	v_add_f32_e32 v28, v28, v29
	global_load_dwordx4 v[54:57], v[56:57], off offset:16
	v_cvt_pk_bf16_f32 v114, v33, v28
	v_mov_b32_e32 v28, v90
	v_mov_b32_e32 v29, v94
	v_pk_mul_f32 v[28:29], v[28:29], v[72:73]
	v_cvt_pk_bf16_f32 v118, v19, v31
	s_nop 0
	v_sub_f32_e32 v19, v28, v29
	v_mov_b32_e32 v28, v91
	v_mov_b32_e32 v29, v95
	v_pk_mul_f32 v[28:29], v[28:29], v[74:75]
	s_nop 0
	v_sub_f32_e32 v31, v28, v29
	v_mov_b32_e32 v28, v94
	v_mov_b32_e32 v29, v90
	v_pk_mul_f32 v[28:29], v[28:29], v[72:73]
	v_mov_b32_e32 v90, v95
	v_add_f32_e32 v33, v28, v29
	v_pk_mul_f32 v[28:29], v[90:91], v[74:75]
	v_cvt_pk_bf16_f32 v119, v19, v31
	s_nop 0
	v_add_f32_e32 v28, v28, v29
	v_cvt_pk_bf16_f32 v115, v33, v28
	v_mov_b32_e32 v28, v2
	s_waitcnt vmcnt(8)
	v_mov_b32_e32 v29, v20
	v_pk_mul_f32 v[28:29], v[28:29], v[76:77]
	s_nop 0
	v_sub_f32_e32 v19, v28, v29
	v_mov_b32_e32 v28, v3
	v_mov_b32_e32 v29, v21
	v_pk_mul_f32 v[28:29], v[28:29], v[78:79]
	s_nop 0
	v_sub_f32_e32 v31, v28, v29
	v_mov_b32_e32 v29, v2
	v_mov_b32_e32 v2, v21
	v_mov_b32_e32 v28, v20
	v_pk_mul_f32 v[2:3], v[2:3], v[78:79]
	v_pk_mul_f32 v[28:29], v[28:29], v[76:77]
	v_add_f32_e32 v2, v2, v3
	v_add_f32_e32 v20, v28, v29
	v_cvt_pk_bf16_f32 v116, v20, v2
	v_mov_b32_e32 v2, v4
	v_mov_b32_e32 v3, v22
	v_pk_mul_f32 v[2:3], v[2:3], v[44:45]
	v_cvt_pk_bf16_f32 v120, v19, v31
	s_nop 0
	v_sub_f32_e32 v19, v2, v3
	v_mov_b32_e32 v2, v5
	v_mov_b32_e32 v3, v23
	v_pk_mul_f32 v[2:3], v[2:3], v[80:81]
	s_nop 0
	v_sub_f32_e32 v20, v2, v3
	v_mov_b32_e32 v2, v22
	v_mov_b32_e32 v3, v4
	v_pk_mul_f32 v[2:3], v[2:3], v[44:45]
	v_mov_b32_e32 v4, v23
	v_add_f32_e32 v21, v2, v3
	v_pk_mul_f32 v[2:3], v[4:5], v[80:81]
	v_cvt_pk_bf16_f32 v121, v19, v20
	s_waitcnt vmcnt(6)
; __device__ __forceinline__ unsigned pk2(float lo, float hi) { unsigned r; asm("v_cvt_pk_bf16_f32 %0, %1, %2" : "=v"(r) : "v"(lo), "v"(hi)); return r; }
; __device__ __forceinline__ int v_rd_base(int lane) { return ((lane & 3) << 3) | (((lane >> 2) & 3) << 6) | (((lane >> 4) & 1) << 5) | (((lane >> 5) & 1) << 8); }
; #define ATT_WAIT_BAR() asm volatile("s_waitcnt vmcnt(0) lgkmcnt(0)\n\ts_barrier" ::: "memory")
; __device__ __forceinline__ void attn_dma_body(const bf16_t* __restrict__ Qb, int ldq, int tpos0, const float* __restrict__ rope, const float* __restrict__ qgain, ...
;     ...
;         for (int i = 0; i < 4; ++i) { const float l0 = lo[2 * i] * cs[2 * i] - hv[2 * i] * sn[2 * i], l1 = lo[2 * i + 1] * cs[2 * i + 1] - hv[2 * i + 1] * sn[2 * i + 1];
;           const float h0 = hv[2 * i] * cs[2 * i] + lo[2 * i] * sn[2 * i], h1 = hv[2 * i + 1] * cs[2 * i + 1] + lo[2 * i + 1] * sn[2 * i + 1];
;           wl[i] = pk2(l0, l1); wh[i] = pk2(h0, h1); }
;         qr[dl] = *reinterpret_cast<bf16x8*>(&wl); qr[dh] = *reinterpret_cast<bf16x8*>(&wh); } } }
; #pragma unroll
;   for (int d0 = 0; d0 < 8; ++d0) asm volatile("" : "+v"(qr[d0]));
;   ATT_WAIT_BAR();
;   if (2 < NT) ATT_DMA(2, 2);
;   const int vb0 = (int)(uintptr_t)lds + 16384 + v_rd_base(lane);
;   f32x16 pA0, pA1, pB0, pB1; float mnA, mnB, alA, alB; bf16x8 pa0, pa1, pa2, pa3;
;   qkt(pA0, pA1, (const bf16_t*)lds, qr, r32, hi); partialSM(pA0, pA1, m_reg, mnA, alA);
	v_mov_b32_e32 v4, v14
	v_add_f32_e32 v2, v2, v3
	v_cvt_pk_bf16_f32 v117, v21, v2
	s_waitcnt vmcnt(4)
	v_mov_b32_e32 v5, v60
	v_mov_b32_e32 v60, v15
	v_pk_mul_f32 v[14:15], v[18:19], v[48:49] op_sel_hi:[0,1]
	v_mov_b32_e32 v20, v16
	v_mov_b32_e32 v21, v62
	v_pk_mul_f32 v[14:15], v[14:15], v[20:21]
	v_pk_mul_f32 v[20:21], v[18:19], v[46:47] op_sel_hi:[0,1]
	v_mov_b32_e32 v62, v17
	v_pk_mul_f32 v[16:17], v[20:21], v[62:63]
	v_pk_mul_f32 v[20:21], v[18:19], v[42:43] op_sel_hi:[0,1]
	v_mov_b32_e32 v22, v6
	v_mov_b32_e32 v23, v24
	v_pk_mul_f32 v[2:3], v[18:19], v[52:53] op_sel_hi:[0,1]
	v_pk_mul_f32 v[20:21], v[20:21], v[22:23]
	v_pk_mul_f32 v[22:23], v[18:19], v[40:41] op_sel_hi:[0,1]
	v_mov_b32_e32 v24, v7
	v_pk_mul_f32 v[2:3], v[2:3], v[4:5]
	v_pk_mul_f32 v[4:5], v[18:19], v[50:51] op_sel_hi:[0,1]
	v_pk_mul_f32 v[6:7], v[22:23], v[24:25]
	v_pk_mul_f32 v[22:23], v[18:19], v[38:39] op_sel_hi:[0,1]
	v_mov_b32_e32 v25, v26
	v_pk_mul_f32 v[18:19], v[18:19], v[36:37] op_sel_hi:[0,1]
	v_mov_b32_e32 v26, v9
	v_mov_b32_e32 v24, v8
	v_pk_mul_f32 v[8:9], v[18:19], v[26:27]
	s_waitcnt vmcnt(1)
	v_mov_b32_e32 v18, v68
	v_mov_b32_e32 v19, v10
	v_pk_mul_f32 v[18:19], v[18:19], v[2:3]
	v_pk_mul_f32 v[4:5], v[4:5], v[60:61]
	v_pk_mul_f32 v[22:23], v[22:23], v[24:25]
	v_sub_f32_e32 v24, v18, v19
	v_mov_b32_e32 v18, v69
	v_mov_b32_e32 v19, v11
	v_pk_mul_f32 v[18:19], v[18:19], v[4:5]
	s_nop 0
	v_sub_f32_e32 v25, v18, v19
	v_mov_b32_e32 v18, v10
	v_mov_b32_e32 v19, v68
	v_pk_mul_f32 v[2:3], v[18:19], v[2:3]
	v_mov_b32_e32 v68, v11
	v_add_f32_e32 v10, v2, v3
	v_pk_mul_f32 v[2:3], v[68:69], v[4:5]
	v_cvt_pk_bf16_f32 v126, v24, v25
	s_nop 0
	v_add_f32_e32 v2, v2, v3
	v_cvt_pk_bf16_f32 v122, v10, v2
	v_mov_b32_e32 v2, v70
	v_mov_b32_e32 v3, v12
	v_pk_mul_f32 v[2:3], v[2:3], v[14:15]
	s_nop 0
	v_sub_f32_e32 v4, v2, v3
	v_mov_b32_e32 v2, v71
	v_mov_b32_e32 v3, v13
	v_pk_mul_f32 v[2:3], v[2:3], v[16:17]
	s_nop 0
	v_sub_f32_e32 v5, v2, v3
	v_mov_b32_e32 v2, v12
	v_mov_b32_e32 v3, v70
	v_pk_mul_f32 v[2:3], v[2:3], v[14:15]
	v_mov_b32_e32 v70, v13
	v_add_f32_e32 v10, v2, v3
	v_pk_mul_f32 v[2:3], v[70:71], v[16:17]
	v_cvt_pk_bf16_f32 v127, v4, v5
	s_nop 0
	v_add_f32_e32 v2, v2, v3
	v_cvt_pk_bf16_f32 v123, v10, v2
	v_mov_b32_e32 v2, v64
	s_waitcnt vmcnt(0)
	v_mov_b32_e32 v3, v54
	v_pk_mul_f32 v[2:3], v[2:3], v[20:21]
	s_nop 0
	v_sub_f32_e32 v4, v2, v3
	v_mov_b32_e32 v2, v65
	v_mov_b32_e32 v3, v55
	v_pk_mul_f32 v[2:3], v[2:3], v[6:7]
	s_nop 0
	v_sub_f32_e32 v5, v2, v3
	v_mov_b32_e32 v2, v54
	v_mov_b32_e32 v3, v64
	v_pk_mul_f32 v[2:3], v[2:3], v[20:21]
	v_mov_b32_e32 v64, v55
	v_add_f32_e32 v10, v2, v3
	v_pk_mul_f32 v[2:3], v[64:65], v[6:7]
	v_cvt_pk_bf16_f32 v128, v4, v5
	s_nop 0
	v_add_f32_e32 v2, v2, v3
	v_cvt_pk_bf16_f32 v124, v10, v2
	v_mov_b32_e32 v2, v66
	v_mov_b32_e32 v3, v56
	v_pk_mul_f32 v[2:3], v[2:3], v[22:23]
	s_nop 0
	v_sub_f32_e32 v4, v2, v3
	v_mov_b32_e32 v2, v67
	v_mov_b32_e32 v3, v57
	v_pk_mul_f32 v[2:3], v[2:3], v[8:9]
	s_nop 0
	v_sub_f32_e32 v5, v2, v3
	v_mov_b32_e32 v2, v56
	v_mov_b32_e32 v3, v66
	v_pk_mul_f32 v[2:3], v[2:3], v[22:23]
	v_mov_b32_e32 v66, v57
	v_add_f32_e32 v6, v2, v3
	v_pk_mul_f32 v[2:3], v[66:67], v[8:9]
	v_cvt_pk_bf16_f32 v129, v4, v5
	s_nop 0
	v_add_f32_e32 v2, v2, v3
	v_cvt_pk_bf16_f32 v125, v6, v2
.LBB0_408:
	s_add_u32 s2, s38, 0x8000
	s_addc_u32 s3, s39, 0
	s_add_u32 s4, s40, 0x8000
	v_mov_b32_e32 v31, v163
	s_waitcnt vmcnt(0)
	s_waitcnt vmcnt(0) lgkmcnt(0)
	s_barrier
	s_addc_u32 s5, s41, 0
	s_add_i32 m0, s96, 0x10000
	s_add_i32 s6, s96, 0x14000
	v_lshl_add_u64 v[2:3], s[2:3], 0, v[162:163]
	v_mov_b32_e32 v33, v163
	global_load_lds_dwordx4 v[2:3], off
	v_lshl_add_u64 v[2:3], s[4:5], 0, v[30:31]
	s_mov_b32 m0, s6
	v_mov_b32_e32 v35, v163
	global_load_lds_dwordx4 v[2:3], off
	v_lshl_add_u64 v[2:3], s[2:3], 0, v[32:33]
	s_add_i32 m0, s96, 0x12000
	v_lshlrev_b32_e32 v10, 8, v177
	global_load_lds_dwordx4 v[2:3], off
	v_lshl_add_u64 v[2:3], s[4:5], 0, v[34:35]
	s_add_i32 m0, s96, 0x16000
	v_and_b32_e32 v167, 63, v147
	global_load_lds_dwordx4 v[2:3], off
	v_lshlrev_b32_e32 v2, 4, v177
	v_and_b32_e32 v11, 0x70, v2
	v_bitop3_b32 v183, v166, v10, v11 bitop3:0xde
	v_add_u32_e32 v6, 0, v183
	ds_read_b128 v[2:5], v6
	ds_read_b128 v[6:9], v6 offset:8192
	s_waitcnt lgkmcnt(0)
	v_mfma_f32_32x32x16_bf16 v[18:33], v[2:5], v[102:105], 0
	v_or_b32_e32 v2, 32, v166
	v_bitop3_b32 v184, v2, v10, v11 bitop3:0xde
	v_and_b32_e32 v12, 0x3fffffc0, v147
	v_lshl_add_u32 v165, v12, 2, s90
	v_lshlrev_b32_e32 v12, 3, v167
	s_cmp_lg_u32 0, -1
	s_cselect_b32 s2, 0, 0
	v_mfma_f32_32x32x16_bf16 v[34:49], v[6:9], v[102:105], 0
	v_add_u32_e32 v6, 0, v184
	ds_read_b128 v[2:5], v6
	ds_read_b128 v[6:9], v6 offset:8192
	s_addk_i32 s2, 0x4000
	s_mov_b32 s72, s73
	s_mov_b32 s74, s73
	s_mov_b32 s75, s73
	s_mov_b32 s76, s73
	s_waitcnt lgkmcnt(0)
	v_mfma_f32_32x32x16_bf16 v[18:33], v[2:5], v[110:113], v[18:33]
	v_or_b32_e32 v2, 64, v166
	v_bitop3_b32 v186, v2, v10, v11 bitop3:0xde
	s_mov_b32 s77, s73
	s_mov_b32 s78, s73
	s_mov_b32 s79, s73
	s_mov_b32 s80, s73
	s_mov_b32 s81, s73
	v_mfma_f32_32x32x16_bf16 v[34:49], v[6:9], v[110:113], v[34:49]
	v_add_u32_e32 v6, 0, v186
	ds_read_b128 v[2:5], v6
	ds_read_b128 v[6:9], v6 offset:8192
	s_mov_b32 s82, s73
	s_mov_b32 s83, s73
	s_mov_b32 s84, s73
	s_mov_b32 s85, s73
	s_mov_b32 s86, s73
	s_waitcnt lgkmcnt(0)
	v_mfma_f32_32x32x16_bf16 v[18:33], v[2:5], v[98:101], v[18:33]
	v_or_b32_e32 v2, 0x60, v166
	v_bitop3_b32 v185, v2, v10, v11 bitop3:0xde
	s_mov_b32 s87, s73
	s_mov_b32 s36, 0x10000
	s_mov_b32 s97, -1
	v_lshl_add_u32 v180, v177, 2, v165
	v_mov_b32_e32 v169, v163
	v_mfma_f32_32x32x16_bf16 v[34:49], v[6:9], v[98:101], v[34:49]
	v_add_u32_e32 v6, 0, v185
	ds_read_b128 v[2:5], v6
	ds_read_b128 v[6:9], v6 offset:8192
	v_add_u32_e32 v170, v149, v150
	v_mov_b32_e32 v171, v163
	v_add_u32_e32 v172, v151, v152
	v_mov_b32_e32 v173, v163
	v_mov_b32_e32 v182, 0
	s_waitcnt lgkmcnt(0)
; __device__ __forceinline__ void partialSM(f32x16& p0, f32x16& p1, float& m_reg, float& mn, float& alpha) {
;   constexpr float C = SCALE * 1.4426950408889634f;
;   float pmax = p0[0]; for (int r = 1; r < 16; ++r) pmax = fmaxf(pmax, p0[r]); for (int r = 0; r < 16; ++r) pmax = fmaxf(pmax, p1[r]);
;   { auto rr = __builtin_amdgcn_permlane32_swap(__float_as_uint(pmax), __float_as_uint(pmax), false, false);
;     pmax = fmaxf(__uint_as_float(rr[0]), __uint_as_float(rr[1])); }
;   if (__builtin_expect(__all(pmax - m_reg <= THR / SCALE), 1)) { mn = m_reg; alpha = 1.f; }
;   else { mn = fmaxf(m_reg, pmax); alpha = __builtin_amdgcn_exp2f((m_reg - mn) * C); m_reg = mn; }
;   float mnC = -mn * C;
;   for (int r = 0; r < 16; ++r) p0[r] = fmaf(p0[r], C, mnC); for (int r = 0; r < 16; ++r) p1[r] = fmaf(p1[r], C, mnC);
;   for (int r = 0; r < 16; ++r) p0[r] = __builtin_amdgcn_exp2f(p0[r]);
; }
; __device__ __forceinline__ void finishSM(f32x16& p0, f32x16& p1, float alpha, float& l_reg, bf16x8& pa0, bf16x8& pa1, bf16x8& pa2, bf16x8& pa3) {
;   for (int r = 0; r < 16; ++r) p1[r] = __builtin_amdgcn_exp2f(p1[r]);
;   float ps = 0; for (int r = 0; r < 16; ++r) ps += p0[r]; for (int r = 0; r < 16; ++r) ps += p1[r];
;   { auto rr = __builtin_amdgcn_permlane32_swap(__float_as_uint(ps), __float_as_uint(ps), false, false);
;     ps = __uint_as_float(rr[0]) + __uint_as_float(rr[1]); }
;   l_reg = l_reg * alpha + ps;
;     ...
;   PK4(p0, 0, pa0); PK4(p0, 8, pa1); PK4(p1, 0, pa2); PK4(p1, 8, pa3);
;     ...
; }
; __device__ __forceinline__ void qkt(f32x16& p0, f32x16& p1, const bf16_t* Ks, const bf16x8* qr, int r32, int hi) {
;   p0 = f32x16{}; p1 = f32x16{};
; __device__ __forceinline__ void attn_dma_body(const bf16_t* __restrict__ Qb, int ldq, int tpos0, const float* __restrict__ rope, const float* __restrict__ qgain, ...
;     ...
;   qkt(pA0, pA1, (const bf16_t*)lds, qr, r32, hi); partialSM(pA0, pA1, m_reg, mnA, alA);
;   const bool lead = __builtin_amdgcn_readfirstlane(wid) < 4;
;     ...
;   for (int j = 1; j + 1 < NT; j += 2) {
;     { SBAR(); qkt(pB0, pB1, (const bf16_t*)(lds + (j & 3) * SHM_SLOT), qr, r32, hi);
;       finishSM(pA0, pA1, alA, l_reg, pa0, pa1, pa2, pa3); s16x4 va[8]; pv_rd<0>(va, vb0 + ((j - 1) & 3) * (int)SHM_SLOT); SBAR();
;       if (!lead) ATT_SYNC(j + 2);
;       pv_d0_pre(o, vb0 + ((j - 1) & 3) * (int)SHM_SLOT, va, pa0, pa1, pa2, pa3); partialSM(pB0, pB1, m_reg, mnB, alB);
	v_mfma_f32_32x32x16_bf16 v[18:33], v[2:5], v[106:109], v[18:33]
	v_or_b32_e32 v2, 0x80, v166
	v_bitop3_b32 v187, v2, v10, v11 bitop3:0xde
	v_mfma_f32_32x32x16_bf16 v[34:49], v[6:9], v[106:109], v[34:49]
	v_add_u32_e32 v6, 0, v187
	ds_read_b128 v[2:5], v6
	ds_read_b128 v[6:9], v6 offset:8192
	s_waitcnt lgkmcnt(0)
	v_mfma_f32_32x32x16_bf16 v[18:33], v[2:5], v[118:121], v[18:33]
	v_or_b32_e32 v2, 0xa0, v166
	v_bitop3_b32 v188, v2, v10, v11 bitop3:0xde
	v_add_u32_e32 v13, 0, v188
	ds_read_b128 v[2:5], v13
	v_mfma_f32_32x32x16_bf16 v[34:49], v[6:9], v[118:121], v[34:49]
	v_lshlrev_b32_e32 v6, 4, v167
	v_and_b32_e32 v6, 0xc0, v6
	v_and_or_b32 v14, v12, 24, v6
	v_lshlrev_b32_e32 v6, 1, v167
	v_and_b32_e32 v15, 32, v6
	v_and_b32_e32 v12, 0x100, v12
	v_or3_b32 v181, v14, v15, v12
	s_waitcnt lgkmcnt(0)
	v_mfma_f32_32x32x16_bf16 v[18:33], v[2:5], v[126:129], v[18:33]
	v_or_b32_e32 v2, 0xc0, v166
	v_bitop3_b32 v189, v2, v10, v11 bitop3:0xde
	v_add_u32_e32 v12, 0, v189
	ds_read_b128 v[6:9], v13 offset:8192
	ds_read_b128 v[2:5], v12
	v_add_u32_e32 v191, s2, v181
	v_readfirstlane_b32 s2, v179
	s_waitcnt lgkmcnt(0)
	v_mfma_f32_32x32x16_bf16 v[34:49], v[6:9], v[126:129], v[34:49]
	ds_read_b128 v[6:9], v12 offset:8192
	s_cmp_lt_i32 s2, 4
	s_cselect_b64 s[34:35], -1, 0
	s_cmp_gt_i32 s2, 3
	s_cselect_b64 s[38:39], -1, 0
	v_cmp_gt_u32_e64 s[2:3], 32, v167
	v_mfma_f32_32x32x16_bf16 v[18:33], v[2:5], v[114:117], v[18:33]
	v_or_b32_e32 v2, 0xe0, v166
	v_bitop3_b32 v190, v2, v10, v11 bitop3:0xde
	v_add_u32_e32 v10, 0, v190
	ds_read_b128 v[2:5], v10
	ds_read_b128 v[50:53], v10 offset:8192
	s_waitcnt lgkmcnt(0)
	v_mfma_f32_32x32x16_bf16 v[18:33], v[2:5], v[122:125], v[18:33]
	v_mfma_f32_32x32x16_bf16 v[34:49], v[6:9], v[114:117], v[34:49]
	s_nop 10
	v_mov_b64_e32 v[2:3], s[72:73]
	v_mov_b64_e32 v[16:17], s[86:87]
	v_mov_b64_e32 v[4:5], s[74:75]
	v_mov_b64_e32 v[6:7], s[76:77]
	v_mfma_f32_32x32x16_bf16 v[34:49], v[50:53], v[122:125], v[34:49]
	s_nop 4
	v_exp_f32_e32 v203, v18
	v_exp_f32_e32 v207, v19
	v_exp_f32_e32 v204, v20
	v_exp_f32_e32 v208, v21
	v_exp_f32_e32 v205, v22
	v_exp_f32_e32 v209, v23
	v_exp_f32_e32 v202, v24
	v_exp_f32_e32 v206, v25
	v_exp_f32_e32 v159, v26
	v_exp_f32_e32 v199, v27
	v_exp_f32_e32 v160, v28
	v_exp_f32_e32 v200, v29
	v_exp_f32_e32 v157, v30
	v_exp_f32_e32 v161, v31
	v_exp_f32_e32 v158, v32
	v_exp_f32_e32 v201, v33
	v_add3_u32 v18, v154, v148, v156
	v_lshlrev_b32_e32 v19, 1, v147
	v_lshlrev_b32_e32 v20, 4, v147
	v_mov_b64_e32 v[130:131], v[48:49]
	v_mov_b64_e32 v[132:133], v[46:47]
	v_mov_b64_e32 v[134:135], v[44:45]
	v_mov_b64_e32 v[136:137], v[42:43]
	v_mov_b64_e32 v[138:139], v[40:41]
	v_mov_b64_e32 v[140:141], v[38:39]
	v_mov_b64_e32 v[142:143], v[36:37]
	v_mov_b64_e32 v[144:145], v[34:35]
	v_add_lshl_u32 v18, v18, v146, 8
	v_and_b32_e32 v19, 0xc0, v19
	v_and_b32_e32 v20, 48, v20
	v_or3_b32 v162, v18, v19, v20
	v_add3_u32 v18, v153, v148, v155
	v_add_lshl_u32 v18, v18, v146, 8
	v_mov_b64_e32 v[8:9], s[78:79]
	v_mov_b64_e32 v[10:11], s[80:81]
	v_mov_b64_e32 v[12:13], s[82:83]
	v_mov_b64_e32 v[14:15], s[84:85]
	v_mov_b32_e32 v192, 1.0
	s_add_u32 s40, s28, s69
	v_or3_b32 v168, v18, v19, v20
	v_mov_b64_e32 v[64:65], v[16:17]
	v_mov_b64_e32 v[48:49], v[16:17]
	v_mov_b64_e32 v[32:33], v[16:17]
	s_addc_u32 s41, s29, s65
	v_mov_b64_e32 v[62:63], v[14:15]
	v_mov_b64_e32 v[60:61], v[12:13]
	v_mov_b64_e32 v[58:59], v[10:11]
	v_mov_b64_e32 v[56:57], v[8:9]
	v_mov_b64_e32 v[54:55], v[6:7]
	v_mov_b64_e32 v[52:53], v[4:5]
	v_mov_b64_e32 v[50:51], v[2:3]
	v_mov_b64_e32 v[46:47], v[14:15]
	v_mov_b64_e32 v[44:45], v[12:13]
	v_mov_b64_e32 v[42:43], v[10:11]
	v_mov_b64_e32 v[40:41], v[8:9]
	v_mov_b64_e32 v[38:39], v[6:7]
	v_mov_b64_e32 v[36:37], v[4:5]
	v_mov_b64_e32 v[34:35], v[2:3]
	v_mov_b64_e32 v[30:31], v[14:15]
	v_mov_b64_e32 v[28:29], v[12:13]
	v_mov_b64_e32 v[26:27], v[10:11]
	v_mov_b64_e32 v[24:25], v[8:9]
	v_mov_b64_e32 v[22:23], v[6:7]
	v_mov_b64_e32 v[20:21], v[4:5]
	v_mov_b64_e32 v[18:19], v[2:3]
	s_and_b64 vcc, exec, s[38:39]
	s_cbranch_vccz .Lprio_skip
	s_setprio 1
.Lprio_skip:
.LBB0_409:
	s_add_i32 s4, s36, 0xffff8000
	s_and_b32 s69, s4, 0x18000
	s_add_i32 s4, s69, 0
	v_add_u32_e32 v70, s4, v183
	ds_read_b128 v[66:69], v70
	ds_read_b128 v[70:73], v70 offset:8192
	v_add_u32_e32 v154, s4, v186
	v_add_u32_e32 v155, s4, v185
	v_add_u32_e32 v156, s4, v187
	s_waitcnt lgkmcnt(0)
	v_mfma_f32_32x32x16_bf16 v[82:97], v[66:69], v[102:105], 0
	v_add_u32_e32 v66, s4, v184
	ds_read_b128 v[146:149], v66
	ds_read_b128 v[150:153], v66 offset:8192
	ds_read_b128 v[194:197], v154
	ds_read_b128 v[210:213], v154 offset:8192
	ds_read_b128 v[214:217], v155
	ds_read_b128 v[218:221], v155 offset:8192
	ds_read_b128 v[222:225], v156
	ds_read_b128 v[226:229], v156 offset:8192
	v_add_u32_e32 v154, s4, v188
	v_exp_f32_e32 v144, v144
	v_exp_f32_e32 v145, v145
	v_exp_f32_e32 v142, v142
	v_mfma_f32_32x32x16_bf16 v[66:81], v[70:73], v[102:105], 0
	v_exp_f32_e32 v143, v143
	v_exp_f32_e32 v140, v140
	v_exp_f32_e32 v141, v141
	v_exp_f32_e32 v155, v139
	v_exp_f32_e32 v156, v136
	v_exp_f32_e32 v198, v135
	v_exp_f32_e32 v246, v132
	s_waitcnt lgkmcnt(0)
; __device__ __forceinline__ void finishSM(f32x16& p0, f32x16& p1, float alpha, float& l_reg, bf16x8& pa0, bf16x8& pa1, bf16x8& pa2, bf16x8& pa3) {
;   for (int r = 0; r < 16; ++r) p1[r] = __builtin_amdgcn_exp2f(p1[r]);
;   float ps = 0; for (int r = 0; r < 16; ++r) ps += p0[r]; for (int r = 0; r < 16; ++r) ps += p1[r];
;   { auto rr = __builtin_amdgcn_permlane32_swap(__float_as_uint(ps), __float_as_uint(ps), false, false);
;     ps = __uint_as_float(rr[0]) + __uint_as_float(rr[1]); }
;   l_reg = l_reg * alpha + ps;
;     ...
;   PK4(p0, 0, pa0); PK4(p0, 8, pa1); PK4(p1, 0, pa2); PK4(p1, 8, pa3);
;     ...
; }
; __device__ __forceinline__ void qkt(f32x16& p0, f32x16& p1, const bf16_t* Ks, const bf16x8* qr, int r32, int hi) {
;   p0 = f32x16{}; p1 = f32x16{};
;   for (int d0 = 0; d0 < 8; ++d0) { int cb = (d0 * 16 + hi * 8) * 2;
;     bf16x8 b0 = *reinterpret_cast<const bf16x8*>((const char*)Ks + KSWZ(r32, cb));
;     bf16x8 b1 = *reinterpret_cast<const bf16x8*>((const char*)Ks + KSWZ(32 + r32, cb));
;     p0 = __builtin_amdgcn_mfma_f32_32x32x16_bf16(b0, qr[d0], p0, 0, 0, 0);
;     p1 = __builtin_amdgcn_mfma_f32_32x32x16_bf16(b1, qr[d0], p1, 0, 0, 0); }
; }
; __device__ __forceinline__ int v_st(int k, int c) { const int kk = (k & ~0xC) | ((k & 4) << 1) | ((k & 8) >> 1); return ((kk >> 3) * 4 + (c >> 5)) * 512 + ((kk & 7) * 32 + (c & 31)) * 2; }
; __device__ __forceinline__ int v_rd_base(int lane) { return ((lane & 3) << 3) | (((lane >> 2) & 3) << 6) | (((lane >> 4) & 1) << 5) | (((lane >> 5) & 1) << 8); }
; template <int OFF> __device__ __forceinline__ s16x4 tr_read(int vb) {
;   s16x4 r; asm volatile("ds_read_b64_tr_b16 %0, %1 offset:%2" : "=&v"(r) : "v"(vb), "i"(OFF) : "memory"); return r;
; }
; template <int D0> __device__ __forceinline__ void pv_one(f32x16& od, int vb, bf16x8 pa0, bf16x8 pa1, bf16x8 pa2, bf16x8 pa3) {
;   const s16x4 l0 = tr_read<v_rd_off(D0, 0, 0)>(vb), h0 = tr_read<v_rd_off(D0, 0, 1)>(vb), l1 = tr_read<v_rd_off(D0, 1, 0)>(vb), h1 = tr_read<v_rd_off(D0, 1, 1)>(vb);
;   const s16x4 l2 = tr_read<v_rd_off(D0, 2, 0)>(vb), h2 = tr_read<v_rd_off(D0, 2, 1)>(vb), l3 = tr_read<v_rd_off(D0, 3, 0)>(vb), h3 = tr_read<v_rd_off(D0, 3, 1)>(vb);
;   asm volatile("s_waitcnt lgkmcnt(0)" ::: "memory"); SBAR();
;     ...
;   od = __builtin_amdgcn_mfma_f32_32x32x16_bf16(pa0, PK(l0, h0), od, 0, 0, 0);
;   od = __builtin_amdgcn_mfma_f32_32x32x16_bf16(pa1, PK(l1, h1), od, 0, 0, 0);
	v_mfma_f32_32x32x16_bf16 v[82:97], v[146:149], v[110:113], v[82:97]
	ds_read_b128 v[146:149], v154
	ds_read_b128 v[230:233], v154 offset:8192
	v_add_u32_e32 v154, s4, v189
	ds_read_b128 v[234:237], v154
	ds_read_b128 v[238:241], v154 offset:8192
	v_add_u32_e32 v154, s4, v190
	s_add_i32 s37, s36, 0x10000
	s_and_b32 s65, s37, 0x18000
	v_mfma_f32_32x32x16_bf16 v[66:81], v[150:153], v[110:113], v[66:81]
	ds_read_b128 v[150:153], v154
	ds_read_b128 v[242:245], v154 offset:8192
	v_exp_f32_e32 v154, v138
	v_mfma_f32_32x32x16_bf16 v[82:97], v[194:197], v[98:101], v[82:97]
	v_exp_f32_e32 v196, v137
	v_exp_f32_e32 v197, v134
	v_mfma_f32_32x32x16_bf16 v[66:81], v[210:213], v[98:101], v[66:81]
	v_exp_f32_e32 v211, v130
	v_add_f32_e32 v130, v207, v203
	v_add_f32_e32 v130, v204, v130
	v_add_f32_e32 v130, v208, v130
	v_add_f32_e32 v130, v205, v130
	v_add_f32_e32 v130, v209, v130
	v_mfma_f32_32x32x16_bf16 v[82:97], v[214:217], v[106:109], v[82:97]
	v_add_f32_e32 v130, v202, v130
	v_add_f32_e32 v130, v206, v130
	v_add_f32_e32 v130, v159, v130
	v_add_f32_e32 v130, v199, v130
	v_add_f32_e32 v130, v160, v130
	v_add_f32_e32 v130, v200, v130
	v_add_f32_e32 v130, v157, v130
	v_mfma_f32_32x32x16_bf16 v[66:81], v[218:221], v[106:109], v[66:81]
	v_add_f32_e32 v130, v161, v130
	v_add_f32_e32 v130, v158, v130
	v_add_f32_e32 v130, v201, v130
	v_add_f32_e32 v130, v144, v130
	v_add_f32_e32 v130, v145, v130
	v_add_f32_e32 v130, v142, v130
	v_add_f32_e32 v130, v143, v130
	v_mfma_f32_32x32x16_bf16 v[82:97], v[222:225], v[118:121], v[82:97]
	v_add_f32_e32 v130, v140, v130
	v_add_f32_e32 v130, v141, v130
	v_add_f32_e32 v130, v154, v130
	v_add_f32_e32 v130, v155, v130
	v_add_f32_e32 v130, v156, v130
	v_exp_f32_e32 v210, v133
	v_add_f32_e32 v130, v196, v130
	v_mfma_f32_32x32x16_bf16 v[66:81], v[226:229], v[118:121], v[66:81]
	v_add_f32_e32 v130, v197, v130
	v_exp_f32_e32 v212, v131
	v_add_f32_e32 v130, v198, v130
	v_add_f32_e32 v130, v246, v130
	v_add_f32_e32 v130, v210, v130
	v_add_f32_e32 v130, v211, v130
	v_add_f32_e32 v194, v212, v130
	s_waitcnt lgkmcnt(0)
	v_mfma_f32_32x32x16_bf16 v[82:97], v[146:149], v[126:129], v[82:97]
	v_cvt_pk_bf16_f32 v130, v203, v207
	v_cvt_pk_bf16_f32 v131, v204, v208
	v_cvt_pk_bf16_f32 v132, v205, v209
	v_cvt_pk_bf16_f32 v133, v202, v206
	v_cvt_pk_bf16_f32 v134, v159, v199
	v_cvt_pk_bf16_f32 v135, v160, v200
	v_cvt_pk_bf16_f32 v136, v157, v161
	v_mfma_f32_32x32x16_bf16 v[66:81], v[230:233], v[126:129], v[66:81]
	v_cvt_pk_bf16_f32 v137, v158, v201
	v_cvt_pk_bf16_f32 v138, v144, v145
	v_cvt_pk_bf16_f32 v139, v142, v143
	v_cvt_pk_bf16_f32 v140, v140, v141
	v_cvt_pk_bf16_f32 v141, v154, v155
	v_cvt_pk_bf16_f32 v142, v156, v196
	v_cvt_pk_bf16_f32 v143, v197, v198
	v_mfma_f32_32x32x16_bf16 v[82:97], v[234:237], v[114:117], v[82:97]
	v_cvt_pk_bf16_f32 v144, v246, v210
	v_cvt_pk_bf16_f32 v145, v211, v212
	v_add_u32_e32 v196, s65, v191
	ds_read_b64_tr_b16 v[158:159], v196 offset:0
	ds_read_b64_tr_b16 v[160:161], v196 offset:0x800
	ds_read_b64_tr_b16 v[154:155], v196 offset:0x1000
	ds_read_b64_tr_b16 v[156:157], v196 offset:0x1800
	v_mfma_f32_32x32x16_bf16 v[66:81], v[238:241], v[114:117], v[66:81]
	v_mov_b32_e32 v195, v194
	s_nop 1
	v_permlane32_swap_b32_e32 v194, v195
	v_mfma_f32_32x32x16_bf16 v[82:97], v[150:153], v[122:125], v[82:97]
	ds_read_b64_tr_b16 v[150:151], v196 offset:0x2000
	ds_read_b64_tr_b16 v[152:153], v196 offset:0x2800
	ds_read_b64_tr_b16 v[146:147], v196 offset:0x3000
	ds_read_b64_tr_b16 v[148:149], v196 offset:0x3800
	v_mfma_f32_32x32x16_bf16 v[66:81], v[242:245], v[122:125], v[66:81]
	s_andn2_b64 s[6:7], exec, s[38:39]
	s_andn2_b64 vcc, exec, s[38:39]
	s_cbranch_vccnz .LBB0_411
	s_add_u32 s98, s40, s26
	s_addc_u32 s99, s41, s27
	s_add_u32 s8, s40, s58
	s_addc_u32 s9, s41, s59
	s_add_i32 s4, s36, 0x8000
	s_and_b32 s4, s4, 0x18000
	s_add_i32 s4, s96, s4
	s_waitcnt vmcnt(0) lgkmcnt(0)
	s_barrier
	s_mov_b32 m0, s4
	s_add_i32 s5, s4, 0x4000
	global_load_lds_dwordx4 v170, s[98:99]
	s_mov_b32 m0, s5
	s_nop 0
	global_load_lds_dwordx4 v162, s[8:9]
	s_add_i32 m0, s4, 0x2000
	s_nop 0
	global_load_lds_dwordx4 v172, s[98:99]
	s_add_i32 m0, s4, 0x6000
	s_nop 0
	global_load_lds_dwordx4 v168, s[8:9]
.LBB0_411:
	ds_read_b64_tr_b16 v[198:199], v196 offset:0x200
	ds_read_b64_tr_b16 v[200:201], v196 offset:0xa00
	ds_read_b64_tr_b16 v[202:203], v196 offset:0x1200
	ds_read_b64_tr_b16 v[204:205], v196 offset:0x1a00
	ds_read_b64_tr_b16 v[206:207], v196 offset:0x2200
	ds_read_b64_tr_b16 v[208:209], v196 offset:0x2a00
	ds_read_b64_tr_b16 v[210:211], v196 offset:0x3200
	ds_read_b64_tr_b16 v[212:213], v196 offset:0x3a00
	s_waitcnt lgkmcnt(8)
	v_mfma_f32_32x32x16_bf16 v[2:17], v[130:133], v[158:161], v[2:17]
	v_mfma_f32_32x32x16_bf16 v[2:17], v[134:137], v[154:157], v[2:17]
	ds_read_b64_tr_b16 v[154:155], v196 offset:0x400
	ds_read_b64_tr_b16 v[156:157], v196 offset:0xc00
	v_mfma_f32_32x32x16_bf16 v[2:17], v[138:141], v[150:153], v[2:17]
	ds_read_b64_tr_b16 v[150:151], v196 offset:0x1400
	ds_read_b64_tr_b16 v[152:153], v196 offset:0x1c00
	ds_read_b64_tr_b16 v[158:159], v196 offset:0x2400
	ds_read_b64_tr_b16 v[160:161], v196 offset:0x2c00
	ds_read_b64_tr_b16 v[214:215], v196 offset:0x3400
	ds_read_b64_tr_b16 v[216:217], v196 offset:0x3c00
	s_waitcnt lgkmcnt(8)
	v_mfma_f32_32x32x16_bf16 v[2:17], v[142:145], v[146:149], v[2:17]
	v_mfma_f32_32x32x16_bf16 v[50:65], v[130:133], v[198:201], v[50:65]
	ds_read_b64_tr_b16 v[146:147], v196 offset:0x600
	ds_read_b64_tr_b16 v[148:149], v196 offset:0xe00
	ds_read_b64_tr_b16 v[198:199], v196 offset:0x1600
	ds_read_b64_tr_b16 v[200:201], v196 offset:0x1e00
	v_mfma_f32_32x32x16_bf16 v[50:65], v[134:137], v[202:205], v[50:65]
	ds_read_b64_tr_b16 v[202:203], v196 offset:0x2600
	ds_read_b64_tr_b16 v[204:205], v196 offset:0x2e00
	v_mfma_f32_32x32x16_bf16 v[50:65], v[138:141], v[206:209], v[50:65]
	ds_read_b64_tr_b16 v[206:207], v196 offset:0x3600
	ds_read_b64_tr_b16 v[208:209], v196 offset:0x3e00
	s_waitcnt lgkmcnt(8)
	v_mfma_f32_32x32x16_bf16 v[50:65], v[142:145], v[210:213], v[50:65]
	v_mfma_f32_32x32x16_bf16 v[34:49], v[130:133], v[154:157], v[34:49]
	s_waitcnt lgkmcnt(0)
	v_mfma_f32_32x32x16_bf16 v[34:49], v[134:137], v[150:153], v[34:49]
	v_mfma_f32_32x32x16_bf16 v[34:49], v[138:141], v[158:161], v[34:49]
	v_mfma_f32_32x32x16_bf16 v[34:49], v[142:145], v[214:217], v[34:49]
	v_mfma_f32_32x32x16_bf16 v[18:33], v[130:133], v[146:149], v[18:33]
	v_mfma_f32_32x32x16_bf16 v[18:33], v[134:137], v[198:201], v[18:33]
	v_mfma_f32_32x32x16_bf16 v[18:33], v[138:141], v[202:205], v[18:33]
	v_mfma_f32_32x32x16_bf16 v[18:33], v[142:145], v[206:209], v[18:33]
	s_andn2_b64 s[4:5], exec, s[34:35]
	s_andn2_b64 vcc, exec, s[34:35]
	s_cbranch_vccnz .LBB0_413
; #define SBAR() __builtin_amdgcn_sched_barrier(0)
; __device__ __forceinline__ void finishSM(f32x16& p0, f32x16& p1, float alpha, float& l_reg, bf16x8& pa0, bf16x8& pa1, bf16x8& pa2, bf16x8& pa3) {
;   for (int r = 0; r < 16; ++r) p1[r] = __builtin_amdgcn_exp2f(p1[r]);
;   float ps = 0; for (int r = 0; r < 16; ++r) ps += p0[r]; for (int r = 0; r < 16; ++r) ps += p1[r];
;   { auto rr = __builtin_amdgcn_permlane32_swap(__float_as_uint(ps), __float_as_uint(ps), false, false);
;     ps = __uint_as_float(rr[0]) + __uint_as_float(rr[1]); }
;   l_reg = l_reg * alpha + ps;
;     ...
;   PK4(p0, 0, pa0); PK4(p0, 8, pa1); PK4(p1, 0, pa2); PK4(p1, 8, pa3);
;     ...
; }
; __device__ __forceinline__ void qkt(f32x16& p0, f32x16& p1, const bf16_t* Ks, const bf16x8* qr, int r32, int hi) {
;   p0 = f32x16{}; p1 = f32x16{};
;   for (int d0 = 0; d0 < 8; ++d0) { int cb = (d0 * 16 + hi * 8) * 2;
;     bf16x8 b0 = *reinterpret_cast<const bf16x8*>((const char*)Ks + KSWZ(r32, cb));
;     bf16x8 b1 = *reinterpret_cast<const bf16x8*>((const char*)Ks + KSWZ(32 + r32, cb));
;     p0 = __builtin_amdgcn_mfma_f32_32x32x16_bf16(b0, qr[d0], p0, 0, 0, 0);
;     p1 = __builtin_amdgcn_mfma_f32_32x32x16_bf16(b1, qr[d0], p1, 0, 0, 0); }
; }
; __device__ __forceinline__ int v_st(int k, int c) { const int kk = (k & ~0xC) | ((k & 4) << 1) | ((k & 8) >> 1); return ((kk >> 3) * 4 + (c >> 5)) * 512 + ((kk & 7) * 32 + (c & 31)) * 2; }
; __device__ __forceinline__ int v_rd_base(int lane) { return ((lane & 3) << 3) | (((lane >> 2) & 3) << 6) | (((lane >> 4) & 1) << 5) | (((lane >> 5) & 1) << 8); }
; template <int OFF> __device__ __forceinline__ s16x4 tr_read(int vb) {
;   s16x4 r; asm volatile("ds_read_b64_tr_b16 %0, %1 offset:%2" : "=&v"(r) : "v"(vb), "i"(OFF) : "memory"); return r;
; }
; __device__ __forceinline__ void attn_dma_body(const bf16_t* __restrict__ Qb, int ldq, int tpos0, const float* __restrict__ rope, const float* __restrict__ qgain, ...
;     ...
;       if (lead) ATT_SYNC(j + 2);
;       RESC(alB); }
;     { SBAR(); qkt(pA0, pA1, (const bf16_t*)(lds + ((j + 1) & 3) * SHM_SLOT), qr, r32, hi);
;       finishSM(pB0, pB1, alB, l_reg, pa0, pa1, pa2, pa3); s16x4 va[8]; pv_rd<0>(va, vb0 + (j & 3) * (int)SHM_SLOT); SBAR();
;       if (!lead) ATT_SYNC(j + 3);
;       pv_d0_pre(o, vb0 + (j & 3) * (int)SHM_SLOT, va, pa0, pa1, pa2, pa3); partialSM(pA0, pA1, m_reg, mnA, alA);
;       if (lead) ATT_SYNC(j + 3);
	s_add_u32 s98, s40, s26
	s_addc_u32 s99, s41, s27
	s_add_u32 s8, s40, s58
	s_addc_u32 s9, s41, s59
	s_add_i32 s42, s36, 0x8000
	s_and_b32 s42, s42, 0x18000
	s_add_i32 s42, s96, s42
	s_waitcnt vmcnt(0) lgkmcnt(0)
	s_barrier
	s_mov_b32 m0, s42
	s_add_i32 s43, s42, 0x4000
	global_load_lds_dwordx4 v170, s[98:99]
	s_mov_b32 m0, s43
	s_nop 0
	global_load_lds_dwordx4 v162, s[8:9]
	s_add_i32 m0, s42, 0x2000
	s_nop 0
	global_load_lds_dwordx4 v172, s[98:99]
	s_add_i32 m0, s42, 0x6000
	s_nop 0
	global_load_lds_dwordx4 v168, s[8:9]
.LBB0_413:
	v_mov_b32_e32 v196, 1.0
.LBB0_417:
	v_mov_b32_e32 v198, v66
	v_mov_b32_e32 v199, v67
	v_mov_b32_e32 v220, v68
	v_mov_b32_e32 v221, v69
	v_mov_b32_e32 v222, v70
	v_mov_b32_e32 v223, v71
	v_mov_b32_e32 v224, v72
	v_mov_b32_e32 v225, v73
	v_mov_b32_e32 v226, v74
	v_mov_b32_e32 v227, v75
	v_mov_b32_e32 v228, v76
	v_mov_b32_e32 v229, v77
	v_mov_b32_e32 v230, v78
	v_mov_b32_e32 v231, v79
	v_mov_b32_e32 v248, v80
	v_mov_b32_e32 v197, v81
	s_add_i32 s97, s97, 2
	v_exp_f32_e32 v232, v82
	v_exp_f32_e32 v233, v83
	v_exp_f32_e32 v234, v84
	v_exp_f32_e32 v235, v85
	v_exp_f32_e32 v236, v86
	v_exp_f32_e32 v237, v87
	v_exp_f32_e32 v238, v88
	v_exp_f32_e32 v239, v89
	v_exp_f32_e32 v240, v90
	v_exp_f32_e32 v241, v91
	v_exp_f32_e32 v242, v92
	v_exp_f32_e32 v243, v93
	v_exp_f32_e32 v244, v94
	v_exp_f32_e32 v245, v95
	v_exp_f32_e32 v246, v96
	v_exp_f32_e32 v247, v97
	s_and_b32 s8, s36, 0x18000
	s_add_i32 s8, s8, 0
	v_add_u32_e32 v70, s8, v183
	ds_read_b128 v[66:69], v70
	ds_read_b128 v[70:73], v70 offset:8192
	v_add_u32_e32 v142, s8, v186
	v_add_u32_e32 v150, s8, v185
	v_add_u32_e32 v158, s8, v187
	s_waitcnt lgkmcnt(0)
	v_mfma_f32_32x32x16_bf16 v[82:97], v[66:69], v[102:105], 0
	v_add_u32_e32 v66, s8, v184
	ds_read_b128 v[130:133], v66
	ds_read_b128 v[134:137], v66 offset:8192
	ds_read_b128 v[138:141], v142
	ds_read_b128 v[142:145], v142 offset:8192
	ds_read_b128 v[146:149], v150
	ds_read_b128 v[150:153], v150 offset:8192
	ds_read_b128 v[154:157], v158
	ds_read_b128 v[158:161], v158 offset:8192
	v_add_u32_e32 v200, s8, v188
	v_exp_f32_e32 v249, v198
	v_exp_f32_e32 v199, v199
	v_exp_f32_e32 v220, v220
	v_mfma_f32_32x32x16_bf16 v[66:81], v[70:73], v[102:105], 0
	v_exp_f32_e32 v221, v221
	v_exp_f32_e32 v222, v222
	v_exp_f32_e32 v223, v223
	v_add_u32_e32 v208, s8, v189
	v_add_u32_e32 v216, s8, v190
	s_waitcnt lgkmcnt(0)
	v_mfma_f32_32x32x16_bf16 v[82:97], v[130:133], v[110:113], v[82:97]
	ds_read_b128 v[130:133], v200
	ds_read_b128 v[200:203], v200 offset:8192
	ds_read_b128 v[204:207], v208
	ds_read_b128 v[208:211], v208 offset:8192
	ds_read_b128 v[212:215], v216
	ds_read_b128 v[216:219], v216 offset:8192
	v_mfma_f32_32x32x16_bf16 v[66:81], v[134:137], v[110:113], v[66:81]
	v_add_f32_e32 v134, v233, v232
	v_add_f32_e32 v134, v234, v134
	v_add_f32_e32 v134, v235, v134
	v_add_f32_e32 v134, v236, v134
	v_add_f32_e32 v134, v237, v134
	v_add_f32_e32 v134, v238, v134
	v_mfma_f32_32x32x16_bf16 v[82:97], v[138:141], v[98:101], v[82:97]
	v_add_f32_e32 v134, v239, v134
	v_add_f32_e32 v134, v240, v134
	v_add_f32_e32 v134, v241, v134
	v_add_f32_e32 v134, v242, v134
	v_add_f32_e32 v134, v243, v134
	v_add_f32_e32 v134, v244, v134
	v_add_f32_e32 v134, v245, v134
	v_mfma_f32_32x32x16_bf16 v[66:81], v[142:145], v[98:101], v[66:81]
	v_add_f32_e32 v134, v246, v134
	v_add_f32_e32 v134, v247, v134
	v_add_f32_e32 v134, v249, v134
	v_add_f32_e32 v134, v199, v134
	v_exp_f32_e32 v138, v224
	v_add_f32_e32 v134, v220, v134
	v_exp_f32_e32 v139, v225
	v_mfma_f32_32x32x16_bf16 v[82:97], v[146:149], v[106:109], v[82:97]
	v_add_f32_e32 v134, v221, v134
	v_exp_f32_e32 v140, v226
	v_add_f32_e32 v134, v222, v134
	v_exp_f32_e32 v141, v227
	v_add_f32_e32 v134, v223, v134
	v_exp_f32_e32 v224, v228
	v_add_f32_e32 v134, v138, v134
	v_mfma_f32_32x32x16_bf16 v[66:81], v[150:153], v[106:109], v[66:81]
	v_exp_f32_e32 v225, v229
	v_add_f32_e32 v134, v139, v134
	v_exp_f32_e32 v226, v230
	v_add_f32_e32 v134, v140, v134
	v_exp_f32_e32 v227, v231
	v_add_f32_e32 v134, v141, v134
	v_exp_f32_e32 v228, v248
	v_mfma_f32_32x32x16_bf16 v[82:97], v[154:157], v[118:121], v[82:97]
	v_add_f32_e32 v134, v224, v134
	v_exp_f32_e32 v229, v197
	v_add_f32_e32 v134, v225, v134
	v_add_f32_e32 v134, v226, v134
	v_add_f32_e32 v134, v227, v134
	v_add_f32_e32 v134, v228, v134
	v_add_f32_e32 v197, v229, v134
	v_mfma_f32_32x32x16_bf16 v[66:81], v[158:161], v[118:121], v[66:81]
	v_mov_b32_e32 v198, v197
	s_nop 1
	v_permlane32_swap_b32_e32 v197, v198
	s_waitcnt lgkmcnt(0)
	v_mfma_f32_32x32x16_bf16 v[82:97], v[130:133], v[126:129], v[82:97]
	v_cvt_pk_bf16_f32 v130, v232, v233
	v_cvt_pk_bf16_f32 v131, v234, v235
	v_cvt_pk_bf16_f32 v132, v236, v237
	v_cvt_pk_bf16_f32 v133, v238, v239
	v_cvt_pk_bf16_f32 v134, v240, v241
	v_cvt_pk_bf16_f32 v135, v242, v243
	v_cvt_pk_bf16_f32 v136, v244, v245
	v_mfma_f32_32x32x16_bf16 v[66:81], v[200:203], v[126:129], v[66:81]
	v_cvt_pk_bf16_f32 v137, v246, v247
	v_cvt_pk_bf16_f32 v142, v249, v199
	v_cvt_pk_bf16_f32 v143, v220, v221
	v_cvt_pk_bf16_f32 v144, v222, v223
	v_cvt_pk_bf16_f32 v145, v138, v139
	v_cvt_pk_bf16_f32 v138, v140, v141
	v_cvt_pk_bf16_f32 v139, v224, v225
	v_mfma_f32_32x32x16_bf16 v[82:97], v[204:207], v[114:117], v[82:97]
	v_cvt_pk_bf16_f32 v140, v226, v227
	v_cvt_pk_bf16_f32 v141, v228, v229
	v_add_u32_e32 v199, s69, v191
	ds_read_b64_tr_b16 v[158:159], v199 offset:0
	ds_read_b64_tr_b16 v[160:161], v199 offset:0x800
	ds_read_b64_tr_b16 v[154:155], v199 offset:0x1000
	ds_read_b64_tr_b16 v[156:157], v199 offset:0x1800
	v_mfma_f32_32x32x16_bf16 v[66:81], v[208:211], v[114:117], v[66:81]
	ds_read_b64_tr_b16 v[150:151], v199 offset:0x2000
	ds_read_b64_tr_b16 v[152:153], v199 offset:0x2800
	ds_read_b64_tr_b16 v[146:147], v199 offset:0x3000
	ds_read_b64_tr_b16 v[148:149], v199 offset:0x3800
	v_mfma_f32_32x32x16_bf16 v[82:97], v[212:215], v[122:125], v[82:97]
	v_mfma_f32_32x32x16_bf16 v[66:81], v[216:219], v[122:125], v[66:81]
	s_and_b64 vcc, exec, s[6:7]
	s_cbranch_vccnz .LBB0_420
	s_waitcnt vmcnt(0) lgkmcnt(0)
	s_barrier
	s_cmpk_gt_u32 s97, 0x80
	s_cbranch_scc1 .LBB0_420
	s_add_u32 s98, s40, s60
	s_addc_u32 s99, s41, s61
	s_add_u32 s8, s40, s62
	s_addc_u32 s9, s41, s63
	s_add_i32 s6, s96, s65
	s_mov_b32 m0, s6
	s_add_i32 s7, s6, 0x4000
	global_load_lds_dwordx4 v170, s[98:99]
	s_mov_b32 m0, s7
	s_nop 0
	global_load_lds_dwordx4 v162, s[8:9]
	s_add_i32 m0, s6, 0x2000
	s_nop 0
	global_load_lds_dwordx4 v172, s[98:99]
	s_add_i32 m0, s6, 0x6000
	s_nop 0
	global_load_lds_dwordx4 v168, s[8:9]
; #define SBAR() __builtin_amdgcn_sched_barrier(0)
; #define RESC(a) do { if (__any((a) < 1.f)) { if (hi == 0) al_l[r32] = (a); asm volatile("s_waitcnt lgkmcnt(0)" ::: "memory"); \
;     for (int d = 0; d < 4; ++d) for (int r = 0; r < 16; ++r) o[d][r] *= al_l[crow(r, hi)]; } } while (0)
; #define RESC(a) do { if (__any((a) < 1.f)) { if (hi == 0) al_l[r32] = (a); asm volatile("s_waitcnt lgkmcnt(0)" ::: "memory"); \
;     for (int d = 0; d < 4; ++d) for (int r = 0; r < 16; ++r) o[d][r] *= al_l[crow(r, hi)]; } } while (0)
; #define ATT_SYNC(jn) do { ATT_WAIT_BAR(); if ((jn) < NT) ATT_DMA((jn), (jn) & 3); } while (0)
; __device__ __forceinline__ void pv_d0(f32x16* o, int vb, bf16x8 pa0, bf16x8 pa1, bf16x8 pa2, bf16x8 pa3) {
;   s16x4 ra[8], rb[8];
;   pv_rd<0>(ra, vb); pv_rd<1>(rb, vb);
;   asm volatile("s_waitcnt lgkmcnt(8)" ::: "memory"); SBAR(); pv_mm(o[0], ra, pa0, pa1, pa2, pa3); pv_rd<2>(ra, vb);
;   asm volatile("s_waitcnt lgkmcnt(8)" ::: "memory"); SBAR(); pv_mm(o[1], rb, pa0, pa1, pa2, pa3); pv_rd<3>(rb, vb);
;   asm volatile("s_waitcnt lgkmcnt(8)" ::: "memory"); SBAR(); pv_mm(o[2], ra, pa0, pa1, pa2, pa3);
;   asm volatile("s_waitcnt lgkmcnt(0)" ::: "memory"); SBAR(); pv_mm(o[3], rb, pa0, pa1, pa2, pa3);
; }
; __device__ __forceinline__ void pv_d0_pre(f32x16* o, int vb, s16x4 (&ra)[8], bf16x8 pa0, bf16x8 pa1, bf16x8 pa2, bf16x8 pa3) {
;   s16x4 rb[8];
;   pv_rd<1>(rb, vb);
;   asm volatile("s_waitcnt lgkmcnt(8)" ::: "memory"); SBAR(); pv_mm(o[0], ra, pa0, pa1, pa2, pa3); pv_rd<2>(ra, vb);
;   asm volatile("s_waitcnt lgkmcnt(8)" ::: "memory"); SBAR(); pv_mm(o[1], rb, pa0, pa1, pa2, pa3); pv_rd<3>(rb, vb);
;   asm volatile("s_waitcnt lgkmcnt(8)" ::: "memory"); SBAR(); pv_mm(o[2], ra, pa0, pa1, pa2, pa3);
;   asm volatile("s_waitcnt lgkmcnt(0)" ::: "memory"); SBAR(); pv_mm(o[3], rb, pa0, pa1, pa2, pa3);
; }
; __device__ __forceinline__ void attn_dma_body(const bf16_t* __restrict__ Qb, int ldq, int tpos0, const float* __restrict__ rope, const float* __restrict__ qgain, ...
;     ...
;       if (!lead) ATT_SYNC(j + 3);
;       pv_d0_pre(o, vb0 + (j & 3) * (int)SHM_SLOT, va, pa0, pa1, pa2, pa3); partialSM(pA0, pA1, m_reg, mnA, alA);
;       if (lead) ATT_SYNC(j + 3);
;       RESC(alA); }
;   }
.LBB0_420:
	ds_read_b64_tr_b16 v[200:201], v199 offset:0x200
	ds_read_b64_tr_b16 v[202:203], v199 offset:0xa00
	ds_read_b64_tr_b16 v[204:205], v199 offset:0x1200
	ds_read_b64_tr_b16 v[206:207], v199 offset:0x1a00
	ds_read_b64_tr_b16 v[208:209], v199 offset:0x2200
	ds_read_b64_tr_b16 v[210:211], v199 offset:0x2a00
	ds_read_b64_tr_b16 v[212:213], v199 offset:0x3200
	ds_read_b64_tr_b16 v[214:215], v199 offset:0x3a00
	s_waitcnt lgkmcnt(8)
	v_mfma_f32_32x32x16_bf16 v[2:17], v[130:133], v[158:161], v[2:17]
	v_mfma_f32_32x32x16_bf16 v[2:17], v[134:137], v[154:157], v[2:17]
	ds_read_b64_tr_b16 v[154:155], v199 offset:0x400
	ds_read_b64_tr_b16 v[156:157], v199 offset:0xc00
	v_mfma_f32_32x32x16_bf16 v[2:17], v[142:145], v[150:153], v[2:17]
	ds_read_b64_tr_b16 v[150:151], v199 offset:0x1400
	ds_read_b64_tr_b16 v[152:153], v199 offset:0x1c00
	ds_read_b64_tr_b16 v[158:159], v199 offset:0x2400
	ds_read_b64_tr_b16 v[160:161], v199 offset:0x2c00
	ds_read_b64_tr_b16 v[216:217], v199 offset:0x3400
	ds_read_b64_tr_b16 v[218:219], v199 offset:0x3c00
	s_waitcnt lgkmcnt(8)
	v_mfma_f32_32x32x16_bf16 v[2:17], v[138:141], v[146:149], v[2:17]
	v_mfma_f32_32x32x16_bf16 v[50:65], v[130:133], v[200:203], v[50:65]
	ds_read_b64_tr_b16 v[146:147], v199 offset:0x600
	ds_read_b64_tr_b16 v[148:149], v199 offset:0xe00
	ds_read_b64_tr_b16 v[200:201], v199 offset:0x1600
	ds_read_b64_tr_b16 v[202:203], v199 offset:0x1e00
	v_mfma_f32_32x32x16_bf16 v[50:65], v[134:137], v[204:207], v[50:65]
	ds_read_b64_tr_b16 v[204:205], v199 offset:0x2600
	ds_read_b64_tr_b16 v[206:207], v199 offset:0x2e00
	v_mfma_f32_32x32x16_bf16 v[50:65], v[142:145], v[208:211], v[50:65]
	ds_read_b64_tr_b16 v[208:209], v199 offset:0x3600
	ds_read_b64_tr_b16 v[210:211], v199 offset:0x3e00
	s_waitcnt lgkmcnt(8)
	v_mfma_f32_32x32x16_bf16 v[50:65], v[138:141], v[212:215], v[50:65]
	v_mfma_f32_32x32x16_bf16 v[34:49], v[130:133], v[154:157], v[34:49]
	s_waitcnt lgkmcnt(0)
	v_mfma_f32_32x32x16_bf16 v[34:49], v[134:137], v[150:153], v[34:49]
	v_mfma_f32_32x32x16_bf16 v[34:49], v[142:145], v[158:161], v[34:49]
	v_mfma_f32_32x32x16_bf16 v[34:49], v[138:141], v[216:219], v[34:49]
	v_mfma_f32_32x32x16_bf16 v[18:33], v[130:133], v[146:149], v[18:33]
	v_mfma_f32_32x32x16_bf16 v[18:33], v[134:137], v[200:203], v[18:33]
	v_mfma_f32_32x32x16_bf16 v[18:33], v[142:145], v[204:207], v[18:33]
	v_mfma_f32_32x32x16_bf16 v[18:33], v[138:141], v[208:211], v[18:33]
	s_and_b64 vcc, exec, s[4:5]
	s_cbranch_vccnz .LBB0_423
	s_waitcnt vmcnt(0) lgkmcnt(0)
	s_barrier
	s_cmpk_gt_u32 s97, 0x80
	s_cbranch_scc1 .LBB0_423
	s_add_u32 s98, s40, s60
	s_addc_u32 s99, s41, s61
	s_add_u32 s8, s40, s62
	s_addc_u32 s9, s41, s63
	s_add_i32 s4, s96, s65
	s_mov_b32 m0, s4
	s_add_i32 s5, s4, 0x4000
	global_load_lds_dwordx4 v170, s[98:99]
	s_mov_b32 m0, s5
	s_nop 0
	global_load_lds_dwordx4 v162, s[8:9]
	s_add_i32 m0, s4, 0x2000
	s_nop 0
	global_load_lds_dwordx4 v172, s[98:99]
	s_add_i32 m0, s4, 0x6000
	s_nop 0
	global_load_lds_dwordx4 v168, s[8:9]
.LBB0_423:
	v_mov_b32_e32 v146, 1.0
.LBB0_427:
	v_exp_f32_e32 v203, v82
	v_exp_f32_e32 v207, v83
	v_exp_f32_e32 v204, v84
	v_exp_f32_e32 v208, v85
	v_exp_f32_e32 v205, v86
	v_exp_f32_e32 v209, v87
	v_exp_f32_e32 v202, v88
	v_exp_f32_e32 v206, v89
	v_exp_f32_e32 v159, v90
	v_exp_f32_e32 v199, v91
	v_exp_f32_e32 v160, v92
	v_exp_f32_e32 v200, v93
	v_exp_f32_e32 v157, v94
	v_exp_f32_e32 v161, v95
	v_exp_f32_e32 v158, v96
	v_exp_f32_e32 v201, v97
	v_mov_b64_e32 v[144:145], v[66:67]
	v_add_f32_e32 v66, v194, v195
	s_add_u32 s40, s40, 0x8000
	v_fmac_f32_e32 v66, v192, v182
	v_add_f32_e32 v182, v197, v198
	s_addc_u32 s41, s41, 0
	v_mov_b64_e32 v[142:143], v[68:69]
	v_mov_b64_e32 v[140:141], v[70:71]
	v_mov_b64_e32 v[138:139], v[72:73]
	v_mov_b64_e32 v[136:137], v[74:75]
	v_mov_b64_e32 v[134:135], v[76:77]
	v_mov_b64_e32 v[132:133], v[78:79]
	v_mov_b64_e32 v[130:131], v[80:81]
	s_cmpk_gt_u32 s97, 0x80
	v_fmac_f32_e32 v182, v66, v196
	s_cbranch_scc1 .LBB0_429
	s_mov_b32 s36, s37
	v_mov_b32_e32 v192, v146
	s_branch .LBB0_409
; #define SBAR() __builtin_amdgcn_sched_barrier(0)
; __device__ __forceinline__ void finishSM(f32x16& p0, f32x16& p1, float alpha, float& l_reg, bf16x8& pa0, bf16x8& pa1, bf16x8& pa2, bf16x8& pa3) {
;   for (int r = 0; r < 16; ++r) p1[r] = __builtin_amdgcn_exp2f(p1[r]);
;   float ps = 0; for (int r = 0; r < 16; ++r) ps += p0[r]; for (int r = 0; r < 16; ++r) ps += p1[r];
;   { auto rr = __builtin_amdgcn_permlane32_swap(__float_as_uint(ps), __float_as_uint(ps), false, false);
;     ps = __uint_as_float(rr[0]) + __uint_as_float(rr[1]); }
;   l_reg = l_reg * alpha + ps;
;     ...
;   PK4(p0, 0, pa0); PK4(p0, 8, pa1); PK4(p1, 0, pa2); PK4(p1, 8, pa3);
;     ...
; }
; __device__ __forceinline__ void qkt(f32x16& p0, f32x16& p1, const bf16_t* Ks, const bf16x8* qr, int r32, int hi) {
;   p0 = f32x16{}; p1 = f32x16{};
;   for (int d0 = 0; d0 < 8; ++d0) { int cb = (d0 * 16 + hi * 8) * 2;
;     bf16x8 b0 = *reinterpret_cast<const bf16x8*>((const char*)Ks + KSWZ(r32, cb));
;     bf16x8 b1 = *reinterpret_cast<const bf16x8*>((const char*)Ks + KSWZ(32 + r32, cb));
;     p0 = __builtin_amdgcn_mfma_f32_32x32x16_bf16(b0, qr[d0], p0, 0, 0, 0);
;     p1 = __builtin_amdgcn_mfma_f32_32x32x16_bf16(b1, qr[d0], p1, 0, 0, 0); }
; }
; __device__ __forceinline__ int v_st(int k, int c) { const int kk = (k & ~0xC) | ((k & 4) << 1) | ((k & 8) >> 1); return ((kk >> 3) * 4 + (c >> 5)) * 512 + ((kk & 7) * 32 + (c & 31)) * 2; }
; __device__ __forceinline__ int v_rd_base(int lane) { return ((lane & 3) << 3) | (((lane >> 2) & 3) << 6) | (((lane >> 4) & 1) << 5) | (((lane >> 5) & 1) << 8); }
; template <int OFF> __device__ __forceinline__ s16x4 tr_read(int vb) {
;   s16x4 r; asm volatile("ds_read_b64_tr_b16 %0, %1 offset:%2" : "=&v"(r) : "v"(vb), "i"(OFF) : "memory"); return r;
; }
; __device__ __forceinline__ void attn_dma_body(const bf16_t* __restrict__ Qb, int ldq, int tpos0, const float* __restrict__ rope, const float* __restrict__ qgain, ...
;     ...
;   { SBAR(); qkt(pB0, pB1, (const bf16_t*)(lds + ((NT - 1) & 3) * SHM_SLOT), qr, r32, hi);
;     finishSM(pA0, pA1, alA, l_reg, pa0, pa1, pa2, pa3); SBAR();
;     pv_d0(o, vb0 + ((NT - 2) & 3) * (int)SHM_SLOT, pa0, pa1, pa2, pa3); partialSM(pB0, pB1, m_reg, mnB, alB);
;     RESC(alB);
;     finishSM(pB0, pB1, alB, l_reg, pa0, pa1, pa2, pa3); SBAR();
;     pv_d0(o, vb0 + ((NT - 1) & 3) * (int)SHM_SLOT, pa0, pa1, pa2, pa3); }
.LBB0_429:
	s_add_i32 s4, 0, 0x18000
	v_add_u32_e32 v70, s4, v183
	ds_read_b128 v[66:69], v70
	ds_read_b128 v[70:73], v70 offset:8192
	v_add_u32_e32 v147, s4, v186
	v_add_u32_e32 v156, s4, v187
	v_exp_f32_e32 v144, v144
	s_waitcnt lgkmcnt(0)
	v_mfma_f32_32x32x16_bf16 v[82:97], v[66:69], v[102:105], 0
	v_add_u32_e32 v66, s4, v184
	ds_read_b128 v[148:151], v66
	ds_read_b128 v[152:155], v66 offset:8192
	v_exp_f32_e32 v145, v145
	v_exp_f32_e32 v142, v142
	v_exp_f32_e32 v143, v143
	v_exp_f32_e32 v140, v140
	v_exp_f32_e32 v141, v141
	v_mfma_f32_32x32x16_bf16 v[66:81], v[70:73], v[102:105], 0
	ds_read_b128 v[102:105], v147
	ds_read_b128 v[168:171], v147 offset:8192
	v_add_u32_e32 v147, s4, v185
	ds_read_b128 v[184:187], v147
	ds_read_b128 v[194:197], v147 offset:8192
	ds_read_b128 v[210:213], v156
	ds_read_b128 v[214:217], v156 offset:8192
	v_add_u32_e32 v147, s4, v188
	v_exp_f32_e32 v138, v138
	v_exp_f32_e32 v139, v139
	v_exp_f32_e32 v136, v136
	s_waitcnt lgkmcnt(0)
	v_mfma_f32_32x32x16_bf16 v[82:97], v[148:151], v[110:113], v[82:97]
	ds_read_b128 v[148:151], v147
	ds_read_b128 v[218:221], v147 offset:8192
	v_add_u32_e32 v147, s4, v189
	ds_read_b128 v[222:225], v147
	ds_read_b128 v[226:229], v147 offset:8192
	v_add_u32_e32 v147, s4, v190
	v_exp_f32_e32 v137, v137
	v_exp_f32_e32 v134, v134
	v_exp_f32_e32 v135, v135
	v_mfma_f32_32x32x16_bf16 v[66:81], v[152:155], v[110:113], v[66:81]
	ds_read_b128 v[110:113], v147
	ds_read_b128 v[152:155], v147 offset:8192
	v_exp_f32_e32 v132, v132
	v_exp_f32_e32 v133, v133
	v_exp_f32_e32 v130, v130
	v_exp_f32_e32 v131, v131
	v_mfma_f32_32x32x16_bf16 v[82:97], v[102:105], v[98:101], v[82:97]
	v_mfma_f32_32x32x16_bf16 v[66:81], v[168:171], v[98:101], v[66:81]
	v_add_f32_e32 v98, 0, v203
	v_add_f32_e32 v98, v207, v98
	v_add_f32_e32 v98, v204, v98
	v_add_f32_e32 v98, v208, v98
	v_add_f32_e32 v98, v205, v98
	v_add_f32_e32 v98, v209, v98
	v_add_f32_e32 v98, v202, v98
	v_mfma_f32_32x32x16_bf16 v[82:97], v[184:187], v[106:109], v[82:97]
	v_add_f32_e32 v98, v206, v98
	v_add_f32_e32 v98, v159, v98
	v_add_f32_e32 v98, v199, v98
	v_add_f32_e32 v98, v160, v98
	v_add_f32_e32 v98, v200, v98
	v_add_f32_e32 v98, v157, v98
	v_add_f32_e32 v98, v161, v98
	v_mfma_f32_32x32x16_bf16 v[66:81], v[194:197], v[106:109], v[66:81]
	v_add_f32_e32 v98, v158, v98
	v_add_f32_e32 v98, v201, v98
	v_add_f32_e32 v98, v144, v98
	v_add_f32_e32 v98, v145, v98
	v_add_f32_e32 v98, v142, v98
	v_add_f32_e32 v98, v143, v98
	v_add_f32_e32 v98, v140, v98
	v_mfma_f32_32x32x16_bf16 v[82:97], v[210:213], v[118:121], v[82:97]
	v_add_f32_e32 v98, v141, v98
	v_add_f32_e32 v98, v138, v98
	v_add_f32_e32 v98, v139, v98
	v_add_f32_e32 v98, v136, v98
	v_add_f32_e32 v98, v137, v98
	v_add_f32_e32 v98, v134, v98
	v_add_f32_e32 v98, v135, v98
	v_mfma_f32_32x32x16_bf16 v[66:81], v[214:217], v[118:121], v[66:81]
	v_add_f32_e32 v98, v132, v98
	v_add_f32_e32 v98, v133, v98
	v_add_f32_e32 v98, v130, v98
	v_add_f32_e32 v98, v131, v98
	v_mov_b32_e32 v99, v98
	v_cvt_pk_bf16_f32 v100, v203, v207
	v_cvt_pk_bf16_f32 v101, v204, v208
	s_waitcnt lgkmcnt(0)
	v_mfma_f32_32x32x16_bf16 v[82:97], v[148:151], v[126:129], v[82:97]
	v_cvt_pk_bf16_f32 v102, v205, v209
	v_cvt_pk_bf16_f32 v103, v202, v206
	v_permlane32_swap_b32_e32 v98, v99
	v_mfma_f32_32x32x16_bf16 v[66:81], v[218:221], v[126:129], v[66:81]
	v_cvt_pk_bf16_f32 v104, v159, v199
	v_cvt_pk_bf16_f32 v105, v160, v200
	v_cvt_pk_bf16_f32 v106, v157, v161
	v_cvt_pk_bf16_f32 v107, v158, v201
	v_cvt_pk_bf16_f32 v118, v144, v145
	v_cvt_pk_bf16_f32 v119, v142, v143
	v_cvt_pk_bf16_f32 v120, v140, v141
	v_mfma_f32_32x32x16_bf16 v[82:97], v[222:225], v[114:117], v[82:97]
	v_cvt_pk_bf16_f32 v121, v138, v139
	v_cvt_pk_bf16_f32 v108, v136, v137
	v_cvt_pk_bf16_f32 v109, v134, v135
	v_mfma_f32_32x32x16_bf16 v[66:81], v[226:229], v[114:117], v[66:81]
	v_mfma_f32_32x32x16_bf16 v[82:97], v[110:113], v[122:125], v[82:97]
	v_cvt_pk_bf16_f32 v110, v132, v133
	v_cvt_pk_bf16_f32 v111, v130, v131
	s_nop 0
	v_mfma_f32_32x32x16_bf16 v[66:81], v[152:155], v[122:125], v[66:81]
	s_cmp_lg_u32 0, -1
	s_cselect_b32 s4, 0, 0
	s_add_i32 s4, s4, 0x14000
	v_add_u32_e32 v116, s4, v181
	ds_read_b64_tr_b16 v[112:113], v116 offset:0
	ds_read_b64_tr_b16 v[114:115], v116 offset:0x800
	ds_read_b64_tr_b16 v[122:123], v116 offset:0x1000
	ds_read_b64_tr_b16 v[124:125], v116 offset:0x1800
	ds_read_b64_tr_b16 v[126:127], v116 offset:0x2000
	ds_read_b64_tr_b16 v[128:129], v116 offset:0x2800
	ds_read_b64_tr_b16 v[130:131], v116 offset:0x3000
	ds_read_b64_tr_b16 v[132:133], v116 offset:0x3800
	ds_read_b64_tr_b16 v[134:135], v116 offset:0x200
	ds_read_b64_tr_b16 v[136:137], v116 offset:0xa00
	ds_read_b64_tr_b16 v[138:139], v116 offset:0x1200
	ds_read_b64_tr_b16 v[140:141], v116 offset:0x1a00
	ds_read_b64_tr_b16 v[142:143], v116 offset:0x2200
	ds_read_b64_tr_b16 v[144:145], v116 offset:0x2a00
	ds_read_b64_tr_b16 v[148:149], v116 offset:0x3200
	ds_read_b64_tr_b16 v[150:151], v116 offset:0x3a00
	s_waitcnt lgkmcnt(8)
	s_nop 0
	v_mfma_f32_32x32x16_bf16 v[2:17], v[100:103], v[112:115], v[2:17]
	ds_read_b64_tr_b16 v[112:113], v116 offset:0x400
	ds_read_b64_tr_b16 v[114:115], v116 offset:0xc00
	v_mfma_f32_32x32x16_bf16 v[2:17], v[104:107], v[122:125], v[2:17]
	ds_read_b64_tr_b16 v[122:123], v116 offset:0x1400
	ds_read_b64_tr_b16 v[124:125], v116 offset:0x1c00
	v_mfma_f32_32x32x16_bf16 v[2:17], v[118:121], v[126:129], v[2:17]
	ds_read_b64_tr_b16 v[126:127], v116 offset:0x2400
	ds_read_b64_tr_b16 v[128:129], v116 offset:0x2c00
	ds_read_b64_tr_b16 v[152:153], v116 offset:0x3400
	ds_read_b64_tr_b16 v[154:155], v116 offset:0x3c00
	s_waitcnt lgkmcnt(8)
	v_mfma_f32_32x32x16_bf16 v[2:17], v[108:111], v[130:133], v[2:17]
	v_mfma_f32_32x32x16_bf16 v[50:65], v[100:103], v[134:137], v[50:65]
	ds_read_b64_tr_b16 v[130:131], v116 offset:0x600
	ds_read_b64_tr_b16 v[132:133], v116 offset:0xe00
	ds_read_b64_tr_b16 v[134:135], v116 offset:0x1600
	ds_read_b64_tr_b16 v[136:137], v116 offset:0x1e00
	v_mfma_f32_32x32x16_bf16 v[50:65], v[104:107], v[138:141], v[50:65]
	ds_read_b64_tr_b16 v[138:139], v116 offset:0x2600
	ds_read_b64_tr_b16 v[140:141], v116 offset:0x2e00
	v_mfma_f32_32x32x16_bf16 v[50:65], v[118:121], v[142:145], v[50:65]
	ds_read_b64_tr_b16 v[142:143], v116 offset:0x3600
	ds_read_b64_tr_b16 v[144:145], v116 offset:0x3e00
	s_waitcnt lgkmcnt(8)
	v_mfma_f32_32x32x16_bf16 v[50:65], v[108:111], v[148:151], v[50:65]
	v_mfma_f32_32x32x16_bf16 v[34:49], v[100:103], v[112:115], v[34:49]
	s_waitcnt lgkmcnt(0)
	v_mfma_f32_32x32x16_bf16 v[34:49], v[104:107], v[122:125], v[34:49]
	v_mfma_f32_32x32x16_bf16 v[34:49], v[118:121], v[126:129], v[34:49]
	v_mfma_f32_32x32x16_bf16 v[34:49], v[108:111], v[152:155], v[34:49]
	v_mfma_f32_32x32x16_bf16 v[18:33], v[100:103], v[130:133], v[18:33]
	v_mfma_f32_32x32x16_bf16 v[18:33], v[104:107], v[134:137], v[18:33]
	v_mfma_f32_32x32x16_bf16 v[18:33], v[118:121], v[138:141], v[18:33]
	v_mfma_f32_32x32x16_bf16 v[18:33], v[108:111], v[142:145], v[18:33]
	v_mov_b32_e32 v100, 1.0

; #define SBAR() __builtin_amdgcn_sched_barrier(0)
; __device__ __forceinline__ int crow(int r, int hi) { return (r & 3) + 8 * (r >> 2) + 4 * hi; }
; __device__ __forceinline__ void finishSM(f32x16& p0, f32x16& p1, float alpha, float& l_reg, bf16x8& pa0, bf16x8& pa1, bf16x8& pa2, bf16x8& pa3) {
;   for (int r = 0; r < 16; ++r) p1[r] = __builtin_amdgcn_exp2f(p1[r]);
;   float ps = 0; for (int r = 0; r < 16; ++r) ps += p0[r]; for (int r = 0; r < 16; ++r) ps += p1[r];
;   { auto rr = __builtin_amdgcn_permlane32_swap(__float_as_uint(ps), __float_as_uint(ps), false, false);
;     ps = __uint_as_float(rr[0]) + __uint_as_float(rr[1]); }
;   l_reg = l_reg * alpha + ps;
;     ...
;   PK4(p0, 0, pa0); PK4(p0, 8, pa1); PK4(p1, 0, pa2); PK4(p1, 8, pa3);
;     ...
; }
; __device__ __forceinline__ void attn_dma_body(const bf16_t* __restrict__ Qb, int ldq, int tpos0, const float* __restrict__ rope, const float* __restrict__ qgain, ...
;     ...
;     finishSM(pB0, pB1, alB, l_reg, pa0, pa1, pa2, pa3); SBAR();
;     pv_d0(o, vb0 + ((NT - 1) & 3) * (int)SHM_SLOT, pa0, pa1, pa2, pa3); }
;   if (hi == 0) li_l[r32] = l_reg; asm volatile("s_waitcnt lgkmcnt(0)" ::: "memory");
;   float rli[16];
; #pragma unroll
;   for (int r = 0; r < 16; ++r) rli[r] = __builtin_amdgcn_rcpf(li_l[crow(r, hi)]);
;   bf16_t* Ow = Ob + (long)(wid * QBLK) * LDO;
;   asm volatile("s_waitcnt lgkmcnt(0)\n\ts_barrier" ::: "memory");
.LBB0_434:
	v_mov_b32_e32 v101, v81
	v_exp_f32_e32 v81, v82
	v_exp_f32_e32 v82, v83
	v_exp_f32_e32 v83, v84
	v_exp_f32_e32 v84, v85
	v_exp_f32_e32 v85, v86
	v_exp_f32_e32 v86, v87
	v_exp_f32_e32 v87, v88
	v_exp_f32_e32 v88, v89
	v_exp_f32_e32 v89, v90
	v_exp_f32_e32 v90, v91
	v_exp_f32_e32 v91, v92
	v_exp_f32_e32 v92, v93
	v_exp_f32_e32 v93, v94
	v_exp_f32_e32 v94, v95
	v_exp_f32_e32 v95, v96
	v_exp_f32_e32 v96, v97
	v_exp_f32_e32 v97, v66
	v_add_f32_e32 v66, 0, v81
	v_add_f32_e32 v66, v82, v66
	v_add_f32_e32 v66, v83, v66
	v_add_f32_e32 v66, v84, v66
	v_add_f32_e32 v66, v85, v66
	v_add_f32_e32 v66, v86, v66
	v_add_f32_e32 v66, v87, v66
	v_add_f32_e32 v66, v88, v66
	v_add_f32_e32 v66, v89, v66
	v_add_f32_e32 v66, v90, v66
	v_add_f32_e32 v66, v91, v66
	v_add_f32_e32 v66, v92, v66
	v_add_f32_e32 v66, v93, v66
	v_exp_f32_e32 v102, v67
	v_add_f32_e32 v66, v94, v66
	v_exp_f32_e32 v103, v68
	v_add_f32_e32 v66, v95, v66
	v_exp_f32_e32 v104, v69
	v_add_f32_e32 v66, v96, v66
	v_exp_f32_e32 v105, v70
	v_add_f32_e32 v66, v97, v66
	v_exp_f32_e32 v106, v71
	v_add_f32_e32 v66, v102, v66
	v_exp_f32_e32 v107, v72
	v_add_f32_e32 v66, v103, v66
	v_exp_f32_e32 v108, v73
	v_add_f32_e32 v66, v104, v66
	v_exp_f32_e32 v109, v74
	v_add_f32_e32 v66, v105, v66
	v_exp_f32_e32 v110, v75
	v_add_f32_e32 v66, v106, v66
	v_exp_f32_e32 v111, v76
	v_add_f32_e32 v66, v107, v66
	v_exp_f32_e32 v112, v77
	v_add_f32_e32 v66, v108, v66
	v_exp_f32_e32 v113, v78
	v_add_f32_e32 v66, v109, v66
	v_exp_f32_e32 v114, v79
	v_add_f32_e32 v66, v110, v66
	v_exp_f32_e32 v115, v80
	v_add_f32_e32 v66, v111, v66
	v_exp_f32_e32 v101, v101
	v_add_f32_e32 v66, v112, v66
	v_add_f32_e32 v66, v113, v66
	v_add_f32_e32 v66, v114, v66
	v_add_f32_e32 v66, v115, v66
	v_add_f32_e32 v66, v101, v66
	v_mov_b32_e32 v67, v66
	s_nop 1
	v_permlane32_swap_b32_e32 v66, v67
	v_cvt_pk_bf16_f32 v68, v81, v82
	v_cvt_pk_bf16_f32 v69, v83, v84
	v_cvt_pk_bf16_f32 v70, v85, v86
	v_cvt_pk_bf16_f32 v71, v87, v88
	v_cvt_pk_bf16_f32 v72, v89, v90
	v_cvt_pk_bf16_f32 v73, v91, v92
	v_cvt_pk_bf16_f32 v74, v93, v94
	v_cvt_pk_bf16_f32 v75, v95, v96
	v_cvt_pk_bf16_f32 v76, v97, v102
	v_cvt_pk_bf16_f32 v77, v103, v104
	v_cvt_pk_bf16_f32 v78, v105, v106
	v_cvt_pk_bf16_f32 v79, v107, v108
	v_cvt_pk_bf16_f32 v80, v109, v110
	v_cvt_pk_bf16_f32 v81, v111, v112
	v_cvt_pk_bf16_f32 v82, v113, v114
	v_cvt_pk_bf16_f32 v83, v115, v101
	s_nop 0
	s_cmp_lg_u32 0, -1
	s_cselect_b32 s4, 0, 0
	s_add_i32 s4, s4, 0x1c000
	v_add_u32_e32 v96, s4, v181
	ds_read_b64_tr_b16 v[84:85], v96 offset:0
	ds_read_b64_tr_b16 v[86:87], v96 offset:0x800
	ds_read_b64_tr_b16 v[88:89], v96 offset:0x1000
	ds_read_b64_tr_b16 v[90:91], v96 offset:0x1800
	ds_read_b64_tr_b16 v[92:93], v96 offset:0x2000
	ds_read_b64_tr_b16 v[94:95], v96 offset:0x2800
	ds_read_b64_tr_b16 v[102:103], v96 offset:0x3000
	ds_read_b64_tr_b16 v[104:105], v96 offset:0x3800
	ds_read_b64_tr_b16 v[106:107], v96 offset:0x200
	ds_read_b64_tr_b16 v[108:109], v96 offset:0xa00
	ds_read_b64_tr_b16 v[110:111], v96 offset:0x1200
	ds_read_b64_tr_b16 v[112:113], v96 offset:0x1a00
	ds_read_b64_tr_b16 v[114:115], v96 offset:0x2200
	ds_read_b64_tr_b16 v[116:117], v96 offset:0x2a00
	ds_read_b64_tr_b16 v[118:119], v96 offset:0x3200
	ds_read_b64_tr_b16 v[120:121], v96 offset:0x3a00
	s_waitcnt lgkmcnt(8)
	s_nop 0
	v_mfma_f32_32x32x16_bf16 v[2:17], v[68:71], v[84:87], v[2:17]
	ds_read_b64_tr_b16 v[84:85], v96 offset:0x400
	ds_read_b64_tr_b16 v[86:87], v96 offset:0xc00
	v_mfma_f32_32x32x16_bf16 v[2:17], v[72:75], v[88:91], v[2:17]
	ds_read_b64_tr_b16 v[88:89], v96 offset:0x1400
	ds_read_b64_tr_b16 v[90:91], v96 offset:0x1c00
	v_mfma_f32_32x32x16_bf16 v[2:17], v[76:79], v[92:95], v[2:17]
	ds_read_b64_tr_b16 v[92:93], v96 offset:0x2400
	ds_read_b64_tr_b16 v[94:95], v96 offset:0x2c00
	ds_read_b64_tr_b16 v[122:123], v96 offset:0x3400
	ds_read_b64_tr_b16 v[124:125], v96 offset:0x3c00
	s_waitcnt lgkmcnt(8)
	v_mfma_f32_32x32x16_bf16 v[2:17], v[80:83], v[102:105], v[2:17]
	v_mfma_f32_32x32x16_bf16 v[50:65], v[68:71], v[106:109], v[50:65]
	ds_read_b64_tr_b16 v[102:103], v96 offset:0x600
	ds_read_b64_tr_b16 v[104:105], v96 offset:0xe00
	ds_read_b64_tr_b16 v[106:107], v96 offset:0x1600
	ds_read_b64_tr_b16 v[108:109], v96 offset:0x1e00
	v_mfma_f32_32x32x16_bf16 v[50:65], v[72:75], v[110:113], v[50:65]
	ds_read_b64_tr_b16 v[110:111], v96 offset:0x2600
	ds_read_b64_tr_b16 v[112:113], v96 offset:0x2e00
	v_mfma_f32_32x32x16_bf16 v[50:65], v[76:79], v[114:117], v[50:65]
	ds_read_b64_tr_b16 v[114:115], v96 offset:0x3600
	ds_read_b64_tr_b16 v[116:117], v96 offset:0x3e00
	s_waitcnt lgkmcnt(8)
	v_mfma_f32_32x32x16_bf16 v[50:65], v[80:83], v[118:121], v[50:65]
	v_mfma_f32_32x32x16_bf16 v[34:49], v[68:71], v[84:87], v[34:49]
	s_waitcnt lgkmcnt(0)
	v_mfma_f32_32x32x16_bf16 v[34:49], v[72:75], v[88:91], v[34:49]
	v_mfma_f32_32x32x16_bf16 v[34:49], v[76:79], v[92:95], v[34:49]
	v_mfma_f32_32x32x16_bf16 v[34:49], v[80:83], v[122:125], v[34:49]
	v_mfma_f32_32x32x16_bf16 v[18:33], v[68:71], v[102:105], v[18:33]
	v_mfma_f32_32x32x16_bf16 v[18:33], v[72:75], v[106:109], v[18:33]
	v_mfma_f32_32x32x16_bf16 v[18:33], v[76:79], v[110:113], v[18:33]
	v_mfma_f32_32x32x16_bf16 v[18:33], v[80:83], v[114:117], v[18:33]
	s_setprio 0
	s_and_saveexec_b64 s[4:5], s[2:3]
	v_add_f32_e32 v68, v98, v99
	v_fmac_f32_e32 v68, v182, v146
	v_add_f32_e32 v66, v66, v67
	v_fmac_f32_e32 v66, v68, v100
	ds_write_b32 v180, v66
	s_or_b64 exec, exec, s[4:5]
	s_waitcnt lgkmcnt(0)
	v_add_u32_e32 v74, v165, v166
	ds_read_b128 v[66:69], v74
	ds_read_b128 v[70:73], v74 offset:32
	v_mul_lo_u32 v84, v179, s91
	v_add_u32_e32 v84, 0, v84
	v_lshlrev_b32_e32 v85, 1, v177
	s_waitcnt lgkmcnt(0)
	v_rcp_f32_e32 v75, v66
	v_mul_u32_u24_e32 v86, 0x440, v178
	v_add3_u32 v85, v84, v85, v86
	v_rcp_f32_e32 v76, v67
	v_mul_f32_e32 v2, v2, v75
	v_bfe_u32 v86, v2, 16, 1
	v_add3_u32 v2, v2, v86, s92
	v_rcp_f32_e32 v77, v68
	v_rcp_f32_e32 v78, v69
	v_rcp_f32_e32 v79, v70
	ds_read_b128 v[66:69], v74 offset:64
	v_rcp_f32_e32 v80, v71
	v_rcp_f32_e32 v81, v72
	v_rcp_f32_e32 v82, v73
	ds_read_b128 v[70:73], v74 offset:96
	s_waitcnt lgkmcnt(0)
	s_barrier
; __device__ __forceinline__ unsigned f2bf(float f) { unsigned u = __builtin_bit_cast(unsigned, f); return (u + 0x7fffu + ((u >> 16) & 1u)) >> 16; }
; __device__ __forceinline__ int crow(int r, int hi) { return (r & 3) + 8 * (r >> 2) + 4 * hi; }
; __device__ __forceinline__ void attn_dma_body(const bf16_t* __restrict__ Qb, int ldq, int tpos0, const float* __restrict__ rope, const float* __restrict__ qgain, ...
;     ...
;   { char* st = lds + wid * 8704;
; #pragma unroll
;     for (int r = 0; r < 16; ++r) { const int orow = crow(r, hi);
; #pragma unroll
;       for (int d0 = 0; d0 < 4; ++d0) *(bf16_t*)(st + orow * 272 + (d0 * 32 + r32) * 2) = (bf16_t)f2bf(o[d0][r] * rli[r]); }
;     asm volatile("s_waitcnt lgkmcnt(0)" ::: "memory");
	ds_write_b16_d16_hi v85, v2
	v_mul_f32_e32 v2, v50, v75
	v_bfe_u32 v50, v2, 16, 1
	v_add3_u32 v2, v2, v50, s92
	ds_write_b16_d16_hi v85, v2 offset:64
	v_mul_f32_e32 v2, v34, v75
	v_bfe_u32 v34, v2, 16, 1
	v_add3_u32 v2, v2, v34, s92
	ds_write_b16_d16_hi v85, v2 offset:128
	v_mul_f32_e32 v2, v18, v75
	v_bfe_u32 v18, v2, 16, 1
	v_add3_u32 v2, v2, v18, s92
	ds_write_b16_d16_hi v85, v2 offset:192
	v_mul_f32_e32 v2, v3, v76
	v_bfe_u32 v3, v2, 16, 1
	v_add3_u32 v2, v2, v3, s92
	ds_write_b16_d16_hi v85, v2 offset:272
	v_mul_f32_e32 v2, v51, v76
	v_bfe_u32 v3, v2, 16, 1
	v_add3_u32 v2, v2, v3, s92
	ds_write_b16_d16_hi v85, v2 offset:336
	v_mul_f32_e32 v2, v35, v76
	v_bfe_u32 v3, v2, 16, 1
	v_add3_u32 v2, v2, v3, s92
	ds_write_b16_d16_hi v85, v2 offset:400
	v_mul_f32_e32 v2, v19, v76
	v_bfe_u32 v3, v2, 16, 1
	v_add3_u32 v2, v2, v3, s92
	ds_write_b16_d16_hi v85, v2 offset:464
	v_mul_f32_e32 v2, v4, v77
	v_bfe_u32 v3, v2, 16, 1
	v_add3_u32 v2, v2, v3, s92
	ds_write_b16_d16_hi v85, v2 offset:544
	v_mul_f32_e32 v2, v52, v77
	v_bfe_u32 v3, v2, 16, 1
	v_add3_u32 v2, v2, v3, s92
	ds_write_b16_d16_hi v85, v2 offset:608
	v_mul_f32_e32 v2, v36, v77
	v_bfe_u32 v3, v2, 16, 1
	v_add3_u32 v2, v2, v3, s92
	ds_write_b16_d16_hi v85, v2 offset:672
	v_mul_f32_e32 v2, v20, v77
	v_bfe_u32 v3, v2, 16, 1
	v_add3_u32 v2, v2, v3, s92
	ds_write_b16_d16_hi v85, v2 offset:736
	v_mul_f32_e32 v2, v5, v78
	v_bfe_u32 v3, v2, 16, 1
	v_add3_u32 v2, v2, v3, s92
	ds_write_b16_d16_hi v85, v2 offset:816
	v_mul_f32_e32 v2, v53, v78
	v_bfe_u32 v3, v2, 16, 1
	v_add3_u32 v2, v2, v3, s92
	ds_write_b16_d16_hi v85, v2 offset:880
	v_mul_f32_e32 v2, v37, v78
	v_bfe_u32 v3, v2, 16, 1
	v_add3_u32 v2, v2, v3, s92
	ds_write_b16_d16_hi v85, v2 offset:944
	v_mul_f32_e32 v2, v21, v78
	v_bfe_u32 v3, v2, 16, 1
	v_add3_u32 v2, v2, v3, s92
	ds_write_b16_d16_hi v85, v2 offset:1008
	v_mul_f32_e32 v2, v6, v79
	v_bfe_u32 v3, v2, 16, 1
	v_add3_u32 v2, v2, v3, s92
	ds_write_b16_d16_hi v85, v2 offset:2176
	v_mul_f32_e32 v2, v54, v79
	v_bfe_u32 v3, v2, 16, 1
	v_add3_u32 v2, v2, v3, s92
	ds_write_b16_d16_hi v85, v2 offset:2240
	v_mul_f32_e32 v2, v38, v79
	v_bfe_u32 v3, v2, 16, 1
	v_add3_u32 v2, v2, v3, s92
	ds_write_b16_d16_hi v85, v2 offset:2304
	v_mul_f32_e32 v2, v22, v79
	v_bfe_u32 v3, v2, 16, 1
	v_add3_u32 v2, v2, v3, s92
	ds_write_b16_d16_hi v85, v2 offset:2368
	v_mul_f32_e32 v2, v7, v80
	v_bfe_u32 v3, v2, 16, 1
	v_add3_u32 v2, v2, v3, s92
	ds_write_b16_d16_hi v85, v2 offset:2448
	v_mul_f32_e32 v2, v55, v80
	v_bfe_u32 v3, v2, 16, 1
	v_add3_u32 v2, v2, v3, s92
	ds_write_b16_d16_hi v85, v2 offset:2512
	v_mul_f32_e32 v2, v39, v80
	v_bfe_u32 v3, v2, 16, 1
	v_add3_u32 v2, v2, v3, s92
	ds_write_b16_d16_hi v85, v2 offset:2576
	v_mul_f32_e32 v2, v23, v80
	v_bfe_u32 v3, v2, 16, 1
	v_add3_u32 v2, v2, v3, s92
	ds_write_b16_d16_hi v85, v2 offset:2640
	v_mul_f32_e32 v2, v8, v81
	v_bfe_u32 v3, v2, 16, 1
	v_add3_u32 v2, v2, v3, s92
	ds_write_b16_d16_hi v85, v2 offset:2720
	v_mul_f32_e32 v2, v56, v81
	v_bfe_u32 v3, v2, 16, 1
	v_add3_u32 v2, v2, v3, s92
	ds_write_b16_d16_hi v85, v2 offset:2784
	v_mul_f32_e32 v2, v40, v81
	v_bfe_u32 v3, v2, 16, 1
	v_add3_u32 v2, v2, v3, s92
	ds_write_b16_d16_hi v85, v2 offset:2848
	v_mul_f32_e32 v2, v24, v81
	v_bfe_u32 v3, v2, 16, 1
	v_add3_u32 v2, v2, v3, s92
	ds_write_b16_d16_hi v85, v2 offset:2912
	v_mul_f32_e32 v2, v9, v82
	v_bfe_u32 v3, v2, 16, 1
	v_add3_u32 v2, v2, v3, s92
	ds_write_b16_d16_hi v85, v2 offset:2992
	v_mul_f32_e32 v2, v57, v82
	v_bfe_u32 v3, v2, 16, 1
	v_add3_u32 v2, v2, v3, s92
	ds_write_b16_d16_hi v85, v2 offset:3056
	v_mul_f32_e32 v2, v41, v82
	v_bfe_u32 v3, v2, 16, 1
	s_waitcnt lgkmcnt(0)
	v_rcp_f32_e32 v74, v66
	v_add3_u32 v2, v2, v3, s92
	ds_write_b16_d16_hi v85, v2 offset:3120
	v_mul_f32_e32 v2, v25, v82
	v_bfe_u32 v3, v2, 16, 1
	v_add3_u32 v2, v2, v3, s92
	ds_write_b16_d16_hi v85, v2 offset:3184
	v_mul_f32_e32 v2, v10, v74
	v_bfe_u32 v3, v2, 16, 1
	v_add3_u32 v2, v2, v3, s92
	ds_write_b16_d16_hi v85, v2 offset:4352
	v_mul_f32_e32 v2, v58, v74
	v_bfe_u32 v3, v2, 16, 1
	v_add3_u32 v2, v2, v3, s92
	ds_write_b16_d16_hi v85, v2 offset:4416
	v_mul_f32_e32 v2, v42, v74
	v_bfe_u32 v3, v2, 16, 1
	v_rcp_f32_e32 v83, v67
	v_add3_u32 v2, v2, v3, s92
	ds_write_b16_d16_hi v85, v2 offset:4480
	v_mul_f32_e32 v2, v26, v74
	v_bfe_u32 v3, v2, 16, 1
	v_add3_u32 v2, v2, v3, s92
	ds_write_b16_d16_hi v85, v2 offset:4544
	v_mul_f32_e32 v2, v11, v83
	v_bfe_u32 v3, v2, 16, 1
	v_add3_u32 v2, v2, v3, s92
	ds_write_b16_d16_hi v85, v2 offset:4624
	v_mul_f32_e32 v2, v59, v83
	v_bfe_u32 v3, v2, 16, 1
	v_add3_u32 v2, v2, v3, s92
	ds_write_b16_d16_hi v85, v2 offset:4688
	v_mul_f32_e32 v2, v43, v83
	v_bfe_u32 v3, v2, 16, 1
	v_rcp_f32_e32 v68, v68
	v_add3_u32 v2, v2, v3, s92
	ds_write_b16_d16_hi v85, v2 offset:4752
	v_mul_f32_e32 v2, v27, v83
	v_bfe_u32 v3, v2, 16, 1
	v_add3_u32 v2, v2, v3, s92
	ds_write_b16_d16_hi v85, v2 offset:4816
	v_mul_f32_e32 v2, v12, v68
	v_bfe_u32 v3, v2, 16, 1
	v_add3_u32 v2, v2, v3, s92
	ds_write_b16_d16_hi v85, v2 offset:4896
	v_mul_f32_e32 v2, v60, v68
	v_bfe_u32 v3, v2, 16, 1
	v_add3_u32 v2, v2, v3, s92
	ds_write_b16_d16_hi v85, v2 offset:4960
	v_mul_f32_e32 v2, v44, v68
	v_bfe_u32 v3, v2, 16, 1
	v_rcp_f32_e32 v69, v69
	v_add3_u32 v2, v2, v3, s92
	ds_write_b16_d16_hi v85, v2 offset:5024
	v_mul_f32_e32 v2, v28, v68
	v_bfe_u32 v3, v2, 16, 1
	v_add3_u32 v2, v2, v3, s92
	ds_write_b16_d16_hi v85, v2 offset:5088
	v_mul_f32_e32 v2, v13, v69
	v_bfe_u32 v3, v2, 16, 1
	v_add3_u32 v2, v2, v3, s92
	ds_write_b16_d16_hi v85, v2 offset:5168
	v_mul_f32_e32 v2, v61, v69
	v_bfe_u32 v3, v2, 16, 1
	v_add3_u32 v2, v2, v3, s92
	ds_write_b16_d16_hi v85, v2 offset:5232
	v_mul_f32_e32 v2, v45, v69
; __device__ __forceinline__ unsigned f2bf(float f) { unsigned u = __builtin_bit_cast(unsigned, f); return (u + 0x7fffu + ((u >> 16) & 1u)) >> 16; }
; __device__ __forceinline__ int crow(int r, int hi) { return (r & 3) + 8 * (r >> 2) + 4 * hi; }
; #define ATT_WAIT_BAR() asm volatile("s_waitcnt vmcnt(0) lgkmcnt(0)\n\ts_barrier" ::: "memory")
; __device__ __forceinline__ void attn_dma_body(const bf16_t* __restrict__ Qb, int ldq, int tpos0, const float* __restrict__ rope, const float* __restrict__ qgain, ...
;     ...
;   { char* st = lds + wid * 8704;
; #pragma unroll
;     for (int r = 0; r < 16; ++r) { const int orow = crow(r, hi);
; #pragma unroll
;       for (int d0 = 0; d0 < 4; ++d0) *(bf16_t*)(st + orow * 272 + (d0 * 32 + r32) * 2) = (bf16_t)f2bf(o[d0][r] * rli[r]); }
;     asm volatile("s_waitcnt lgkmcnt(0)" ::: "memory");
; #pragma unroll
;     for (int i = 0; i < 8; ++i) { const int c = i * 64 + lane, row = c >> 4, cc = c & 15; const u32x4 v = *(const u32x4*)(st + row * 272 + cc * 16);
;       const bf16_t* gp = Ow + (long)row * LDO + cc * 8;
;       asm volatile("global_store_dwordx4 %0, %1, off sc1\n\ts_nop 1" :: "v"(gp), "v"(v) : "memory"); } }
;   ATT_WAIT_BAR();
	v_bfe_u32 v3, v2, 16, 1
	v_rcp_f32_e32 v70, v70
	v_add3_u32 v2, v2, v3, s92
	ds_write_b16_d16_hi v85, v2 offset:5296
	v_mul_f32_e32 v2, v29, v69
	v_bfe_u32 v3, v2, 16, 1
	v_add3_u32 v2, v2, v3, s92
	ds_write_b16_d16_hi v85, v2 offset:5360
	v_mul_f32_e32 v2, v14, v70
	v_bfe_u32 v3, v2, 16, 1
	v_add3_u32 v2, v2, v3, s92
	ds_write_b16_d16_hi v85, v2 offset:6528
	v_mul_f32_e32 v2, v62, v70
	v_bfe_u32 v3, v2, 16, 1
	v_add3_u32 v2, v2, v3, s92
	ds_write_b16_d16_hi v85, v2 offset:6592
	v_mul_f32_e32 v2, v46, v70
	v_bfe_u32 v3, v2, 16, 1
	v_rcp_f32_e32 v71, v71
	v_add3_u32 v2, v2, v3, s92
	ds_write_b16_d16_hi v85, v2 offset:6656
	v_mul_f32_e32 v2, v30, v70
	v_bfe_u32 v3, v2, 16, 1
	v_add3_u32 v2, v2, v3, s92
	ds_write_b16_d16_hi v85, v2 offset:6720
	v_mul_f32_e32 v2, v15, v71
	v_bfe_u32 v3, v2, 16, 1
	v_add3_u32 v2, v2, v3, s92
	ds_write_b16_d16_hi v85, v2 offset:6800
	v_mul_f32_e32 v2, v63, v71
	v_bfe_u32 v3, v2, 16, 1
	v_add3_u32 v2, v2, v3, s92
	ds_write_b16_d16_hi v85, v2 offset:6864
	v_mul_f32_e32 v2, v47, v71
	v_bfe_u32 v3, v2, 16, 1
	v_rcp_f32_e32 v72, v72
	v_add3_u32 v2, v2, v3, s92
	ds_write_b16_d16_hi v85, v2 offset:6928
	v_mul_f32_e32 v2, v31, v71
	v_bfe_u32 v3, v2, 16, 1
	v_add3_u32 v2, v2, v3, s92
	ds_write_b16_d16_hi v85, v2 offset:6992
	v_mul_f32_e32 v2, v16, v72
	v_bfe_u32 v3, v2, 16, 1
	v_add3_u32 v2, v2, v3, s92
	ds_write_b16_d16_hi v85, v2 offset:7072
	v_mul_f32_e32 v2, v64, v72
	v_bfe_u32 v3, v2, 16, 1
	v_add3_u32 v2, v2, v3, s92
	ds_write_b16_d16_hi v85, v2 offset:7136
	v_mul_f32_e32 v2, v48, v72
	v_bfe_u32 v3, v2, 16, 1
	v_rcp_f32_e32 v73, v73
	v_add3_u32 v2, v2, v3, s92
	ds_write_b16_d16_hi v85, v2 offset:7200
	v_mul_f32_e32 v2, v32, v72
	v_bfe_u32 v3, v2, 16, 1
	v_add3_u32 v2, v2, v3, s92
	ds_write_b16_d16_hi v85, v2 offset:7264
	v_mul_f32_e32 v2, v17, v73
	v_bfe_u32 v3, v2, 16, 1
	v_add3_u32 v2, v2, v3, s92
	ds_write_b16_d16_hi v85, v2 offset:7344
	v_mul_f32_e32 v2, v65, v73
	v_bfe_u32 v3, v2, 16, 1
	v_add3_u32 v2, v2, v3, s92
	ds_write_b16_d16_hi v85, v2 offset:7408
	v_mul_f32_e32 v2, v49, v73
	s_lshl_b64 s[2:3], s[70:71], 12
	v_bfe_u32 v3, v2, 16, 1
	s_add_u32 s2, s23, s2
	v_add3_u32 v2, v2, v3, s92
	s_addc_u32 s3, s94, s3
	ds_write_b16_d16_hi v85, v2 offset:7472
	v_mul_f32_e32 v2, v33, v73
	s_add_u32 s2, s2, s44
	v_ashrrev_i32_e32 v165, 31, v164
	v_bfe_u32 v3, v2, 16, 1
	s_addc_u32 s3, s3, s45
	v_lshlrev_b64 v[66:67], 12, v[164:165]
	v_add3_u32 v2, v2, v3, s92
	v_lshrrev_b32_e32 v8, 4, v167
	ds_write_b16_d16_hi v85, v2 offset:7536
	v_lshlrev_b32_e32 v162, 4, v176
	v_mul_u32_u24_e32 v2, 0x110, v8
	v_lshl_add_u64 v[6:7], s[2:3], 0, v[66:67]
	v_add3_u32 v10, v84, v162, v2
	v_lshl_add_u64 v[6:7], v[6:7], 0, v[162:163]
	v_lshlrev_b32_e32 v162, 12, v8
	s_waitcnt lgkmcnt(0)
	v_lshl_add_u64 v[8:9], v[6:7], 0, v[162:163]
	ds_read_b128 v[2:5], v10
	s_waitcnt lgkmcnt(0)
	global_store_dwordx4 v[8:9], v[2:5], off sc1
	s_nop 1
	v_or_b32_e32 v8, 0x4000, v162
	v_mov_b32_e32 v9, v163
	v_lshl_add_u64 v[8:9], v[6:7], 0, v[8:9]
	ds_read_b128 v[2:5], v10 offset:1088
	s_waitcnt lgkmcnt(0)
	global_store_dwordx4 v[8:9], v[2:5], off sc1
	s_nop 1
	v_or_b32_e32 v8, 0x8000, v162
	v_mov_b32_e32 v9, v163
	v_lshl_add_u64 v[8:9], v[6:7], 0, v[8:9]
	ds_read_b128 v[2:5], v10 offset:2176
	s_waitcnt lgkmcnt(0)
	global_store_dwordx4 v[8:9], v[2:5], off sc1
	s_nop 1
	v_or_b32_e32 v8, 0xc000, v162
	v_mov_b32_e32 v9, v163
	v_lshl_add_u64 v[8:9], v[6:7], 0, v[8:9]
	ds_read_b128 v[2:5], v10 offset:3264
	s_waitcnt lgkmcnt(0)
	global_store_dwordx4 v[8:9], v[2:5], off sc1
	s_nop 1
	v_or_b32_e32 v8, 0x10000, v162
	v_mov_b32_e32 v9, v163
	v_lshl_add_u64 v[8:9], v[6:7], 0, v[8:9]
	ds_read_b128 v[2:5], v10 offset:4352
	s_waitcnt lgkmcnt(0)
	global_store_dwordx4 v[8:9], v[2:5], off sc1
	s_nop 1
	v_or_b32_e32 v8, 0x14000, v162
	v_mov_b32_e32 v9, v163
	v_lshl_add_u64 v[8:9], v[6:7], 0, v[8:9]
	ds_read_b128 v[2:5], v10 offset:5440
	s_waitcnt lgkmcnt(0)
	global_store_dwordx4 v[8:9], v[2:5], off sc1
	s_nop 1
	v_or_b32_e32 v8, 0x18000, v162
	v_mov_b32_e32 v9, v163
	ds_read_b128 v[2:5], v10 offset:6528
	v_lshl_add_u64 v[8:9], v[6:7], 0, v[8:9]
	s_waitcnt lgkmcnt(0)
	global_store_dwordx4 v[8:9], v[2:5], off sc1
	s_nop 1
	v_or_b32_e32 v162, 0x1c000, v162
	ds_read_b128 v[2:5], v10 offset:7616
	v_lshl_add_u64 v[6:7], v[6:7], 0, v[162:163]
	s_waitcnt lgkmcnt(0)
	global_store_dwordx4 v[6:7], v[2:5], off sc1
	s_nop 1
	s_waitcnt vmcnt(0) lgkmcnt(0)
	s_barrier
	s_branch .LBB0_437
; __device__ __forceinline__ int otid() { int t = threadIdx.x; asm volatile("" : "+v"(t)); return t; }
; __device__ __forceinline__ void attn_dma_body(const bf16_t* __restrict__ Qb, int ldq, int tpos0, const float* __restrict__ rope, const float* __restrict__ qgain, ...
;   const int tid = otid(), wid = tid >> 6, lane = tid & 63, r32 = lane & 31, hi = lane >> 5;
;   float* ws = (float*)(lds + TAB_OFF + 1024) + wid * 64; float* li_l = ws; float* al_l = ws + 32;
;   float m_reg = -1e30f, l_reg = 0; f32x16 o[4] = {}; bf16x8 qr[8];
;   const bf16_t* Qw = Qb + (long)(wid * QBLK + r32) * ldq + hi * 8;
;   unsigned koff[2], voff[2];
; #pragma unroll
;   for (int c = 0; c < 2; ++c) { const int g = c * 512 + tid;
;     { const int row = g >> 4, ch = (g & 15) ^ (row & 7); koff[c] = (unsigned)(row * 128 + ch * 8) * 2u; }
;     { const int sub = g >> 5, kk = (sub >> 2) * 8 + ((g >> 2) & 7), k = (kk & ~0xC) | ((kk & 4) << 1) | ((kk & 8) >> 1), col = (sub & 3) * 32 + (g & 3) * 8; voff[c] = (unsigned)(k * 128 + col) * 2u; } }
;   const unsigned wbase = (unsigned)__builtin_amdgcn_readfirstlane(wid) * 1024u;
;   typedef __attribute__((address_space(3))) unsigned lds_u32;
;   lds_u32* ldsl = (lds_u32*)(__attribute__((address_space(3))) char*)lds;
;     ...
;   const int NT = seq / KVBLK;
;   ATT_DMA(0, 0); ATT_DMA(1, 1);
; #pragma unroll
;   for (int d0 = 0; d0 < 8; ++d0) qr[d0] = ld8(Qw + d0 * 16);
;   if (tpos0 >= 0) {
;     float ss = 0.f;
; #pragma unroll
;     for (int d0 = 0; d0 < 8; ++d0)
; #pragma unroll
;       for (int i = 0; i < 8; ++i) { const float x = bf2f((unsigned)(unsigned short)qr[d0][i]); ss += x * x; }
;     { auto rr = __builtin_amdgcn_permlane32_swap(__float_as_uint(ss), __float_as_uint(ss), false, false); ss = __uint_as_float(rr[0]) + __uint_as_float(rr[1]); }
;     const float rinv = 1.0f / sqrtf(ss * (1.0f / 128.0f) + RMS_EPS);
.Lorig_entry:
	v_mov_b32_e32 v147, v0
	s_mul_i32 s2, s71, 0x1800
	s_waitcnt vmcnt(0)
	v_and_b32_e32 v3, 0x60, v147
	v_lshlrev_b32_e32 v5, 3, v147
	v_and_b32_e32 v176, 15, v147
	v_lshrrev_b32_e32 v2, 1, v147
	v_and_or_b32 v3, v5, 24, v3
	v_ashrrev_i32_e32 v5, 4, v147
	v_bfe_u32 v146, v147, 2, 2
	v_and_b32_e32 v148, 8, v2
	v_bitop3_b32 v6, v5, v176, 7 bitop3:0x6c
	v_lshlrev_b32_e32 v149, 8, v5
	v_and_b32_e32 v154, 0xfffff0, v5
	v_lshrrev_b32_e32 v5, 1, v5
	v_or_b32_e32 v2, v148, v146
	v_and_b32_e32 v156, 4, v5
	s_mul_hi_u32 s3, s70, 0x1800
	v_lshlrev_b32_e32 v3, 1, v3
	v_or3_b32 v5, v154, v156, v2
	s_add_i32 s3, s3, s2
	s_mul_i32 s2, s70, 0x1800
	v_lshl_or_b32 v30, v5, 8, v3
	v_add_u32_e32 v5, 0x200, v147
	s_add_u32 s2, s22, s2
	v_ashrrev_i32_e32 v5, 4, v5
	s_addc_u32 s3, s88, s3
	s_lshl_b64 s[44:45], s[72:73], 1
	v_lshlrev_b32_e32 v150, 4, v6
	v_bitop3_b32 v6, v5, v176, 7 bitop3:0x6c
	v_lshlrev_b32_e32 v151, 8, v5
	v_and_b32_e32 v153, 0xfffff0, v5
	v_lshrrev_b32_e32 v5, 1, v5
	s_add_u32 s2, s2, s44
	v_ashrrev_i32_e32 v179, 6, v147
	v_and_b32_e32 v155, 4, v5
	s_addc_u32 s3, s3, s45
	v_and_b32_e32 v177, 31, v147
	v_lshlrev_b32_e32 v164, 5, v179
	v_or3_b32 v2, v153, v155, v2
	v_or_b32_e32 v4, v164, v177
	v_lshl_or_b32 v34, v2, 8, v3
	v_mov_b64_e32 v[2:3], s[2:3]
	s_movk_i32 s2, 0x1800
	v_mad_i64_i32 v[2:3], s[2:3], v4, s2, v[2:3]
	v_readfirstlane_b32 s2, v179
	s_lshl_b32 s2, s2, 10
	s_add_i32 s96, s2, 0
	v_or_b32_e32 v162, v150, v149
	s_add_i32 s2, s96, 0x4000
	s_mov_b32 m0, s96
	v_lshlrev_b32_e32 v152, 4, v6
	global_load_lds_dwordx4 v162, s[38:39]
	s_mov_b32 m0, s2
	v_or_b32_e32 v32, v152, v151
	global_load_lds_dwordx4 v30, s[40:41]
	s_add_i32 m0, s96, 0x2000
	v_bfe_u32 v178, v147, 5, 1
	global_load_lds_dwordx4 v32, s[38:39]
	s_add_i32 m0, s96, 0x6000
	s_add_u32 s2, s38, 0x4000
	s_addc_u32 s3, s39, 0
	s_add_u32 s4, s40, 0x4000
	global_load_lds_dwordx4 v34, s[40:41]
	s_addc_u32 s5, s41, 0
	s_add_i32 m0, s96, 0x8000
	s_add_i32 s6, s96, 0xc000
	global_load_lds_dwordx4 v162, s[2:3]
	s_mov_b32 m0, s6
	v_lshlrev_b32_e32 v166, 4, v178
	global_load_lds_dwordx4 v30, s[4:5]
	s_add_i32 m0, s96, 0xa000
	v_mov_b32_e32 v167, v163
	global_load_lds_dwordx4 v32, s[2:3]
	s_add_i32 m0, s96, 0xe000
	v_lshl_add_u64 v[2:3], v[2:3], 0, v[166:167]
	global_load_lds_dwordx4 v34, s[4:5]
	global_load_dwordx4 v[102:105], v[2:3], off
	global_load_dwordx4 v[110:113], v[2:3], off offset:32
	global_load_dwordx4 v[98:101], v[2:3], off offset:64
	global_load_dwordx4 v[106:109], v[2:3], off offset:96
	global_load_dwordx4 v[118:121], v[2:3], off offset:128
	global_load_dwordx4 v[126:129], v[2:3], off offset:160
	global_load_dwordx4 v[114:117], v[2:3], off offset:192
	global_load_dwordx4 v[122:125], v[2:3], off offset:224
	s_cmp_lt_i32 s68, 0
	s_cbranch_scc1 .Lorig_408
	v_lshl_or_b32 v3, s68, 8, v177
	v_lshlrev_b32_e32 v2, 3, v178
	v_add_u32_e32 v26, v3, v164
	v_lshlrev_b32_e32 v44, 2, v2
	v_ashrrev_i32_e32 v2, 1, v26
	v_and_b32_e32 v2, 0xffffffe0, v2
	v_ashrrev_i32_e32 v3, 31, v2
	v_mov_b32_e32 v45, v163
	v_lshl_add_u64 v[2:3], v[2:3], 2, s[16:17]
	v_lshl_add_u64 v[76:77], v[2:3], 0, v[44:45]
	s_mov_b64 s[2:3], 0x4000
	v_lshl_add_u64 v[6:7], v[76:77], 0, s[2:3]
	s_waitcnt lgkmcnt(0)
	global_load_dwordx4 v[130:133], v44, s[14:15] offset:16
	global_load_dwordx4 v[14:17], v44, s[14:15] offset:144
	global_load_dwordx4 v[2:5], v[76:77], off offset:16
	s_nop 0
	global_load_dwordx4 v[6:9], v[6:7], off offset:16
	s_nop 0
	global_load_dwordx4 v[22:25], v44, s[14:15]
	global_load_dwordx4 v[18:21], v44, s[14:15] offset:128
	s_waitcnt vmcnt(0)
	v_lshlrev_b32_e32 v38, 16, v129
	v_and_b32_e32 v36, 0xffff0000, v129
	v_lshlrev_b32_e32 v129, 16, v102
	v_lshlrev_b32_e32 v39, 16, v125
	v_and_b32_e32 v37, 0xffff0000, v125
	v_lshlrev_b32_e32 v49, 16, v123
	v_lshlrev_b32_e32 v48, 16, v127
	v_and_b32_e32 v47, 0xffff0000, v123
	v_and_b32_e32 v46, 0xffff0000, v127
	v_lshlrev_b32_e32 v123, 16, v99
	v_and_b32_e32 v127, 0xffff0000, v99
	v_and_b32_e32 v99, 0xffff0000, v102
	v_lshlrev_b32_e32 v53, 16, v122
	v_and_b32_e32 v51, 0xffff0000, v122
	v_lshlrev_b32_e32 v122, 16, v103
	v_lshlrev_b32_e32 v52, 16, v126
	v_and_b32_e32 v50, 0xffff0000, v126
	v_and_b32_e32 v126, 0xffff0000, v103
	v_lshlrev_b32_e32 v90, 16, v111
	v_and_b32_e32 v88, 0xffff0000, v111
	v_lshlrev_b32_e32 v92, 16, v110
	v_and_b32_e32 v94, 0xffff0000, v110
	v_lshlrev_b32_e32 v111, 16, v100
	v_lshlrev_b32_e32 v110, 16, v104
	v_lshlrev_b32_e32 v65, 16, v116
	v_and_b32_e32 v63, 0xffff0000, v116
	v_lshlrev_b32_e32 v73, 16, v114
	v_and_b32_e32 v71, 0xffff0000, v114
	v_lshlrev_b32_e32 v114, 16, v105
	v_and_b32_e32 v116, 0xffff0000, v105
	v_and_b32_e32 v105, 0xffff0000, v100
	v_and_b32_e32 v104, 0xffff0000, v104
	v_lshlrev_b32_e32 v69, 16, v115
	v_and_b32_e32 v67, 0xffff0000, v115
	v_lshlrev_b32_e32 v115, 16, v101
	v_lshlrev_b32_e32 v61, 16, v117
	v_and_b32_e32 v55, 0xffff0000, v117
	v_and_b32_e32 v117, 0xffff0000, v101
	v_lshlrev_b32_e32 v93, 16, v106
	v_and_b32_e32 v95, 0xffff0000, v106
	v_lshlrev_b32_e32 v91, 16, v107
	v_and_b32_e32 v89, 0xffff0000, v107
	v_lshlrev_b32_e32 v87, 16, v108
	v_lshlrev_b32_e32 v86, 16, v112
	v_and_b32_e32 v85, 0xffff0000, v108
	v_and_b32_e32 v84, 0xffff0000, v112
	v_lshlrev_b32_e32 v83, 16, v109
	v_lshlrev_b32_e32 v82, 16, v113
	v_and_b32_e32 v81, 0xffff0000, v109
	v_and_b32_e32 v80, 0xffff0000, v113
	v_lshlrev_b32_e32 v42, 16, v128
	v_and_b32_e32 v40, 0xffff0000, v128
	v_lshlrev_b32_e32 v128, 16, v98
	v_and_b32_e32 v98, 0xffff0000, v98
	s_movk_i32 s4, 0x4000
	v_lshlrev_b32_e32 v26, 7, v26
	v_add_co_u32_e32 v78, vcc, s4, v76
	v_mov_b32_e32 v27, v163
	v_and_b32_e32 v26, 0x1f80, v26
	v_addc_co_u32_e32 v79, vcc, 0, v77, vcc
; __device__ __forceinline__ void attn_dma_body(const bf16_t* __restrict__ Qb, int ldq, int tpos0, const float* __restrict__ rope, const float* __restrict__ qgain, ...
;     ...
;   if (tpos0 >= 0) {
;     float ss = 0.f;
; #pragma unroll
;     for (int d0 = 0; d0 < 8; ++d0)
; #pragma unroll
;       for (int i = 0; i < 8; ++i) { const float x = bf2f((unsigned)(unsigned short)qr[d0][i]); ss += x * x; }
;     { auto rr = __builtin_amdgcn_permlane32_swap(__float_as_uint(ss), __float_as_uint(ss), false, false); ss = __uint_as_float(rr[0]) + __uint_as_float(rr[1]); }
;     const float rinv = 1.0f / sqrtf(ss * (1.0f / 128.0f) + RMS_EPS);
;     const int t = tpos0 + wid * QBLK + r32;
; #pragma unroll
;     for (int ax = 0; ax < 2; ++ax) { const int pos = ax ? (t & 63) : (t >> 6);
; #pragma unroll
;       for (int q = 0; q < 2; ++q) { const int dl = 4 * ax + q, dh = dl + 2, p0 = q * 16 + 8 * hi;
;         const float* cp_ = rope + pos * 32 + p0; const float* gl = qgain + dl * 16 + 8 * hi; const float* gh = qgain + dh * 16 + 8 * hi;
	v_lshl_add_u64 v[26:27], s[16:17], 0, v[26:27]
	global_load_dwordx4 v[10:13], v[78:79], off
	v_lshl_add_u64 v[58:59], v[26:27], 0, v[44:45]
	global_load_dwordx4 v[26:29], v[76:77], off
	v_lshlrev_b32_e32 v72, 16, v118
	v_and_b32_e32 v70, 0xffff0000, v118
	v_lshlrev_b32_e32 v68, 16, v119
	v_and_b32_e32 v66, 0xffff0000, v119
	v_lshlrev_b32_e32 v64, 16, v120
	v_and_b32_e32 v62, 0xffff0000, v120
	v_lshlrev_b32_e32 v60, 16, v121
	v_and_b32_e32 v54, 0xffff0000, v121
	v_lshlrev_b32_e32 v43, 16, v124
	v_and_b32_e32 v41, 0xffff0000, v124
	v_mov_b32_e32 v134, v37
	v_mov_b32_e32 v135, v39
	v_lshl_add_u64 v[74:75], v[58:59], 0, s[2:3]
	v_mov_b32_e32 v125, v20
	v_mul_f32_e32 v20, v129, v129
	v_fmac_f32_e32 v20, v99, v99
	v_pk_fma_f32 v[102:103], v[122:123], v[122:123], v[20:21] op_sel_hi:[1,1,0]
	v_mul_f32_e32 v20, v123, v123
	v_pk_fma_f32 v[102:103], v[126:127], v[126:127], v[102:103]
	s_mov_b32 s2, 0xf800000
	v_pk_fma_f32 v[102:103], v[110:111], v[110:111], v[102:103]
	v_mov_b32_e32 v124, v24
	v_pk_fma_f32 v[102:103], v[104:105], v[104:105], v[102:103]
	v_mov_b32_e32 v120, v130
	v_pk_fma_f32 v[102:103], v[114:115], v[114:115], v[102:103]
	v_mov_b32_e32 v121, v14
	v_pk_fma_f32 v[102:103], v[116:117], v[116:117], v[102:103]
	v_mov_b32_e32 v14, v131
	v_pk_fma_f32 v[102:103], v[92:93], v[92:93], v[102:103]
	v_mov_b32_e32 v118, v132
	v_pk_fma_f32 v[102:103], v[94:95], v[94:95], v[102:103]
	v_mov_b32_e32 v119, v16
	v_pk_fma_f32 v[102:103], v[90:91], v[90:91], v[102:103]
	v_mov_b32_e32 v16, v133
	v_pk_fma_f32 v[102:103], v[88:89], v[88:89], v[102:103]
	v_mov_b32_e32 v106, v6
	v_pk_fma_f32 v[102:103], v[86:87], v[86:87], v[102:103]
	v_mov_b32_e32 v107, v2
	v_pk_fma_f32 v[102:103], v[84:85], v[84:85], v[102:103]
	v_lshl_add_u64 v[96:97], v[76:77], 0, s[24:25]
	v_pk_fma_f32 v[102:103], v[82:83], v[82:83], v[102:103]
	v_mov_b32_e32 v112, v8
	v_pk_fma_f32 v[102:103], v[80:81], v[80:81], v[102:103]
	v_mov_b32_e32 v113, v4
	v_pk_fma_f32 v[102:103], v[128:129], v[128:129], v[102:103]
	v_mov_b32_e32 v108, v9
	v_pk_fma_f32 v[102:103], v[98:99], v[98:99], v[102:103]
	v_mov_b32_e32 v109, v5
	v_pk_add_f32 v[102:103], v[20:21], v[102:103] op_sel_hi:[0,1]
	v_mul_f32_e32 v20, v127, v127
	v_pk_add_f32 v[102:103], v[20:21], v[102:103] op_sel_hi:[0,1]
	v_mul_f32_e32 v20, v111, v111
	v_pk_add_f32 v[102:103], v[20:21], v[102:103] op_sel_hi:[0,1]
	v_mul_f32_e32 v20, v105, v105
	v_pk_add_f32 v[102:103], v[20:21], v[102:103] op_sel_hi:[0,1]
	v_mul_f32_e32 v20, v115, v115
	v_pk_add_f32 v[102:103], v[20:21], v[102:103] op_sel_hi:[0,1]
	v_mul_f32_e32 v20, v117, v117
	v_pk_add_f32 v[102:103], v[20:21], v[102:103] op_sel_hi:[0,1]
	v_mul_f32_e32 v20, v93, v93
	v_pk_add_f32 v[102:103], v[20:21], v[102:103] op_sel_hi:[0,1]
	v_mul_f32_e32 v20, v95, v95
	v_pk_add_f32 v[102:103], v[20:21], v[102:103] op_sel_hi:[0,1]
	v_mul_f32_e32 v20, v91, v91
	v_pk_add_f32 v[102:103], v[20:21], v[102:103] op_sel_hi:[0,1]
	v_mul_f32_e32 v20, v89, v89
	v_pk_add_f32 v[102:103], v[20:21], v[102:103] op_sel_hi:[0,1]
	v_mul_f32_e32 v20, v87, v87
	v_pk_add_f32 v[102:103], v[20:21], v[102:103] op_sel_hi:[0,1]
	v_mul_f32_e32 v20, v85, v85
	v_pk_add_f32 v[102:103], v[20:21], v[102:103] op_sel_hi:[0,1]
	v_mul_f32_e32 v20, v83, v83
	v_pk_add_f32 v[102:103], v[20:21], v[102:103] op_sel_hi:[0,1]
	v_mul_f32_e32 v20, v81, v81
	v_pk_add_f32 v[102:103], v[20:21], v[102:103] op_sel_hi:[0,1]
	v_pk_fma_f32 v[102:103], v[72:73], v[72:73], v[102:103]
	v_mul_f32_e32 v20, v73, v73
	v_pk_fma_f32 v[102:103], v[70:71], v[70:71], v[102:103]
	s_waitcnt vmcnt(1)
	v_mov_b32_e32 v100, v12
	v_pk_fma_f32 v[102:103], v[68:69], v[68:69], v[102:103]
	s_waitcnt vmcnt(0)
	v_mov_b32_e32 v101, v28
	v_pk_fma_f32 v[102:103], v[66:67], v[66:67], v[102:103]
	v_lshl_add_u64 v[56:57], v[58:59], 0, s[24:25]
	v_pk_fma_f32 v[102:103], v[64:65], v[64:65], v[102:103]
	s_nop 0
	v_pk_fma_f32 v[102:103], v[62:63], v[62:63], v[102:103]
	s_nop 0
	v_pk_fma_f32 v[102:103], v[60:61], v[60:61], v[102:103]
	s_nop 0
	v_pk_fma_f32 v[102:103], v[54:55], v[54:55], v[102:103]
	s_nop 0
	v_pk_fma_f32 v[102:103], v[52:53], v[52:53], v[102:103]
	s_nop 0
	v_pk_fma_f32 v[102:103], v[50:51], v[50:51], v[102:103]
	s_nop 0
	v_pk_fma_f32 v[102:103], v[48:49], v[48:49], v[102:103]
	s_nop 0
	v_pk_fma_f32 v[102:103], v[46:47], v[46:47], v[102:103]
	s_nop 0
	v_pk_fma_f32 v[102:103], v[42:43], v[42:43], v[102:103]
	s_nop 0
	v_pk_fma_f32 v[102:103], v[40:41], v[40:41], v[102:103]
	s_nop 0
	v_pk_fma_f32 v[102:103], v[38:39], v[38:39], v[102:103]
	s_nop 0
	v_pk_fma_f32 v[102:103], v[36:37], v[36:37], v[102:103]
	s_nop 0
	v_pk_add_f32 v[102:103], v[20:21], v[102:103] op_sel_hi:[0,1]
	v_mul_f32_e32 v20, v71, v71
	v_pk_add_f32 v[102:103], v[20:21], v[102:103] op_sel_hi:[0,1]
	v_mul_f32_e32 v20, v69, v69
	v_pk_add_f32 v[102:103], v[20:21], v[102:103] op_sel_hi:[0,1]
	v_mul_f32_e32 v20, v67, v67
	v_pk_add_f32 v[102:103], v[20:21], v[102:103] op_sel_hi:[0,1]
	v_mul_f32_e32 v20, v65, v65
	v_pk_add_f32 v[102:103], v[20:21], v[102:103] op_sel_hi:[0,1]
	v_mul_f32_e32 v20, v63, v63
	v_pk_add_f32 v[102:103], v[20:21], v[102:103] op_sel_hi:[0,1]
	v_mul_f32_e32 v20, v61, v61
	v_pk_add_f32 v[102:103], v[20:21], v[102:103] op_sel_hi:[0,1]
	v_mul_f32_e32 v20, v55, v55
	v_pk_add_f32 v[102:103], v[20:21], v[102:103] op_sel_hi:[0,1]
	v_mul_f32_e32 v20, v53, v53
	v_pk_add_f32 v[102:103], v[20:21], v[102:103] op_sel_hi:[0,1]
	v_mul_f32_e32 v20, v51, v51
	v_pk_add_f32 v[102:103], v[20:21], v[102:103] op_sel_hi:[0,1]
	v_mul_f32_e32 v20, v49, v49
	v_pk_add_f32 v[102:103], v[20:21], v[102:103] op_sel_hi:[0,1]
	v_mul_f32_e32 v20, v47, v47
	v_pk_add_f32 v[102:103], v[20:21], v[102:103] op_sel_hi:[0,1]
; __device__ __forceinline__ unsigned pk2(float lo, float hi) { unsigned r; asm("v_cvt_pk_bf16_f32 %0, %1, %2" : "=v"(r) : "v"(lo), "v"(hi)); return r; }
; __device__ __forceinline__ void attn_dma_body(const bf16_t* __restrict__ Qb, int ldq, int tpos0, const float* __restrict__ rope, const float* __restrict__ qgain, ...
;     ...
;     { auto rr = __builtin_amdgcn_permlane32_swap(__float_as_uint(ss), __float_as_uint(ss), false, false); ss = __uint_as_float(rr[0]) + __uint_as_float(rr[1]); }
;     const float rinv = 1.0f / sqrtf(ss * (1.0f / 128.0f) + RMS_EPS);
;     const int t = tpos0 + wid * QBLK + r32;
; #pragma unroll
;     for (int ax = 0; ax < 2; ++ax) { const int pos = ax ? (t & 63) : (t >> 6);
; #pragma unroll
;       for (int q = 0; q < 2; ++q) { const int dl = 4 * ax + q, dh = dl + 2, p0 = q * 16 + 8 * hi;
;         const float* cp_ = rope + pos * 32 + p0; const float* gl = qgain + dl * 16 + 8 * hi; const float* gh = qgain + dh * 16 + 8 * hi;
;         float cs[8], sn[8], lo[8], hv[8];
; #pragma unroll
;         for (int i = 0; i < 8; ++i) { cs[i] = cp_[i]; sn[i] = cp_[4096 + i];
;           lo[i] = bf2f((unsigned)(unsigned short)qr[dl][i]) * rinv * gl[i]; hv[i] = bf2f((unsigned)(unsigned short)qr[dh][i]) * rinv * gh[i]; }
;         u32x4 wl, wh;
; #pragma unroll
;         for (int i = 0; i < 4; ++i) { const float l0 = lo[2 * i] * cs[2 * i] - hv[2 * i] * sn[2 * i], l1 = lo[2 * i + 1] * cs[2 * i + 1] - hv[2 * i + 1] * sn[2 * i + 1];
;           const float h0 = hv[2 * i] * cs[2 * i] + lo[2 * i] * sn[2 * i], h1 = hv[2 * i + 1] * cs[2 * i + 1] + lo[2 * i + 1] * sn[2 * i + 1];
;           wl[i] = pk2(l0, l1); wh[i] = pk2(h0, h1); }
;         qr[dl] = *reinterpret_cast<bf16x8*>(&wl); qr[dh] = *reinterpret_cast<bf16x8*>(&wh); } } }
	v_mul_f32_e32 v20, v43, v43
	v_pk_add_f32 v[102:103], v[20:21], v[102:103] op_sel_hi:[0,1]
	v_mul_f32_e32 v20, v41, v41
	v_pk_add_f32 v[102:103], v[20:21], v[102:103] op_sel_hi:[0,1]
	v_mul_f32_e32 v20, v39, v39
	v_pk_add_f32 v[102:103], v[20:21], v[102:103] op_sel_hi:[0,1]
	v_pk_fma_f32 v[102:103], v[134:135], v[134:135], v[102:103]
	global_load_dwordx4 v[130:133], v44, s[14:15] offset:80
	global_load_dwordx4 v[134:137], v44, s[14:15] offset:64
	global_load_dwordx4 v[138:141], v44, s[14:15] offset:208
	global_load_dwordx4 v[142:145], v44, s[14:15] offset:192
	v_mov_b32_e32 v20, v102
	s_nop 1
	v_permlane32_swap_b32_e32 v102, v20
	v_add_f32_e32 v20, v102, v20
	v_fmamk_f32 v20, v20, 0x3c000000, v1
	v_mul_f32_e32 v24, 0x4f800000, v20
	v_cmp_gt_f32_e32 vcc, s2, v20
	v_mov_b32_e32 v102, v26
	v_mov_b32_e32 v103, v10
	v_cndmask_b32_e32 v31, v20, v24, vcc
	v_sqrt_f32_e32 v33, v31
	v_mov_b32_e32 v24, v18
	v_mov_b32_e32 v20, v25
	v_add_u32_e32 v18, -1, v33
	v_fma_f32 v25, -v18, v33, v31
	v_cmp_ge_f32_e64 s[2:3], 0, v25
	v_add_u32_e32 v25, 1, v33
	s_nop 0
	v_cndmask_b32_e64 v18, v33, v18, s[2:3]
	v_fma_f32 v33, -v25, v33, v31
	v_cmp_lt_f32_e64 s[2:3], 0, v33
	s_nop 1
	v_cndmask_b32_e64 v18, v18, v25, s[2:3]
	v_mul_f32_e32 v25, 0x37800000, v18
	v_cndmask_b32_e32 v18, v18, v25, vcc
	v_cmp_class_f32_e32 vcc, v31, v174
	v_mov_b32_e32 v25, v22
	s_nop 0
	v_cndmask_b32_e32 v18, v18, v31, vcc
	v_div_scale_f32 v31, s[2:3], v18, v18, 1.0
	v_rcp_f32_e32 v33, v31
	s_nop 0
	v_fma_f32 v22, -v31, v33, 1.0
	v_fmac_f32_e32 v33, v22, v33
	v_div_scale_f32 v22, vcc, 1.0, v18, 1.0
	v_mul_f32_e32 v35, v22, v33
	v_fma_f32 v45, -v31, v35, v22
	v_fmac_f32_e32 v35, v45, v33
	v_fma_f32 v22, -v31, v35, v22
	v_div_fmas_f32 v22, v22, v33, v35
	v_div_fixup_f32 v18, v22, v18, 1.0
	v_pk_mul_f32 v[98:99], v[18:19], v[98:99] op_sel_hi:[0,1]
	v_mov_b32_e32 v22, v19
	v_pk_mul_f32 v[98:99], v[98:99], v[22:23]
	v_pk_mul_f32 v[22:23], v[18:19], v[122:123] op_sel_hi:[0,1]
	v_pk_mul_f32 v[122:123], v[22:23], v[124:125]
	v_pk_mul_f32 v[22:23], v[18:19], v[126:127] op_sel_hi:[0,1]
	v_pk_mul_f32 v[124:125], v[22:23], v[20:21]
	v_pk_mul_f32 v[20:21], v[18:19], v[110:111] op_sel_hi:[0,1]
	v_pk_mul_f32 v[110:111], v[20:21], v[120:121]
	v_pk_mul_f32 v[20:21], v[18:19], v[104:105] op_sel_hi:[0,1]
	v_pk_mul_f32 v[104:105], v[20:21], v[14:15]
	v_pk_mul_f32 v[14:15], v[18:19], v[114:115] op_sel_hi:[0,1]
	v_pk_mul_f32 v[128:129], v[18:19], v[128:129] op_sel_hi:[0,1]
	v_pk_mul_f32 v[114:115], v[14:15], v[118:119]
	v_pk_mul_f32 v[14:15], v[18:19], v[116:117] op_sel_hi:[0,1]
	v_pk_mul_f32 v[24:25], v[24:25], v[128:129]
	v_pk_mul_f32 v[116:117], v[14:15], v[16:17]
	v_mov_b32_e32 v14, v10
	v_mov_b32_e32 v15, v26
	v_pk_mul_f32 v[14:15], v[14:15], v[24:25]
	v_mov_b32_e32 v26, v11
	v_sub_f32_e32 v19, v15, v14
	v_pk_mul_f32 v[14:15], v[26:27], v[98:99]
	v_mov_b32_e32 v10, v27
	v_sub_f32_e32 v31, v15, v14
	v_pk_mul_f32 v[14:15], v[102:103], v[24:25]
	v_pk_mul_f32 v[10:11], v[10:11], v[98:99]
	v_add_f32_e32 v33, v14, v15
	global_load_dwordx4 v[14:17], v[76:77], off offset:80
	global_load_dwordx4 v[20:23], v[76:77], off offset:64
	global_load_dwordx4 v[24:27], v[78:79], off offset:64
	v_add_f32_e32 v10, v10, v11
	v_cvt_pk_bf16_f32 v98, v33, v10
	v_mov_b32_e32 v10, v28
	v_mov_b32_e32 v11, v12
	v_pk_mul_f32 v[10:11], v[10:11], v[122:123]
	v_mov_b32_e32 v12, v29
	v_cvt_pk_bf16_f32 v102, v19, v31
	v_sub_f32_e32 v19, v10, v11
	v_pk_mul_f32 v[10:11], v[12:13], v[124:125]
	v_mov_b32_e32 v28, v13
	v_sub_f32_e32 v12, v10, v11
	v_pk_mul_f32 v[10:11], v[100:101], v[122:123]
	v_cvt_pk_bf16_f32 v103, v19, v12
	s_waitcnt vmcnt(3)
	v_mov_b32_e32 v13, v144
	v_add_f32_e32 v31, v10, v11
	v_pk_mul_f32 v[10:11], v[28:29], v[124:125]
	v_mov_b32_e32 v144, v137
	v_add_f32_e32 v10, v10, v11
	v_cvt_pk_bf16_f32 v99, v31, v10
	v_mov_b32_e32 v10, v2
	v_mov_b32_e32 v11, v6
	v_pk_mul_f32 v[10:11], v[10:11], v[110:111]
	v_mov_b32_e32 v6, v3
	v_mov_b32_e32 v2, v7
	v_sub_f32_e32 v12, v10, v11
	v_pk_mul_f32 v[10:11], v[6:7], v[104:105]
	v_pk_mul_f32 v[2:3], v[2:3], v[104:105]
	v_sub_f32_e32 v6, v10, v11
	v_pk_mul_f32 v[10:11], v[106:107], v[110:111]
	v_add_f32_e32 v2, v2, v3
	v_add_f32_e32 v10, v10, v11
	v_cvt_pk_bf16_f32 v100, v10, v2
	v_mov_b32_e32 v2, v4
	v_mov_b32_e32 v3, v8
	v_pk_mul_f32 v[2:3], v[2:3], v[114:115]
	v_mov_b32_e32 v8, v5
	v_cvt_pk_bf16_f32 v104, v12, v6
	v_sub_f32_e32 v4, v2, v3
	v_pk_mul_f32 v[2:3], v[8:9], v[116:117]
	global_load_dwordx4 v[6:9], v[96:97], off offset:16
	v_sub_f32_e32 v5, v2, v3
	v_pk_mul_f32 v[2:3], v[112:113], v[114:115]
	v_mov_b32_e32 v12, v136
	v_add_f32_e32 v10, v2, v3
	v_pk_mul_f32 v[2:3], v[108:109], v[116:117]
	v_cvt_pk_bf16_f32 v105, v4, v5
	v_mov_b32_e32 v4, v134
	v_add_f32_e32 v2, v2, v3
	v_cvt_pk_bf16_f32 v101, v10, v2
	v_pk_mul_f32 v[10:11], v[18:19], v[90:91] op_sel_hi:[0,1]
	v_pk_mul_f32 v[28:29], v[10:11], v[12:13]
	v_pk_mul_f32 v[10:11], v[18:19], v[88:89] op_sel_hi:[0,1]
	v_pk_mul_f32 v[96:97], v[10:11], v[144:145]
	v_pk_mul_f32 v[10:11], v[18:19], v[86:87] op_sel_hi:[0,1]
	v_mov_b32_e32 v12, v130
	v_mov_b32_e32 v13, v138
	v_pk_mul_f32 v[2:3], v[18:19], v[92:93] op_sel_hi:[0,1]
	v_mov_b32_e32 v5, v142
	v_pk_mul_f32 v[108:109], v[10:11], v[12:13]
	v_mov_b32_e32 v13, v140
	v_pk_mul_f32 v[88:89], v[18:19], v[80:81] op_sel_hi:[0,1]
	v_mov_b32_e32 v140, v133
	v_pk_mul_f32 v[2:3], v[2:3], v[4:5]
	v_pk_mul_f32 v[116:117], v[88:89], v[140:141]
	v_pk_mul_f32 v[4:5], v[18:19], v[94:95] op_sel_hi:[0,1]
	v_mov_b32_e32 v142, v135
	v_pk_mul_f32 v[10:11], v[18:19], v[84:85] op_sel_hi:[0,1]
	v_mov_b32_e32 v138, v131
	v_pk_mul_f32 v[4:5], v[4:5], v[142:143]
	v_pk_mul_f32 v[112:113], v[10:11], v[138:139]
	v_pk_mul_f32 v[10:11], v[18:19], v[82:83] op_sel_hi:[0,1]
	v_mov_b32_e32 v12, v132
	v_pk_mul_f32 v[114:115], v[10:11], v[12:13]
	global_load_dwordx4 v[10:13], v44, s[14:15] offset:272
	global_load_dwordx4 v[76:79], v44, s[14:15] offset:256
	global_load_dwordx4 v[80:83], v44, s[14:15] offset:400
	global_load_dwordx4 v[84:87], v44, s[14:15] offset:384
	v_add_co_u32_e32 v118, vcc, s4, v58
	s_waitcnt vmcnt(6)
; __device__ __forceinline__ unsigned pk2(float lo, float hi) { unsigned r; asm("v_cvt_pk_bf16_f32 %0, %1, %2" : "=v"(r) : "v"(lo), "v"(hi)); return r; }
; __device__ __forceinline__ void attn_dma_body(const bf16_t* __restrict__ Qb, int ldq, int tpos0, const float* __restrict__ rope, const float* __restrict__ qgain, ...
;     ...
;     for (int ax = 0; ax < 2; ++ax) { const int pos = ax ? (t & 63) : (t >> 6);
; #pragma unroll
;       for (int q = 0; q < 2; ++q) { const int dl = 4 * ax + q, dh = dl + 2, p0 = q * 16 + 8 * hi;
;         const float* cp_ = rope + pos * 32 + p0; const float* gl = qgain + dl * 16 + 8 * hi; const float* gh = qgain + dh * 16 + 8 * hi;
;         float cs[8], sn[8], lo[8], hv[8];
; #pragma unroll
;         for (int i = 0; i < 8; ++i) { cs[i] = cp_[i]; sn[i] = cp_[4096 + i];
;           lo[i] = bf2f((unsigned)(unsigned short)qr[dl][i]) * rinv * gl[i]; hv[i] = bf2f((unsigned)(unsigned short)qr[dh][i]) * rinv * gh[i]; }
;         u32x4 wl, wh;
; #pragma unroll
;         for (int i = 0; i < 4; ++i) { const float l0 = lo[2 * i] * cs[2 * i] - hv[2 * i] * sn[2 * i], l1 = lo[2 * i + 1] * cs[2 * i + 1] - hv[2 * i + 1] * sn[2 * i + 1];
;           const float h0 = hv[2 * i] * cs[2 * i] + lo[2 * i] * sn[2 * i], h1 = hv[2 * i + 1] * cs[2 * i + 1] + lo[2 * i + 1] * sn[2 * i + 1];
;           wl[i] = pk2(l0, l1); wh[i] = pk2(h0, h1); }
;         qr[dl] = *reinterpret_cast<bf16x8*>(&wl); qr[dh] = *reinterpret_cast<bf16x8*>(&wh); } } }
	v_mov_b32_e32 v88, v20
	s_waitcnt vmcnt(5)
	v_mov_b32_e32 v89, v24
	v_pk_mul_f32 v[88:89], v[88:89], v[2:3]
	v_addc_co_u32_e32 v119, vcc, 0, v59, vcc
	v_sub_f32_e32 v19, v88, v89
	v_mov_b32_e32 v88, v21
	v_mov_b32_e32 v89, v25
	v_pk_mul_f32 v[88:89], v[88:89], v[4:5]
	s_nop 0
	v_sub_f32_e32 v31, v88, v89
	v_mov_b32_e32 v88, v24
	v_mov_b32_e32 v89, v20
	v_pk_mul_f32 v[2:3], v[88:89], v[2:3]
	v_mov_b32_e32 v20, v25
	v_add_f32_e32 v24, v2, v3
	v_pk_mul_f32 v[2:3], v[20:21], v[4:5]
	v_cvt_pk_bf16_f32 v110, v19, v31
	s_nop 0
	v_add_f32_e32 v2, v2, v3
	v_cvt_pk_bf16_f32 v106, v24, v2
	v_mov_b32_e32 v2, v22
	v_mov_b32_e32 v3, v26
	v_pk_mul_f32 v[2:3], v[2:3], v[28:29]
	s_nop 0
	v_sub_f32_e32 v19, v2, v3
	v_mov_b32_e32 v2, v23
	v_mov_b32_e32 v3, v27
	v_pk_mul_f32 v[20:21], v[2:3], v[96:97]
	global_load_dwordx4 v[2:5], v[58:59], off offset:16
	global_load_dwordx4 v[88:91], v[58:59], off
	global_load_dwordx4 v[92:95], v[118:119], off
	v_sub_f32_e32 v24, v20, v21
	v_mov_b32_e32 v20, v26
	v_mov_b32_e32 v21, v22
	v_pk_mul_f32 v[20:21], v[20:21], v[28:29]
	v_mov_b32_e32 v22, v27
	v_add_f32_e32 v25, v20, v21
	v_pk_mul_f32 v[20:21], v[22:23], v[96:97]
	v_cvt_pk_bf16_f32 v111, v19, v24
	s_nop 0
	v_add_f32_e32 v20, v20, v21
	v_cvt_pk_bf16_f32 v107, v25, v20
	v_mov_b32_e32 v20, v14
	s_waitcnt vmcnt(7)
	v_mov_b32_e32 v21, v6
	v_pk_mul_f32 v[20:21], v[20:21], v[108:109]
	s_nop 0
	v_sub_f32_e32 v19, v20, v21
	v_mov_b32_e32 v20, v15
	v_mov_b32_e32 v21, v7
	v_pk_mul_f32 v[20:21], v[20:21], v[112:113]
	s_nop 0
	v_sub_f32_e32 v22, v20, v21
	v_mov_b32_e32 v21, v14
	v_mov_b32_e32 v14, v7
	v_mov_b32_e32 v20, v6
	v_pk_mul_f32 v[6:7], v[14:15], v[112:113]
	v_pk_mul_f32 v[20:21], v[20:21], v[108:109]
	v_add_f32_e32 v6, v6, v7
	v_add_f32_e32 v20, v20, v21
	v_cvt_pk_bf16_f32 v108, v20, v6
	v_mov_b32_e32 v6, v16
	v_mov_b32_e32 v7, v8
	v_cvt_pk_bf16_f32 v112, v19, v22
	v_pk_mul_f32 v[6:7], v[6:7], v[114:115]
	global_load_dwordx4 v[20:23], v[74:75], off offset:16
	v_sub_f32_e32 v14, v6, v7
	v_mov_b32_e32 v6, v17
	v_mov_b32_e32 v7, v9
	v_pk_mul_f32 v[6:7], v[6:7], v[116:117]
	s_nop 0
	v_sub_f32_e32 v15, v6, v7
	v_mov_b32_e32 v6, v8
	v_mov_b32_e32 v7, v16
	v_pk_mul_f32 v[6:7], v[6:7], v[114:115]
	v_mov_b32_e32 v16, v9
	v_add_f32_e32 v8, v6, v7
	v_pk_mul_f32 v[6:7], v[16:17], v[116:117]
	s_waitcnt vmcnt(4)
	v_mov_b32_e32 v9, v84
	v_add_f32_e32 v6, v6, v7
	v_cvt_pk_bf16_f32 v109, v8, v6
	v_pk_mul_f32 v[6:7], v[18:19], v[72:73] op_sel_hi:[0,1]
	v_mov_b32_e32 v8, v76
	v_pk_mul_f32 v[28:29], v[6:7], v[8:9]
	v_pk_mul_f32 v[6:7], v[18:19], v[70:71] op_sel_hi:[0,1]
	v_mov_b32_e32 v84, v77
	v_pk_mul_f32 v[70:71], v[6:7], v[84:85]
	v_pk_mul_f32 v[6:7], v[18:19], v[68:69] op_sel_hi:[0,1]
	v_mov_b32_e32 v8, v78
	v_mov_b32_e32 v9, v86
	v_pk_mul_f32 v[72:73], v[6:7], v[8:9]
	v_pk_mul_f32 v[6:7], v[18:19], v[66:67] op_sel_hi:[0,1]
	v_mov_b32_e32 v86, v79
	v_pk_mul_f32 v[74:75], v[6:7], v[86:87]
	v_pk_mul_f32 v[6:7], v[18:19], v[64:65] op_sel_hi:[0,1]
	v_mov_b32_e32 v8, v10
	v_mov_b32_e32 v9, v80
	v_pk_mul_f32 v[76:77], v[6:7], v[8:9]
	v_pk_mul_f32 v[6:7], v[18:19], v[62:63] op_sel_hi:[0,1]
	v_mov_b32_e32 v80, v11
	v_pk_mul_f32 v[10:11], v[18:19], v[60:61] op_sel_hi:[0,1]
	v_mov_b32_e32 v64, v12
	v_mov_b32_e32 v65, v82
	v_cvt_pk_bf16_f32 v113, v14, v15
	v_pk_mul_f32 v[78:79], v[6:7], v[80:81]
	global_load_dwordx4 v[6:9], v44, s[14:15] offset:336
	global_load_dwordx4 v[14:17], v44, s[14:15] offset:320
	global_load_dwordx4 v[24:27], v44, s[14:15] offset:464
	global_load_dwordx4 v[60:63], v44, s[14:15] offset:448
	v_pk_mul_f32 v[44:45], v[10:11], v[64:65]
	v_pk_mul_f32 v[10:11], v[18:19], v[54:55] op_sel_hi:[0,1]
	v_mov_b32_e32 v82, v13
	v_pk_mul_f32 v[80:81], v[10:11], v[82:83]
	s_waitcnt vmcnt(6)
	v_mov_b32_e32 v54, v88
	s_waitcnt vmcnt(5)
	v_mov_b32_e32 v55, v92
	v_pk_mul_f32 v[54:55], v[54:55], v[28:29]
	global_load_dwordx4 v[10:13], v[118:119], off offset:64
	v_sub_f32_e32 v19, v54, v55
	v_mov_b32_e32 v54, v89
	v_mov_b32_e32 v55, v93
	v_pk_mul_f32 v[54:55], v[54:55], v[70:71]
	s_nop 0
	v_sub_f32_e32 v31, v54, v55
	v_mov_b32_e32 v54, v92
	v_mov_b32_e32 v55, v88
	v_pk_mul_f32 v[28:29], v[54:55], v[28:29]
	v_mov_b32_e32 v88, v93
	v_add_f32_e32 v33, v28, v29
	v_pk_mul_f32 v[28:29], v[88:89], v[70:71]
	global_load_dwordx4 v[64:67], v[58:59], off offset:80
	global_load_dwordx4 v[68:71], v[58:59], off offset:64
	v_add_f32_e32 v28, v28, v29
	global_load_dwordx4 v[54:57], v[56:57], off offset:16
	v_cvt_pk_bf16_f32 v114, v33, v28
	v_mov_b32_e32 v28, v90
	v_mov_b32_e32 v29, v94
	v_pk_mul_f32 v[28:29], v[28:29], v[72:73]
	v_cvt_pk_bf16_f32 v118, v19, v31
	s_nop 0
	v_sub_f32_e32 v19, v28, v29
	v_mov_b32_e32 v28, v91
	v_mov_b32_e32 v29, v95
	v_pk_mul_f32 v[28:29], v[28:29], v[74:75]
	s_nop 0
	v_sub_f32_e32 v31, v28, v29
	v_mov_b32_e32 v28, v94
	v_mov_b32_e32 v29, v90
	v_pk_mul_f32 v[28:29], v[28:29], v[72:73]
	v_mov_b32_e32 v90, v95
	v_add_f32_e32 v33, v28, v29
	v_pk_mul_f32 v[28:29], v[90:91], v[74:75]
	v_cvt_pk_bf16_f32 v119, v19, v31
	s_nop 0
	v_add_f32_e32 v28, v28, v29
	v_cvt_pk_bf16_f32 v115, v33, v28
	v_mov_b32_e32 v28, v2
	s_waitcnt vmcnt(8)
; __device__ __forceinline__ unsigned pk2(float lo, float hi) { unsigned r; asm("v_cvt_pk_bf16_f32 %0, %1, %2" : "=v"(r) : "v"(lo), "v"(hi)); return r; }
; __device__ __forceinline__ void attn_dma_body(const bf16_t* __restrict__ Qb, int ldq, int tpos0, const float* __restrict__ rope, const float* __restrict__ qgain, ...
;     ...
;     for (int ax = 0; ax < 2; ++ax) { const int pos = ax ? (t & 63) : (t >> 6);
; #pragma unroll
;       for (int q = 0; q < 2; ++q) { const int dl = 4 * ax + q, dh = dl + 2, p0 = q * 16 + 8 * hi;
;         const float* cp_ = rope + pos * 32 + p0; const float* gl = qgain + dl * 16 + 8 * hi; const float* gh = qgain + dh * 16 + 8 * hi;
;         float cs[8], sn[8], lo[8], hv[8];
; #pragma unroll
;         for (int i = 0; i < 8; ++i) { cs[i] = cp_[i]; sn[i] = cp_[4096 + i];
;           lo[i] = bf2f((unsigned)(unsigned short)qr[dl][i]) * rinv * gl[i]; hv[i] = bf2f((unsigned)(unsigned short)qr[dh][i]) * rinv * gh[i]; }
;         u32x4 wl, wh;
; #pragma unroll
;         for (int i = 0; i < 4; ++i) { const float l0 = lo[2 * i] * cs[2 * i] - hv[2 * i] * sn[2 * i], l1 = lo[2 * i + 1] * cs[2 * i + 1] - hv[2 * i + 1] * sn[2 * i + 1];
;           const float h0 = hv[2 * i] * cs[2 * i] + lo[2 * i] * sn[2 * i], h1 = hv[2 * i + 1] * cs[2 * i + 1] + lo[2 * i + 1] * sn[2 * i + 1];
;           wl[i] = pk2(l0, l1); wh[i] = pk2(h0, h1); }
;         qr[dl] = *reinterpret_cast<bf16x8*>(&wl); qr[dh] = *reinterpret_cast<bf16x8*>(&wh); } } }
	v_mov_b32_e32 v29, v20
	v_pk_mul_f32 v[28:29], v[28:29], v[76:77]
	s_nop 0
	v_sub_f32_e32 v19, v28, v29
	v_mov_b32_e32 v28, v3
	v_mov_b32_e32 v29, v21
	v_pk_mul_f32 v[28:29], v[28:29], v[78:79]
	s_nop 0
	v_sub_f32_e32 v31, v28, v29
	v_mov_b32_e32 v29, v2
	v_mov_b32_e32 v2, v21
	v_mov_b32_e32 v28, v20
	v_pk_mul_f32 v[2:3], v[2:3], v[78:79]
	v_pk_mul_f32 v[28:29], v[28:29], v[76:77]
	v_add_f32_e32 v2, v2, v3
	v_add_f32_e32 v20, v28, v29
	v_cvt_pk_bf16_f32 v116, v20, v2
	v_mov_b32_e32 v2, v4
	v_mov_b32_e32 v3, v22
	v_pk_mul_f32 v[2:3], v[2:3], v[44:45]
	v_cvt_pk_bf16_f32 v120, v19, v31
	s_nop 0
	v_sub_f32_e32 v19, v2, v3
	v_mov_b32_e32 v2, v5
	v_mov_b32_e32 v3, v23
	v_pk_mul_f32 v[2:3], v[2:3], v[80:81]
	s_nop 0
	v_sub_f32_e32 v20, v2, v3
	v_mov_b32_e32 v2, v22
	v_mov_b32_e32 v3, v4
	v_pk_mul_f32 v[2:3], v[2:3], v[44:45]
	v_mov_b32_e32 v4, v23
	v_add_f32_e32 v21, v2, v3
	v_pk_mul_f32 v[2:3], v[4:5], v[80:81]
	v_cvt_pk_bf16_f32 v121, v19, v20
	s_waitcnt vmcnt(6)
	v_mov_b32_e32 v4, v14
	v_add_f32_e32 v2, v2, v3
	v_cvt_pk_bf16_f32 v117, v21, v2
	s_waitcnt vmcnt(4)
	v_mov_b32_e32 v5, v60
	v_mov_b32_e32 v60, v15
	v_pk_mul_f32 v[14:15], v[18:19], v[48:49] op_sel_hi:[0,1]
	v_mov_b32_e32 v20, v16
	v_mov_b32_e32 v21, v62
	v_pk_mul_f32 v[14:15], v[14:15], v[20:21]
	v_pk_mul_f32 v[20:21], v[18:19], v[46:47] op_sel_hi:[0,1]
	v_mov_b32_e32 v62, v17
	v_pk_mul_f32 v[16:17], v[20:21], v[62:63]
	v_pk_mul_f32 v[20:21], v[18:19], v[42:43] op_sel_hi:[0,1]
	v_mov_b32_e32 v22, v6
	v_mov_b32_e32 v23, v24
	v_pk_mul_f32 v[2:3], v[18:19], v[52:53] op_sel_hi:[0,1]
	v_pk_mul_f32 v[20:21], v[20:21], v[22:23]
	v_pk_mul_f32 v[22:23], v[18:19], v[40:41] op_sel_hi:[0,1]
	v_mov_b32_e32 v24, v7
	v_pk_mul_f32 v[2:3], v[2:3], v[4:5]
	v_pk_mul_f32 v[4:5], v[18:19], v[50:51] op_sel_hi:[0,1]
	v_pk_mul_f32 v[6:7], v[22:23], v[24:25]
	v_pk_mul_f32 v[22:23], v[18:19], v[38:39] op_sel_hi:[0,1]
	v_mov_b32_e32 v25, v26
	v_pk_mul_f32 v[18:19], v[18:19], v[36:37] op_sel_hi:[0,1]
	v_mov_b32_e32 v26, v9
	v_mov_b32_e32 v24, v8
	v_pk_mul_f32 v[8:9], v[18:19], v[26:27]
	s_waitcnt vmcnt(1)
	v_mov_b32_e32 v18, v68
	v_mov_b32_e32 v19, v10
	v_pk_mul_f32 v[18:19], v[18:19], v[2:3]
	v_pk_mul_f32 v[4:5], v[4:5], v[60:61]
	v_pk_mul_f32 v[22:23], v[22:23], v[24:25]
	v_sub_f32_e32 v24, v18, v19
	v_mov_b32_e32 v18, v69
	v_mov_b32_e32 v19, v11
	v_pk_mul_f32 v[18:19], v[18:19], v[4:5]
	s_nop 0
	v_sub_f32_e32 v25, v18, v19
	v_mov_b32_e32 v18, v10
	v_mov_b32_e32 v19, v68
	v_pk_mul_f32 v[2:3], v[18:19], v[2:3]
	v_mov_b32_e32 v68, v11
	v_add_f32_e32 v10, v2, v3
	v_pk_mul_f32 v[2:3], v[68:69], v[4:5]
	v_cvt_pk_bf16_f32 v126, v24, v25
	s_nop 0
	v_add_f32_e32 v2, v2, v3
	v_cvt_pk_bf16_f32 v122, v10, v2
	v_mov_b32_e32 v2, v70
	v_mov_b32_e32 v3, v12
	v_pk_mul_f32 v[2:3], v[2:3], v[14:15]
	s_nop 0
	v_sub_f32_e32 v4, v2, v3
	v_mov_b32_e32 v2, v71
	v_mov_b32_e32 v3, v13
	v_pk_mul_f32 v[2:3], v[2:3], v[16:17]
	s_nop 0
	v_sub_f32_e32 v5, v2, v3
	v_mov_b32_e32 v2, v12
	v_mov_b32_e32 v3, v70
	v_pk_mul_f32 v[2:3], v[2:3], v[14:15]
	v_mov_b32_e32 v70, v13
	v_add_f32_e32 v10, v2, v3
	v_pk_mul_f32 v[2:3], v[70:71], v[16:17]
	v_cvt_pk_bf16_f32 v127, v4, v5
	s_nop 0
	v_add_f32_e32 v2, v2, v3
	v_cvt_pk_bf16_f32 v123, v10, v2
	v_mov_b32_e32 v2, v64
	s_waitcnt vmcnt(0)
	v_mov_b32_e32 v3, v54
	v_pk_mul_f32 v[2:3], v[2:3], v[20:21]
	s_nop 0
	v_sub_f32_e32 v4, v2, v3
	v_mov_b32_e32 v2, v65
	v_mov_b32_e32 v3, v55
	v_pk_mul_f32 v[2:3], v[2:3], v[6:7]
	s_nop 0
	v_sub_f32_e32 v5, v2, v3
	v_mov_b32_e32 v2, v54
	v_mov_b32_e32 v3, v64
	v_pk_mul_f32 v[2:3], v[2:3], v[20:21]
	v_mov_b32_e32 v64, v55
	v_add_f32_e32 v10, v2, v3
	v_pk_mul_f32 v[2:3], v[64:65], v[6:7]
	v_cvt_pk_bf16_f32 v128, v4, v5
	s_nop 0
	v_add_f32_e32 v2, v2, v3
	v_cvt_pk_bf16_f32 v124, v10, v2
	v_mov_b32_e32 v2, v66
	v_mov_b32_e32 v3, v56
	v_pk_mul_f32 v[2:3], v[2:3], v[22:23]
	s_nop 0
	v_sub_f32_e32 v4, v2, v3
	v_mov_b32_e32 v2, v67
	v_mov_b32_e32 v3, v57
	v_pk_mul_f32 v[2:3], v[2:3], v[8:9]
	s_nop 0
	v_sub_f32_e32 v5, v2, v3
	v_mov_b32_e32 v2, v56
	v_mov_b32_e32 v3, v66
	v_pk_mul_f32 v[2:3], v[2:3], v[22:23]
	v_mov_b32_e32 v66, v57
	v_add_f32_e32 v6, v2, v3
	v_pk_mul_f32 v[2:3], v[66:67], v[8:9]
	v_cvt_pk_bf16_f32 v129, v4, v5
	s_nop 0
	v_add_f32_e32 v2, v2, v3
	v_cvt_pk_bf16_f32 v125, v6, v2

; __device__ __forceinline__ unsigned cvt_pk_bf16(float lo, float hi) { unsigned r; asm volatile("v_cvt_pk_bf16_f32 %0, %1, %2" : "=v"(r) : "v"(lo), "v"(hi)); return r; }
; __device__ __forceinline__ float silu_f(float x) { return x / (1.0f + __expf(-x)); }
;     __device__ __forceinline__ void operator()(const f32x4 (&acc)[2][2][4][2], const Unit& u, int wr, int wc, int fr, int fq) const {
;         const int row0 = u.pm * BM + wr * 64 + fr, col0 = u.pn * HALF + wc * 32 + 8 * fq;
; #pragma unroll
;         for (int ai = 0; ai < 2; ++ai)
; #pragma unroll
;             for (int m = 0; m < 4; ++m) { bf16_t* rowp = ACT + (size_t)(row0 + ai * HALF + m * 16) * DE + col0;
;                 float v[8];
; #pragma unroll
;                 for (int n = 0; n < 2; ++n)
; #pragma unroll
;                     for (int j = 0; j < 4; ++j) v[n * 4 + j] = silu_f(acc[ai][0][m][n][j]) * acc[ai][1][m][n][j];
;                 v4u w; w.x = cvt_pk_bf16(v[0], v[1]); w.y = cvt_pk_bf16(v[2], v[3]); w.z = cvt_pk_bf16(v[4], v[5]); w.w = cvt_pk_bf16(v[6], v[7]);
;                 asm volatile("global_store_dwordx4 %0, %1, off sc1\n\ts_nop 1" :: "v"(rowp), "v"(w) : "memory"); }
.LBB0_895:
	v_mul_f32_e32 v138, 0xbfb8aa3b, v126
	v_exp_f32_e32 v138, v138
	v_lshl_add_u32 v142, s74, 8, v145
	v_ashrrev_i32_e32 v143, 31, v142
	v_lshlrev_b64 v[148:149], 11, v[142:143]
	v_add_f32_e32 v138, 1.0, v138
	v_mul_f32_e32 v152, 0xbfb8aa3b, v127
	v_exp_f32_e32 v152, v152
	v_lshl_or_b32 v146, s77, 7, v158
	v_add_f32_e32 v144, 1.0, v152
	v_rcp_f32_e32 v143, v138
	s_nop 0
	v_mul_f32_e32 v126, v126, v143
	v_mul_f32_e32 v143, 0xbfb8aa3b, v128
	v_exp_f32_e32 v143, v143
	v_mul_f32_e32 v122, v126, v122
	v_add_f32_e32 v143, 1.0, v143
	v_rcp_f32_e32 v126, v144
	v_mul_f32_e32 v138, 0xbfb8aa3b, v129
	v_mul_f32_e32 v126, v127, v126
	v_exp_f32_e32 v138, v138
	v_mul_f32_e32 v123, v126, v123
	v_add_f32_e32 v138, 1.0, v138
	v_rcp_f32_e32 v126, v143
	s_nop 0
	v_mul_f32_e32 v126, v128, v126
	v_mul_f32_e32 v128, 0xbfb8aa3b, v118
	v_exp_f32_e32 v128, v128
	v_mul_f32_e32 v124, v126, v124
	v_add_f32_e32 v128, 1.0, v128
	v_rcp_f32_e32 v126, v138
	s_nop 0
	v_mul_f32_e32 v126, v129, v126
	v_mul_f32_e32 v129, 0xbfb8aa3b, v119
	v_exp_f32_e32 v129, v129
	v_mul_f32_e32 v125, v126, v125
	v_add_f32_e32 v129, 1.0, v129
	v_rcp_f32_e32 v126, v128
	v_mul_f32_e32 v127, 0xbfb8aa3b, v120
	v_mul_f32_e32 v118, v118, v126
	v_exp_f32_e32 v127, v127
	v_mul_f32_e32 v126, v118, v114
	v_add_f32_e32 v127, 1.0, v127
	v_rcp_f32_e32 v114, v129
	v_mul_f32_e32 v118, 0xbfb8aa3b, v121
	v_mul_f32_e32 v114, v119, v114
	v_exp_f32_e32 v118, v118
	v_mul_f32_e32 v129, v114, v115
	v_add_f32_e32 v118, 1.0, v118
	v_rcp_f32_e32 v114, v127
	s_nop 0
	v_mul_f32_e32 v114, v120, v114
	v_mul_f32_e32 v127, v114, v116
	v_rcp_f32_e32 v114, v118
	s_nop 0
	v_mul_f32_e32 v114, v121, v114
	v_cvt_pk_bf16_f32 v118, v122, v123
	v_mul_f32_e32 v122, 0xbfb8aa3b, v110
	v_exp_f32_e32 v122, v122
	v_ashrrev_i32_e32 v147, 31, v146
	v_lshl_add_u64 v[148:149], s[16:17], 0, v[148:149]
	v_mul_f32_e32 v121, v114, v117
	v_lshlrev_b64 v[116:117], 1, v[146:147]
	v_cvt_pk_bf16_f32 v119, v124, v125
	v_cvt_pk_bf16_f32 v120, v126, v129
	v_lshl_add_u64 v[114:115], v[148:149], 0, v[116:117]
	v_cvt_pk_bf16_f32 v121, v127, v121
	v_mul_f32_e32 v125, 0xbfb8aa3b, v111
	global_store_dwordx4 v[114:115], v[118:121], off sc1
	s_nop 1
	v_add_f32_e32 v120, 1.0, v122
	v_exp_f32_e32 v125, v125
	v_or_b32_e32 v118, 16, v142
	v_ashrrev_i32_e32 v119, 31, v118
	v_add_f32_e32 v123, 1.0, v125
	v_rcp_f32_e32 v121, v120
	s_nop 0
	v_mul_f32_e32 v110, v110, v121
	v_mul_f32_e32 v121, 0xbfb8aa3b, v112
	v_exp_f32_e32 v121, v121
	v_mul_f32_e32 v106, v110, v106
	v_add_f32_e32 v121, 1.0, v121
	v_rcp_f32_e32 v110, v123
	s_nop 0
	v_mul_f32_e32 v110, v111, v110
	v_mul_f32_e32 v120, 0xbfb8aa3b, v113
	v_mul_f32_e32 v107, v110, v107
	v_exp_f32_e32 v120, v120
	s_nop 0
	v_add_f32_e32 v120, 1.0, v120
	v_rcp_f32_e32 v110, v121
	s_nop 0
	v_mul_f32_e32 v110, v112, v110
	v_mul_f32_e32 v112, 0xbfb8aa3b, v102
	v_exp_f32_e32 v112, v112
	v_mul_f32_e32 v108, v110, v108
	v_add_f32_e32 v112, 1.0, v112
	v_rcp_f32_e32 v110, v120
	s_nop 0
	v_mul_f32_e32 v110, v113, v110
	v_mul_f32_e32 v113, 0xbfb8aa3b, v103
	v_exp_f32_e32 v113, v113
	v_mul_f32_e32 v109, v110, v109
	v_add_f32_e32 v113, 1.0, v113
	v_rcp_f32_e32 v110, v112
	v_mul_f32_e32 v111, 0xbfb8aa3b, v104
	v_mul_f32_e32 v102, v102, v110
	v_exp_f32_e32 v111, v111
	v_mul_f32_e32 v110, v102, v98
	v_add_f32_e32 v111, 1.0, v111
	v_rcp_f32_e32 v98, v113
	v_mul_f32_e32 v102, 0xbfb8aa3b, v105
	v_mul_f32_e32 v98, v103, v98
	v_exp_f32_e32 v102, v102
	v_mul_f32_e32 v113, v98, v99
	v_add_f32_e32 v102, 1.0, v102
	v_rcp_f32_e32 v98, v111
	s_nop 0
	v_mul_f32_e32 v98, v104, v98
	v_mul_f32_e32 v104, v98, v100
	v_rcp_f32_e32 v98, v102
	s_nop 0
	v_mul_f32_e32 v98, v105, v98
	v_mul_f32_e32 v105, 0xbfb8aa3b, v94
	v_exp_f32_e32 v105, v105
	v_lshlrev_b64 v[118:119], 11, v[118:119]
	v_lshl_add_u64 v[118:119], s[16:17], 0, v[118:119]
	v_mul_f32_e32 v101, v98, v101
	v_cvt_pk_bf16_f32 v98, v106, v107
	v_cvt_pk_bf16_f32 v99, v108, v109
	v_cvt_pk_bf16_f32 v100, v110, v113
	v_lshl_add_u64 v[102:103], v[118:119], 0, v[116:117]
	v_cvt_pk_bf16_f32 v101, v104, v101
	s_nop 0
	global_store_dwordx4 v[102:103], v[98:101], off sc1
	s_nop 1
	v_add_f32_e32 v100, 1.0, v105
	v_mul_f32_e32 v105, 0xbfb8aa3b, v95
	v_exp_f32_e32 v105, v105
	v_or_b32_e32 v98, 32, v142
	v_add_f32_e32 v103, 1.0, v105
	v_rcp_f32_e32 v101, v100
	s_nop 0
	v_mul_f32_e32 v94, v94, v101
	v_mul_f32_e32 v101, 0xbfb8aa3b, v96
	v_exp_f32_e32 v101, v101
	v_mul_f32_e32 v90, v94, v90
	v_add_f32_e32 v101, 1.0, v101
	v_rcp_f32_e32 v94, v103
	s_nop 0
	v_mul_f32_e32 v94, v95, v94
	v_mul_f32_e32 v100, 0xbfb8aa3b, v97
	v_mul_f32_e32 v91, v94, v91
	v_exp_f32_e32 v100, v100
	s_nop 0
	v_add_f32_e32 v100, 1.0, v100
	v_rcp_f32_e32 v94, v101
	s_nop 0
	v_mul_f32_e32 v94, v96, v94
	v_mul_f32_e32 v96, 0xbfb8aa3b, v86
	v_exp_f32_e32 v96, v96
	v_mul_f32_e32 v92, v94, v92
	v_add_f32_e32 v96, 1.0, v96
	v_rcp_f32_e32 v94, v100
	s_nop 0
	v_mul_f32_e32 v94, v97, v94
	v_mul_f32_e32 v97, 0xbfb8aa3b, v87
	v_exp_f32_e32 v97, v97
	v_mul_f32_e32 v93, v94, v93
	v_add_f32_e32 v97, 1.0, v97
	v_rcp_f32_e32 v94, v96
	v_mul_f32_e32 v95, 0xbfb8aa3b, v88
	v_mul_f32_e32 v86, v86, v94
	v_exp_f32_e32 v95, v95
	v_mul_f32_e32 v94, v86, v82
	v_add_f32_e32 v95, 1.0, v95
	v_rcp_f32_e32 v82, v97
	v_mul_f32_e32 v86, 0xbfb8aa3b, v89
	v_mul_f32_e32 v82, v87, v82
	v_exp_f32_e32 v86, v86
	v_mul_f32_e32 v97, v82, v83
	v_add_f32_e32 v86, 1.0, v86
	v_rcp_f32_e32 v82, v95
	s_nop 0
	v_mul_f32_e32 v82, v88, v82
	v_mul_f32_e32 v88, v82, v84
	v_rcp_f32_e32 v82, v86
	s_nop 0
	v_mul_f32_e32 v82, v89, v82
	v_mul_f32_e32 v89, 0xbfb8aa3b, v78
	v_exp_f32_e32 v89, v89
	v_ashrrev_i32_e32 v99, 31, v98
	v_lshlrev_b64 v[98:99], 11, v[98:99]
	v_lshl_add_u64 v[98:99], s[16:17], 0, v[98:99]
; __device__ __forceinline__ unsigned cvt_pk_bf16(float lo, float hi) { unsigned r; asm volatile("v_cvt_pk_bf16_f32 %0, %1, %2" : "=v"(r) : "v"(lo), "v"(hi)); return r; }
; __device__ __forceinline__ float silu_f(float x) { return x / (1.0f + __expf(-x)); }
;     __device__ __forceinline__ void operator()(const f32x4 (&acc)[2][2][4][2], const Unit& u, int wr, int wc, int fr, int fq) const {
;         const int row0 = u.pm * BM + wr * 64 + fr, col0 = u.pn * HALF + wc * 32 + 8 * fq;
; #pragma unroll
;         for (int ai = 0; ai < 2; ++ai)
; #pragma unroll
;             for (int m = 0; m < 4; ++m) { bf16_t* rowp = ACT + (size_t)(row0 + ai * HALF + m * 16) * DE + col0;
;                 float v[8];
; #pragma unroll
;                 for (int n = 0; n < 2; ++n)
; #pragma unroll
;                     for (int j = 0; j < 4; ++j) v[n * 4 + j] = silu_f(acc[ai][0][m][n][j]) * acc[ai][1][m][n][j];
;                 v4u w; w.x = cvt_pk_bf16(v[0], v[1]); w.y = cvt_pk_bf16(v[2], v[3]); w.z = cvt_pk_bf16(v[4], v[5]); w.w = cvt_pk_bf16(v[6], v[7]);
;                 asm volatile("global_store_dwordx4 %0, %1, off sc1\n\ts_nop 1" :: "v"(rowp), "v"(w) : "memory"); }
	v_mul_f32_e32 v85, v82, v85
	v_cvt_pk_bf16_f32 v82, v90, v91
	v_cvt_pk_bf16_f32 v83, v92, v93
	v_cvt_pk_bf16_f32 v84, v94, v97
	v_lshl_add_u64 v[86:87], v[98:99], 0, v[116:117]
	v_cvt_pk_bf16_f32 v85, v88, v85
	s_nop 0
	global_store_dwordx4 v[86:87], v[82:85], off sc1
	s_nop 1
	v_add_f32_e32 v84, 1.0, v89
	v_mul_f32_e32 v89, 0xbfb8aa3b, v79
	v_exp_f32_e32 v89, v89
	v_or_b32_e32 v82, 48, v142
	v_add_f32_e32 v87, 1.0, v89
	v_rcp_f32_e32 v85, v84
	s_nop 0
	v_mul_f32_e32 v78, v78, v85
	v_mul_f32_e32 v85, 0xbfb8aa3b, v80
	v_exp_f32_e32 v85, v85
	v_mul_f32_e32 v74, v78, v74
	v_add_f32_e32 v85, 1.0, v85
	v_rcp_f32_e32 v78, v87
	s_nop 0
	v_mul_f32_e32 v78, v79, v78
	v_mul_f32_e32 v84, 0xbfb8aa3b, v81
	v_mul_f32_e32 v75, v78, v75
	v_exp_f32_e32 v84, v84
	s_nop 0
	v_add_f32_e32 v84, 1.0, v84
	v_rcp_f32_e32 v78, v85
	s_nop 0
	v_mul_f32_e32 v78, v80, v78
	v_mul_f32_e32 v80, 0xbfb8aa3b, v70
	v_exp_f32_e32 v80, v80
	v_mul_f32_e32 v76, v78, v76
	v_add_f32_e32 v80, 1.0, v80
	v_rcp_f32_e32 v78, v84
	s_nop 0
	v_mul_f32_e32 v78, v81, v78
	v_mul_f32_e32 v81, 0xbfb8aa3b, v71
	v_exp_f32_e32 v81, v81
	v_mul_f32_e32 v77, v78, v77
	v_add_f32_e32 v81, 1.0, v81
	v_rcp_f32_e32 v78, v80
	v_mul_f32_e32 v79, 0xbfb8aa3b, v72
	v_mul_f32_e32 v70, v70, v78
	v_exp_f32_e32 v79, v79
	v_mul_f32_e32 v78, v70, v66
	v_add_f32_e32 v79, 1.0, v79
	v_rcp_f32_e32 v66, v81
	v_mul_f32_e32 v70, 0xbfb8aa3b, v73
	v_mul_f32_e32 v66, v71, v66
	v_exp_f32_e32 v70, v70
	v_mul_f32_e32 v81, v66, v67
	v_add_f32_e32 v70, 1.0, v70
	v_rcp_f32_e32 v66, v79
	s_nop 0
	v_mul_f32_e32 v66, v72, v66
	v_mul_f32_e32 v72, v66, v68
	v_rcp_f32_e32 v66, v70
	s_nop 0
	v_mul_f32_e32 v66, v73, v66
	v_mul_f32_e32 v69, v66, v69
	v_mul_f32_e32 v66, 0xbfb8aa3b, v62
	v_exp_f32_e32 v68, v66
	v_ashrrev_i32_e32 v83, 31, v82
	v_cvt_pk_bf16_f32 v66, v74, v75
	v_lshlrev_b64 v[82:83], 11, v[82:83]
	v_add_f32_e32 v73, 1.0, v68
	v_lshl_add_u64 v[82:83], s[16:17], 0, v[82:83]
	v_cvt_pk_bf16_f32 v67, v76, v77
	v_cvt_pk_bf16_f32 v68, v78, v81
	v_lshl_add_u64 v[70:71], v[82:83], 0, v[116:117]
	v_cvt_pk_bf16_f32 v69, v72, v69
	s_nop 0
	global_store_dwordx4 v[70:71], v[66:69], off sc1
	s_nop 1
	v_mul_f32_e32 v68, 0xbfb8aa3b, v63
	v_exp_f32_e32 v68, v68
	s_nop 0
	v_add_f32_e32 v68, 1.0, v68
	v_rcp_f32_e32 v66, v73
	s_nop 0
	v_mul_f32_e32 v62, v62, v66
	v_mul_f32_e32 v67, 0xbfb8aa3b, v64
	v_mul_f32_e32 v58, v62, v58
	v_exp_f32_e32 v67, v67
	s_nop 0
	v_add_f32_e32 v67, 1.0, v67
	v_rcp_f32_e32 v62, v68
	v_mul_f32_e32 v66, 0xbfb8aa3b, v65
	v_mul_f32_e32 v62, v63, v62
	v_exp_f32_e32 v66, v66
	v_mul_f32_e32 v59, v62, v59
	v_add_f32_e32 v66, 1.0, v66
	v_rcp_f32_e32 v62, v67
	s_nop 0
	v_mul_f32_e32 v62, v64, v62
	v_mul_f32_e32 v64, 0xbfb8aa3b, v54
	v_exp_f32_e32 v64, v64
	v_mul_f32_e32 v60, v62, v60
	v_add_f32_e32 v64, 1.0, v64
	v_rcp_f32_e32 v62, v66
	s_nop 0
	v_mul_f32_e32 v62, v65, v62
	v_mul_f32_e32 v65, 0xbfb8aa3b, v55
	v_exp_f32_e32 v65, v65
	v_mul_f32_e32 v61, v62, v61
	v_add_f32_e32 v65, 1.0, v65
	v_rcp_f32_e32 v62, v64
	v_mul_f32_e32 v63, 0xbfb8aa3b, v56
	v_mul_f32_e32 v54, v54, v62
	v_exp_f32_e32 v63, v63
	v_mul_f32_e32 v62, v54, v50
	v_add_f32_e32 v63, 1.0, v63
	v_rcp_f32_e32 v50, v65
	v_mul_f32_e32 v54, 0xbfb8aa3b, v57
	v_mul_f32_e32 v50, v55, v50
	v_exp_f32_e32 v54, v54
	v_mul_f32_e32 v65, v50, v51
	v_add_f32_e32 v54, 1.0, v54
	v_rcp_f32_e32 v50, v63
	s_nop 0
	v_mul_f32_e32 v50, v56, v50
	v_mul_f32_e32 v56, v50, v52
	v_rcp_f32_e32 v50, v54
	s_nop 0
	v_mul_f32_e32 v50, v57, v50
	v_mul_f32_e32 v53, v50, v53
	v_mul_f32_e32 v50, 0xbfb8aa3b, v46
	v_exp_f32_e32 v52, v50
	v_cvt_pk_bf16_f32 v50, v58, v59
	v_cvt_pk_bf16_f32 v51, v60, v61
	v_lshl_add_u64 v[54:55], v[114:115], 0, s[24:25]
	v_add_f32_e32 v57, 1.0, v52
	v_cvt_pk_bf16_f32 v52, v62, v65
	v_cvt_pk_bf16_f32 v53, v56, v53
	s_nop 0
	global_store_dwordx4 v[54:55], v[50:53], off sc1
	s_nop 1
	v_mul_f32_e32 v52, 0xbfb8aa3b, v47
	v_exp_f32_e32 v52, v52
	s_nop 0
	v_add_f32_e32 v52, 1.0, v52
	v_rcp_f32_e32 v50, v57
	s_nop 0
	v_mul_f32_e32 v46, v46, v50
	v_mul_f32_e32 v51, 0xbfb8aa3b, v48
	v_mul_f32_e32 v42, v46, v42
	v_exp_f32_e32 v51, v51
	s_nop 0
	v_add_f32_e32 v51, 1.0, v51
	v_rcp_f32_e32 v46, v52
	v_mul_f32_e32 v50, 0xbfb8aa3b, v49
	v_mul_f32_e32 v46, v47, v46
	v_exp_f32_e32 v50, v50
	v_mul_f32_e32 v43, v46, v43
	v_add_f32_e32 v50, 1.0, v50
	v_rcp_f32_e32 v46, v51
	s_nop 0
	v_mul_f32_e32 v46, v48, v46
	v_mul_f32_e32 v48, 0xbfb8aa3b, v38
	v_exp_f32_e32 v48, v48
	v_mul_f32_e32 v44, v46, v44
; __device__ __forceinline__ unsigned cvt_pk_bf16(float lo, float hi) { unsigned r; asm volatile("v_cvt_pk_bf16_f32 %0, %1, %2" : "=v"(r) : "v"(lo), "v"(hi)); return r; }
; __device__ __forceinline__ float silu_f(float x) { return x / (1.0f + __expf(-x)); }
;     __device__ __forceinline__ void operator()(const f32x4 (&acc)[2][2][4][2], const Unit& u, int wr, int wc, int fr, int fq) const {
;         const int row0 = u.pm * BM + wr * 64 + fr, col0 = u.pn * HALF + wc * 32 + 8 * fq;
; #pragma unroll
;         for (int ai = 0; ai < 2; ++ai)
; #pragma unroll
;             for (int m = 0; m < 4; ++m) { bf16_t* rowp = ACT + (size_t)(row0 + ai * HALF + m * 16) * DE + col0;
;                 float v[8];
; #pragma unroll
;                 for (int n = 0; n < 2; ++n)
; #pragma unroll
;                     for (int j = 0; j < 4; ++j) v[n * 4 + j] = silu_f(acc[ai][0][m][n][j]) * acc[ai][1][m][n][j];
;                 v4u w; w.x = cvt_pk_bf16(v[0], v[1]); w.y = cvt_pk_bf16(v[2], v[3]); w.z = cvt_pk_bf16(v[4], v[5]); w.w = cvt_pk_bf16(v[6], v[7]);
;                 asm volatile("global_store_dwordx4 %0, %1, off sc1\n\ts_nop 1" :: "v"(rowp), "v"(w) : "memory"); }
	v_add_f32_e32 v48, 1.0, v48
	v_rcp_f32_e32 v46, v50
	s_nop 0
	v_mul_f32_e32 v46, v49, v46
	v_mul_f32_e32 v49, 0xbfb8aa3b, v39
	v_exp_f32_e32 v49, v49
	v_mul_f32_e32 v45, v46, v45
	v_add_f32_e32 v49, 1.0, v49
	v_rcp_f32_e32 v46, v48
	v_mul_f32_e32 v47, 0xbfb8aa3b, v40
	v_mul_f32_e32 v38, v38, v46
	v_exp_f32_e32 v47, v47
	v_mul_f32_e32 v46, v38, v34
	v_add_f32_e32 v47, 1.0, v47
	v_rcp_f32_e32 v34, v49
	v_mul_f32_e32 v38, 0xbfb8aa3b, v41
	v_mul_f32_e32 v34, v39, v34
	v_exp_f32_e32 v38, v38
	v_mul_f32_e32 v49, v34, v35
	v_add_f32_e32 v38, 1.0, v38
	v_rcp_f32_e32 v34, v47
	s_nop 0
	v_mul_f32_e32 v34, v40, v34
	v_mul_f32_e32 v40, v34, v36
	v_rcp_f32_e32 v34, v38
	s_nop 0
	v_mul_f32_e32 v34, v41, v34
	v_mul_f32_e32 v37, v34, v37
	v_mul_f32_e32 v34, 0xbfb8aa3b, v30
	v_exp_f32_e32 v36, v34
	v_cvt_pk_bf16_f32 v34, v42, v43
	v_cvt_pk_bf16_f32 v35, v44, v45
	v_lshl_add_u64 v[38:39], v[114:115], 0, s[26:27]
	v_add_f32_e32 v41, 1.0, v36
	v_cvt_pk_bf16_f32 v36, v46, v49
	v_cvt_pk_bf16_f32 v37, v40, v37
	s_nop 0
	global_store_dwordx4 v[38:39], v[34:37], off sc1
	s_nop 1
	v_mul_f32_e32 v36, 0xbfb8aa3b, v31
	v_exp_f32_e32 v36, v36
	s_nop 0
	v_add_f32_e32 v36, 1.0, v36
	v_rcp_f32_e32 v34, v41
	s_nop 0
	v_mul_f32_e32 v30, v30, v34
	v_mul_f32_e32 v35, 0xbfb8aa3b, v32
	v_mul_f32_e32 v26, v30, v26
	v_exp_f32_e32 v35, v35
	s_nop 0
	v_add_f32_e32 v35, 1.0, v35
	v_rcp_f32_e32 v30, v36
	v_mul_f32_e32 v34, 0xbfb8aa3b, v33
	v_mul_f32_e32 v30, v31, v30
	v_exp_f32_e32 v34, v34
	v_mul_f32_e32 v27, v30, v27
	v_add_f32_e32 v34, 1.0, v34
	v_rcp_f32_e32 v30, v35
	s_nop 0
	v_mul_f32_e32 v30, v32, v30
	v_mul_f32_e32 v32, 0xbfb8aa3b, v22
	v_exp_f32_e32 v32, v32
	v_mul_f32_e32 v28, v30, v28
	v_add_f32_e32 v32, 1.0, v32
	v_rcp_f32_e32 v30, v34
	s_nop 0
	v_mul_f32_e32 v30, v33, v30
	v_mul_f32_e32 v33, 0xbfb8aa3b, v23
	v_exp_f32_e32 v33, v33
	v_mul_f32_e32 v29, v30, v29
	v_add_f32_e32 v33, 1.0, v33
	v_rcp_f32_e32 v30, v32
	v_mul_f32_e32 v31, 0xbfb8aa3b, v24
	v_mul_f32_e32 v22, v22, v30
	v_exp_f32_e32 v31, v31
	v_mul_f32_e32 v30, v22, v18
	v_add_f32_e32 v31, 1.0, v31
	v_rcp_f32_e32 v18, v33
	v_mul_f32_e32 v22, 0xbfb8aa3b, v25
	v_mul_f32_e32 v18, v23, v18
	v_exp_f32_e32 v22, v22
	v_mul_f32_e32 v33, v18, v19
	v_add_f32_e32 v22, 1.0, v22
	v_rcp_f32_e32 v18, v31
	s_nop 0
	v_mul_f32_e32 v18, v24, v18
	v_mul_f32_e32 v24, v18, v20
	v_rcp_f32_e32 v18, v22
	s_nop 0
	v_mul_f32_e32 v18, v25, v18
	v_mul_f32_e32 v21, v18, v21
	v_mul_f32_e32 v18, 0xbfb8aa3b, v14
	v_exp_f32_e32 v20, v18
	v_cvt_pk_bf16_f32 v18, v26, v27
	v_cvt_pk_bf16_f32 v19, v28, v29
	v_lshl_add_u64 v[22:23], v[114:115], 0, s[28:29]
	v_add_f32_e32 v25, 1.0, v20
	v_cvt_pk_bf16_f32 v20, v30, v33
	v_cvt_pk_bf16_f32 v21, v24, v21
	s_nop 0
	global_store_dwordx4 v[22:23], v[18:21], off sc1
	s_nop 1
	v_mul_f32_e32 v20, 0xbfb8aa3b, v15
	v_exp_f32_e32 v20, v20
	s_nop 0
	v_add_f32_e32 v20, 1.0, v20
	v_rcp_f32_e32 v18, v25
	s_nop 0
	v_mul_f32_e32 v14, v14, v18
	v_mul_f32_e32 v19, 0xbfb8aa3b, v16
	v_mul_f32_e32 v10, v14, v10
	v_exp_f32_e32 v19, v19
	s_nop 0
	v_add_f32_e32 v19, 1.0, v19
	v_rcp_f32_e32 v14, v20
	v_mul_f32_e32 v18, 0xbfb8aa3b, v17
	v_mul_f32_e32 v14, v15, v14
	v_exp_f32_e32 v18, v18
	v_mul_f32_e32 v11, v14, v11
	v_add_f32_e32 v18, 1.0, v18
	v_rcp_f32_e32 v14, v19
	s_nop 0
	v_mul_f32_e32 v14, v16, v14
	v_mul_f32_e32 v16, 0xbfb8aa3b, v6
	v_exp_f32_e32 v16, v16
	v_mul_f32_e32 v12, v14, v12
	v_add_f32_e32 v16, 1.0, v16
	v_rcp_f32_e32 v14, v18
	s_nop 0
	v_mul_f32_e32 v14, v17, v14
	v_mul_f32_e32 v17, 0xbfb8aa3b, v7
	v_exp_f32_e32 v17, v17
	v_mul_f32_e32 v13, v14, v13
	v_add_f32_e32 v17, 1.0, v17
	v_rcp_f32_e32 v14, v16
	v_mul_f32_e32 v15, 0xbfb8aa3b, v8
	v_mul_f32_e32 v6, v6, v14
	v_exp_f32_e32 v15, v15
	v_mul_f32_e32 v14, v6, v2
	v_add_f32_e32 v15, 1.0, v15
	v_rcp_f32_e32 v2, v17
	v_mul_f32_e32 v6, 0xbfb8aa3b, v9
	v_mul_f32_e32 v2, v7, v2
	v_exp_f32_e32 v6, v6
	v_mul_f32_e32 v17, v2, v3
	v_add_f32_e32 v6, 1.0, v6
	v_rcp_f32_e32 v2, v15
	s_nop 0
	v_mul_f32_e32 v2, v8, v2
	v_mul_f32_e32 v8, v2, v4
	v_rcp_f32_e32 v2, v6
	s_nop 0
	v_mul_f32_e32 v2, v9, v2
	v_mul_f32_e32 v5, v2, v5
	v_lshl_add_u64 v[6:7], v[114:115], 0, s[30:31]
	v_cvt_pk_bf16_f32 v2, v10, v11
	v_cvt_pk_bf16_f32 v3, v12, v13
	v_cvt_pk_bf16_f32 v4, v14, v17
	v_cvt_pk_bf16_f32 v5, v8, v5
	s_and_b64 vcc, exec, s[4:5]
	global_store_dwordx4 v[6:7], v[2:5], off sc1
	s_nop 1
	s_mov_b64 s[4:5], -1
	s_cbranch_vccnz .LBB0_899
	s_andn2_b64 vcc, exec, s[14:15]
	s_cbranch_vccnz .LBB0_898
	s_barrier

; __global__ void __launch_bounds__(512, 2) mk_fwd(Params p_unused) {
;     extern __shared__ __attribute__((aligned(16))) unsigned char lds[];
	.amdhsa_kernel _Z6mk_fwd6Params
		.amdhsa_group_segment_fixed_size 0
		.amdhsa_private_segment_fixed_size 0
		.amdhsa_kernarg_size 432
		.amdhsa_user_sgpr_count 2
		.amdhsa_user_sgpr_dispatch_ptr 0
		.amdhsa_user_sgpr_queue_ptr 0
		.amdhsa_user_sgpr_kernarg_segment_ptr 1
		.amdhsa_user_sgpr_dispatch_id 0
		.amdhsa_user_sgpr_kernarg_preload_length 0
		.amdhsa_user_sgpr_kernarg_preload_offset 0
		.amdhsa_user_sgpr_private_segment_size 0
		.amdhsa_uses_dynamic_stack 0
		.amdhsa_enable_private_segment 0
		.amdhsa_system_sgpr_workgroup_id_x 1
		.amdhsa_system_sgpr_workgroup_id_y 0
		.amdhsa_system_sgpr_workgroup_id_z 0
		.amdhsa_system_sgpr_workgroup_info 0
		.amdhsa_system_vgpr_workitem_id 0
		.amdhsa_next_free_vgpr 256
		.amdhsa_next_free_sgpr 102
		.amdhsa_accum_offset 256
		.amdhsa_reserve_vcc 1
		.amdhsa_float_round_mode_32 0
		.amdhsa_float_round_mode_16_64 0
		.amdhsa_float_denorm_mode_32 3
		.amdhsa_float_denorm_mode_16_64 3
		.amdhsa_dx10_clamp 1
		.amdhsa_ieee_mode 1
		.amdhsa_fp16_overflow 0
		.amdhsa_tg_split 0
		.amdhsa_exception_fp_ieee_invalid_op 0
		.amdhsa_exception_fp_denorm_src 0
		.amdhsa_exception_fp_ieee_div_zero 0
		.amdhsa_exception_fp_ieee_overflow 0
		.amdhsa_exception_fp_ieee_underflow 0
		.amdhsa_exception_fp_ieee_inexact 0
		.amdhsa_exception_int_div_zero 0
	.end_amdhsa_kernel

; __global__ void __launch_bounds__(512, 2) mk_fwd(Params p_unused) {
;     extern __shared__ __attribute__((aligned(16))) unsigned char lds[];
amdhsa.kernels:
  - .agpr_count:     0
    .args:
      - .offset:         0
        .size:           176
        .value_kind:     by_value
      - .offset:         176
        .size:           4
        .value_kind:     hidden_block_count_x
      - .offset:         180
        .size:           4
        .value_kind:     hidden_block_count_y
      - .offset:         184
        .size:           4
        .value_kind:     hidden_block_count_z
      - .offset:         188
        .size:           2
        .value_kind:     hidden_group_size_x
      - .offset:         190
        .size:           2
        .value_kind:     hidden_group_size_y
      - .offset:         192
        .size:           2
        .value_kind:     hidden_group_size_z
      - .offset:         194
        .size:           2
        .value_kind:     hidden_remainder_x
      - .offset:         196
        .size:           2
        .value_kind:     hidden_remainder_y
      - .offset:         198
        .size:           2
        .value_kind:     hidden_remainder_z
      - .offset:         216
        .size:           8
        .value_kind:     hidden_global_offset_x
      - .offset:         224
        .size:           8
        .value_kind:     hidden_global_offset_y
      - .offset:         232
        .size:           8
        .value_kind:     hidden_global_offset_z
      - .offset:         240
        .size:           2
        .value_kind:     hidden_grid_dims
      - .offset:         296
        .size:           4
        .value_kind:     hidden_dynamic_lds_size
    .group_segment_fixed_size: 0
    .kernarg_segment_align: 8
    .kernarg_segment_size: 432
    .language:       OpenCL C
    .language_version:
      - 2
      - 0
    .max_flat_workgroup_size: 512
    .name:           _Z6mk_fwd6Params
    .private_segment_fixed_size: 0
    .sgpr_count:     108
    .sgpr_spill_count: 9
    .symbol:         _Z6mk_fwd6Params.kd
    .uniform_work_group_size: 1
    .uses_dynamic_stack: false
    .vgpr_count:     256
    .vgpr_spill_count: 0
    .wavefront_size: 64
